# v13 plus: end-of-compute s_barrier moved before the last MFMA (fp8) / last two MFMAs (bf16) of every K-loop compute segment, leftover MFMAs issued at s_setprio 3
# baseline (speedup 1.0000x reference)
.LBB0_286:
	s_lshl_b32 s10, s51, 19
	s_add_u32 s10, s20, s10
	s_addc_u32 s11, s21, 0
	s_and_b64 s[16:17], s[4:5], exec
	s_cselect_b32 s54, s11, s31
	s_cselect_b32 s55, s10, s30
	s_lshl_b32 s14, s50, 19
	s_add_u32 s16, s15, s14
	s_addc_u32 s17, s26, 0
	s_and_b64 s[36:37], s[4:5], exec
	s_cselect_b32 s56, s17, s23
	s_cselect_b32 s57, s16, s22
	s_add_i32 s60, 0, 0x10000
	v_add_u32_e32 v198, s60, v196
	s_add_i32 s62, 0, 0x14000
	v_add_u32_e32 v199, s62, v196
	ds_read_b128 v[160:163], v198
	ds_read_b128 v[152:155], v198 offset:1024
	ds_read_b128 v[156:159], v198 offset:2048
	ds_read_b128 v[148:151], v198 offset:3072
	ds_read_b128 v[144:147], v199
	ds_read_b128 v[136:139], v199 offset:1024
	ds_read_b128 v[140:143], v199 offset:2048
	ds_read_b128 v[132:135], v199 offset:3072
	s_add_u32 s36, s30, 0x40080
	s_addc_u32 s37, s31, 0
	s_add_i32 s58, s41, 0xc000
	v_lshl_add_u64 v[174:175], s[36:37], 0, v[168:169]
	s_mov_b32 m0, s58
	s_add_i32 s59, s41, 0xe000
	ds_read_b128 v[178:181], v197
	ds_read_b128 v[182:185], v197 offset:1024
	ds_read_b128 v[190:193], v197 offset:2048
	ds_read_b128 v[200:203], v197 offset:3072
	ds_read_b128 v[204:207], v197 offset:4096
	ds_read_b128 v[208:211], v197 offset:5120
	ds_read_b128 v[212:215], v197 offset:6144
	ds_read_b128 v[216:219], v197 offset:7168
	global_load_lds_dwordx4 v[174:175], off
	v_lshl_add_u64 v[174:175], s[36:37], 0, v[166:167]
	s_mov_b32 m0, s59
	s_nop 0
	global_load_lds_dwordx4 v[174:175], off
	s_waitcnt vmcnt(8)
	s_waitcnt lgkmcnt(0)
	s_barrier
	s_setprio 1
	s_waitcnt lgkmcnt(0)
	v_mfma_f32_16x16x32_bf16 v[128:131], v[160:163], v[178:181], 0
	v_mfma_f32_16x16x32_bf16 v[124:127], v[156:159], v[178:181], 0
	v_mfma_f32_16x16x32_bf16 v[116:119], v[156:159], v[190:193], 0
	v_mfma_f32_16x16x32_bf16 v[120:123], v[160:163], v[190:193], 0
	v_mfma_f32_16x16x32_bf16 v[112:115], v[160:163], v[204:207], 0
	v_mfma_f32_16x16x32_bf16 v[108:111], v[156:159], v[204:207], 0
	v_mfma_f32_16x16x32_bf16 v[100:103], v[156:159], v[212:215], 0
	v_mfma_f32_16x16x32_bf16 v[104:107], v[160:163], v[212:215], 0
	s_nop 0
	v_mfma_f32_16x16x32_bf16 v[128:131], v[152:155], v[182:185], v[128:131]
	v_mfma_f32_16x16x32_bf16 v[124:127], v[148:151], v[182:185], v[124:127]
	v_mfma_f32_16x16x32_bf16 v[116:119], v[148:151], v[200:203], v[116:119]
	v_mfma_f32_16x16x32_bf16 v[120:123], v[152:155], v[200:203], v[120:123]
	v_mfma_f32_16x16x32_bf16 v[112:115], v[152:155], v[208:211], v[112:115]
	v_mfma_f32_16x16x32_bf16 v[108:111], v[148:151], v[208:211], v[108:111]
	v_mfma_f32_16x16x32_bf16 v[100:103], v[148:151], v[216:219], v[100:103]
	v_mfma_f32_16x16x32_bf16 v[104:107], v[152:155], v[216:219], v[104:107]
	s_setprio 0
	s_setprio 1
	v_mfma_f32_16x16x32_bf16 v[96:99], v[144:147], v[178:181], 0
	v_mfma_f32_16x16x32_bf16 v[92:95], v[140:143], v[178:181], 0
	v_mfma_f32_16x16x32_bf16 v[84:87], v[140:143], v[190:193], 0
	v_mfma_f32_16x16x32_bf16 v[88:91], v[144:147], v[190:193], 0
	v_mfma_f32_16x16x32_bf16 v[80:83], v[144:147], v[204:207], 0
	v_mfma_f32_16x16x32_bf16 v[76:79], v[140:143], v[204:207], 0
	v_mfma_f32_16x16x32_bf16 v[68:71], v[140:143], v[212:215], 0
	v_mfma_f32_16x16x32_bf16 v[72:75], v[144:147], v[212:215], 0
	s_nop 0
	v_mfma_f32_16x16x32_bf16 v[96:99], v[136:139], v[182:185], v[96:99]
	v_mfma_f32_16x16x32_bf16 v[92:95], v[132:135], v[182:185], v[92:95]
	v_mfma_f32_16x16x32_bf16 v[84:87], v[132:135], v[200:203], v[84:87]
	v_mfma_f32_16x16x32_bf16 v[88:91], v[136:139], v[200:203], v[88:91]
	v_mfma_f32_16x16x32_bf16 v[80:83], v[136:139], v[208:211], v[80:83]
	v_mfma_f32_16x16x32_bf16 v[76:79], v[132:135], v[208:211], v[76:79]
	s_barrier
	s_setprio 3
	v_mfma_f32_16x16x32_bf16 v[68:71], v[132:135], v[216:219], v[68:71]
	v_mfma_f32_16x16x32_bf16 v[72:75], v[136:139], v[216:219], v[72:75]
	s_setprio 0
	v_lshl_add_u64 v[174:175], s[22:23], 0, v[34:35]
	s_add_i32 s60, s60, s40
	v_lshl_add_u64 v[190:191], v[174:175], 0, s[28:29]
	s_mov_b32 m0, s60
	s_add_i32 s61, s60, 0x2000
	ds_read_b128 v[178:181], v197 offset:16384
	ds_read_b128 v[182:185], v197 offset:17408
	ds_read_b128 v[200:203], v197 offset:18432
	ds_read_b128 v[204:207], v197 offset:19456
	ds_read_b128 v[208:211], v197 offset:20480
	ds_read_b128 v[212:215], v197 offset:21504
	ds_read_b128 v[216:219], v197 offset:22528
	ds_read_b128 v[222:225], v197 offset:23552
	global_load_lds_dwordx4 v[190:191], off
	v_lshl_add_u64 v[190:191], s[22:23], 0, v[164:165]
	s_add_u32 s36, s22, 0x40100
	v_lshl_add_u64 v[192:193], v[190:191], 0, s[28:29]
	s_mov_b32 m0, s61
	s_addc_u32 s37, s23, 0
	s_add_i32 s62, s62, s40
	global_load_lds_dwordx4 v[192:193], off
	v_lshl_add_u64 v[192:193], s[36:37], 0, v[34:35]
	s_mov_b32 m0, s62
	s_add_i32 s63, s62, 0x2000
	global_load_lds_dwordx4 v[192:193], off
	v_lshl_add_u64 v[192:193], s[36:37], 0, v[164:165]
	s_mov_b32 m0, s63
	s_nop 0
	global_load_lds_dwordx4 v[192:193], off
	v_lshl_add_u64 v[192:193], s[30:31], 0, v[168:169]
	v_lshl_add_u64 v[194:195], v[192:193], 0, s[28:29]
	s_mov_b32 m0, s41
	s_nop 0
	global_load_lds_dwordx4 v[194:195], off
	v_lshl_add_u64 v[194:195], s[30:31], 0, v[166:167]
	v_lshl_add_u64 v[226:227], v[194:195], 0, s[28:29]
	s_mov_b32 m0, s42
	s_nop 0
	global_load_lds_dwordx4 v[226:227], off
	s_waitcnt vmcnt(8)
	s_waitcnt lgkmcnt(0)
	s_barrier
	s_setprio 1
	s_waitcnt lgkmcnt(0)
	v_mfma_f32_16x16x32_bf16 v[64:67], v[160:163], v[178:181], 0
	v_mfma_f32_16x16x32_bf16 v[60:63], v[156:159], v[178:181], 0
	v_mfma_f32_16x16x32_bf16 v[52:55], v[156:159], v[200:203], 0
	v_mfma_f32_16x16x32_bf16 v[56:59], v[160:163], v[200:203], 0
	v_mfma_f32_16x16x32_bf16 v[48:51], v[160:163], v[208:211], 0
	v_mfma_f32_16x16x32_bf16 v[44:47], v[156:159], v[208:211], 0
	v_mfma_f32_16x16x32_bf16 v[36:39], v[156:159], v[216:219], 0
	v_mfma_f32_16x16x32_bf16 v[40:43], v[160:163], v[216:219], 0
	s_nop 0
	v_mfma_f32_16x16x32_bf16 v[64:67], v[152:155], v[182:185], v[64:67]
	v_mfma_f32_16x16x32_bf16 v[60:63], v[148:151], v[182:185], v[60:63]
	v_mfma_f32_16x16x32_bf16 v[52:55], v[148:151], v[204:207], v[52:55]
	v_mfma_f32_16x16x32_bf16 v[56:59], v[152:155], v[204:207], v[56:59]
	v_mfma_f32_16x16x32_bf16 v[48:51], v[152:155], v[212:215], v[48:51]
	v_mfma_f32_16x16x32_bf16 v[44:47], v[148:151], v[212:215], v[44:47]
	v_mfma_f32_16x16x32_bf16 v[36:39], v[148:151], v[222:225], v[36:39]
	v_mfma_f32_16x16x32_bf16 v[40:43], v[152:155], v[222:225], v[40:43]
	s_setprio 0
	s_setprio 1
	v_mfma_f32_16x16x32_bf16 v[30:33], v[144:147], v[178:181], 0
	v_mfma_f32_16x16x32_bf16 v[26:29], v[140:143], v[178:181], 0
	v_mfma_f32_16x16x32_bf16 v[18:21], v[140:143], v[200:203], 0
	v_mfma_f32_16x16x32_bf16 v[22:25], v[144:147], v[200:203], 0
	v_mfma_f32_16x16x32_bf16 v[14:17], v[144:147], v[208:211], 0
	v_mfma_f32_16x16x32_bf16 v[10:13], v[140:143], v[208:211], 0
	v_mfma_f32_16x16x32_bf16 v[2:5], v[140:143], v[216:219], 0
	v_mfma_f32_16x16x32_bf16 v[6:9], v[144:147], v[216:219], 0
	s_nop 0
	v_mfma_f32_16x16x32_bf16 v[30:33], v[136:139], v[182:185], v[30:33]
	v_mfma_f32_16x16x32_bf16 v[26:29], v[132:135], v[182:185], v[26:29]
	v_mfma_f32_16x16x32_bf16 v[18:21], v[132:135], v[204:207], v[18:21]
	v_mfma_f32_16x16x32_bf16 v[22:25], v[136:139], v[204:207], v[22:25]
	v_mfma_f32_16x16x32_bf16 v[14:17], v[136:139], v[212:215], v[14:17]
	v_mfma_f32_16x16x32_bf16 v[10:13], v[132:135], v[212:215], v[10:13]
	s_barrier
	s_setprio 3
	v_mfma_f32_16x16x32_bf16 v[2:5], v[132:135], v[222:225], v[2:5]
	v_mfma_f32_16x16x32_bf16 v[6:9], v[136:139], v[222:225], v[6:9]
	s_setprio 0
	s_add_i32 s64, 0, 0x18000
	s_add_i32 s66, 0, 0x1c000
	v_add_u32_e32 v132, s64, v196
	v_add_u32_e32 v133, s66, v196
	ds_read_b128 v[134:137], v132
	ds_read_b128 v[138:141], v132 offset:1024
	ds_read_b128 v[142:145], v132 offset:2048
	ds_read_b128 v[146:149], v132 offset:3072
	ds_read_b128 v[150:153], v133
	ds_read_b128 v[154:157], v133 offset:1024
	ds_read_b128 v[158:161], v133 offset:2048
	ds_read_b128 v[178:181], v133 offset:3072
	s_add_u32 s36, s30, 0x40100
	s_addc_u32 s37, s31, 0
	s_mov_b32 m0, s43
	v_lshl_add_u64 v[162:163], s[36:37], 0, v[168:169]
	ds_read_b128 v[182:185], v197 offset:32768
	ds_read_b128 v[200:203], v197 offset:33792
	ds_read_b128 v[204:207], v197 offset:34816
	ds_read_b128 v[208:211], v197 offset:35840
	ds_read_b128 v[212:215], v197 offset:36864
	ds_read_b128 v[216:219], v197 offset:37888
	ds_read_b128 v[222:225], v197 offset:38912
	ds_read_b128 v[226:229], v197 offset:39936
	global_load_lds_dwordx4 v[162:163], off
	v_lshl_add_u64 v[162:163], s[36:37], 0, v[166:167]
	s_mov_b32 m0, s44
	s_nop 0
	global_load_lds_dwordx4 v[162:163], off
	s_waitcnt vmcnt(8)
	s_waitcnt lgkmcnt(0)
	s_barrier
	s_setprio 1
	s_waitcnt lgkmcnt(0)
	v_mfma_f32_16x16x32_bf16 v[128:131], v[134:137], v[182:185], v[128:131]
	v_mfma_f32_16x16x32_bf16 v[124:127], v[142:145], v[182:185], v[124:127]
	v_mfma_f32_16x16x32_bf16 v[116:119], v[142:145], v[204:207], v[116:119]
	v_mfma_f32_16x16x32_bf16 v[120:123], v[134:137], v[204:207], v[120:123]
	v_mfma_f32_16x16x32_bf16 v[112:115], v[134:137], v[212:215], v[112:115]
	v_mfma_f32_16x16x32_bf16 v[108:111], v[142:145], v[212:215], v[108:111]
	v_mfma_f32_16x16x32_bf16 v[100:103], v[142:145], v[222:225], v[100:103]
	v_mfma_f32_16x16x32_bf16 v[104:107], v[134:137], v[222:225], v[104:107]
	v_mfma_f32_16x16x32_bf16 v[128:131], v[138:141], v[200:203], v[128:131]
	v_mfma_f32_16x16x32_bf16 v[124:127], v[146:149], v[200:203], v[124:127]
	v_mfma_f32_16x16x32_bf16 v[116:119], v[146:149], v[208:211], v[116:119]
	v_mfma_f32_16x16x32_bf16 v[120:123], v[138:141], v[208:211], v[120:123]
	v_mfma_f32_16x16x32_bf16 v[112:115], v[138:141], v[216:219], v[112:115]
	v_mfma_f32_16x16x32_bf16 v[108:111], v[146:149], v[216:219], v[108:111]
	v_mfma_f32_16x16x32_bf16 v[100:103], v[146:149], v[226:229], v[100:103]
	v_mfma_f32_16x16x32_bf16 v[104:107], v[138:141], v[226:229], v[104:107]
	s_setprio 0
	s_setprio 1
	v_mfma_f32_16x16x32_bf16 v[96:99], v[150:153], v[182:185], v[96:99]
	v_mfma_f32_16x16x32_bf16 v[92:95], v[158:161], v[182:185], v[92:95]
	v_mfma_f32_16x16x32_bf16 v[84:87], v[158:161], v[204:207], v[84:87]
	v_mfma_f32_16x16x32_bf16 v[88:91], v[150:153], v[204:207], v[88:91]
	v_mfma_f32_16x16x32_bf16 v[80:83], v[150:153], v[212:215], v[80:83]
	v_mfma_f32_16x16x32_bf16 v[76:79], v[158:161], v[212:215], v[76:79]
	v_mfma_f32_16x16x32_bf16 v[68:71], v[158:161], v[222:225], v[68:71]
	v_mfma_f32_16x16x32_bf16 v[72:75], v[150:153], v[222:225], v[72:75]
	v_mfma_f32_16x16x32_bf16 v[96:99], v[154:157], v[200:203], v[96:99]
	v_mfma_f32_16x16x32_bf16 v[92:95], v[178:181], v[200:203], v[92:95]
	v_mfma_f32_16x16x32_bf16 v[84:87], v[178:181], v[208:211], v[84:87]
	v_mfma_f32_16x16x32_bf16 v[88:91], v[154:157], v[208:211], v[88:91]
	v_mfma_f32_16x16x32_bf16 v[80:83], v[154:157], v[216:219], v[80:83]
	v_mfma_f32_16x16x32_bf16 v[76:79], v[178:181], v[216:219], v[76:79]
	s_barrier
	s_setprio 3
	v_mfma_f32_16x16x32_bf16 v[68:71], v[178:181], v[226:229], v[68:71]
	v_mfma_f32_16x16x32_bf16 v[72:75], v[154:157], v[226:229], v[72:75]
	s_setprio 0
	s_add_i32 s64, s64, s40
	s_mov_b64 s[24:25], 0x180
	s_add_i32 s65, s64, 0x2000
	v_lshl_add_u64 v[162:163], v[174:175], 0, s[24:25]
	s_mov_b32 m0, s64
	s_add_u32 s36, s22, 0x40180
	ds_read_b128 v[182:185], v197 offset:49152
	ds_read_b128 v[200:203], v197 offset:50176
	ds_read_b128 v[204:207], v197 offset:51200
	ds_read_b128 v[208:211], v197 offset:52224
	ds_read_b128 v[212:215], v197 offset:53248
	ds_read_b128 v[216:219], v197 offset:54272
	ds_read_b128 v[222:225], v197 offset:55296
	ds_read_b128 v[226:229], v197 offset:56320
	global_load_lds_dwordx4 v[162:163], off
	v_lshl_add_u64 v[162:163], v[190:191], 0, s[24:25]
	s_mov_b32 m0, s65
	s_addc_u32 s37, s23, 0
	s_add_i32 s66, s66, s40
	global_load_lds_dwordx4 v[162:163], off
	v_lshl_add_u64 v[162:163], s[36:37], 0, v[34:35]
	s_mov_b32 m0, s66
	s_add_i32 s67, s66, 0x2000
	global_load_lds_dwordx4 v[162:163], off
	v_lshl_add_u64 v[162:163], s[36:37], 0, v[164:165]
	s_mov_b32 m0, s67
	s_nop 0
	global_load_lds_dwordx4 v[162:163], off
	v_lshl_add_u64 v[162:163], v[192:193], 0, s[24:25]
	s_mov_b32 m0, s47
	s_nop 0
	global_load_lds_dwordx4 v[162:163], off
	v_lshl_add_u64 v[162:163], v[194:195], 0, s[24:25]
	s_mov_b32 m0, s48
	s_nop 0
	global_load_lds_dwordx4 v[162:163], off
	s_waitcnt vmcnt(8)
	s_waitcnt lgkmcnt(0)
	s_barrier
	s_setprio 1
	s_waitcnt lgkmcnt(0)
	v_mfma_f32_16x16x32_bf16 v[64:67], v[134:137], v[182:185], v[64:67]
	v_mfma_f32_16x16x32_bf16 v[60:63], v[142:145], v[182:185], v[60:63]
	v_mfma_f32_16x16x32_bf16 v[52:55], v[142:145], v[204:207], v[52:55]
	v_mfma_f32_16x16x32_bf16 v[56:59], v[134:137], v[204:207], v[56:59]
	v_mfma_f32_16x16x32_bf16 v[48:51], v[134:137], v[212:215], v[48:51]
	v_mfma_f32_16x16x32_bf16 v[44:47], v[142:145], v[212:215], v[44:47]
	v_mfma_f32_16x16x32_bf16 v[36:39], v[142:145], v[222:225], v[36:39]
	v_mfma_f32_16x16x32_bf16 v[40:43], v[134:137], v[222:225], v[40:43]
	v_mfma_f32_16x16x32_bf16 v[64:67], v[138:141], v[200:203], v[64:67]
	v_mfma_f32_16x16x32_bf16 v[60:63], v[146:149], v[200:203], v[60:63]
	v_mfma_f32_16x16x32_bf16 v[52:55], v[146:149], v[208:211], v[52:55]
	v_mfma_f32_16x16x32_bf16 v[56:59], v[138:141], v[208:211], v[56:59]
	v_mfma_f32_16x16x32_bf16 v[48:51], v[138:141], v[216:219], v[48:51]
	v_mfma_f32_16x16x32_bf16 v[44:47], v[146:149], v[216:219], v[44:47]
	v_mfma_f32_16x16x32_bf16 v[36:39], v[146:149], v[226:229], v[36:39]
	v_mfma_f32_16x16x32_bf16 v[40:43], v[138:141], v[226:229], v[40:43]
	s_setprio 0
	s_setprio 1
	v_mfma_f32_16x16x32_bf16 v[30:33], v[150:153], v[182:185], v[30:33]
	v_mfma_f32_16x16x32_bf16 v[26:29], v[158:161], v[182:185], v[26:29]
	v_mfma_f32_16x16x32_bf16 v[18:21], v[158:161], v[204:207], v[18:21]
	v_mfma_f32_16x16x32_bf16 v[22:25], v[150:153], v[204:207], v[22:25]
	v_mfma_f32_16x16x32_bf16 v[14:17], v[150:153], v[212:215], v[14:17]
	v_mfma_f32_16x16x32_bf16 v[10:13], v[158:161], v[212:215], v[10:13]
	v_mfma_f32_16x16x32_bf16 v[2:5], v[158:161], v[222:225], v[2:5]
	v_mfma_f32_16x16x32_bf16 v[6:9], v[150:153], v[222:225], v[6:9]
	v_mfma_f32_16x16x32_bf16 v[30:33], v[154:157], v[200:203], v[30:33]
	v_mfma_f32_16x16x32_bf16 v[26:29], v[178:181], v[200:203], v[26:29]
	v_mfma_f32_16x16x32_bf16 v[18:21], v[178:181], v[208:211], v[18:21]
	v_mfma_f32_16x16x32_bf16 v[22:25], v[154:157], v[208:211], v[22:25]
	v_mfma_f32_16x16x32_bf16 v[14:17], v[154:157], v[216:219], v[14:17]
	v_mfma_f32_16x16x32_bf16 v[10:13], v[178:181], v[216:219], v[10:13]
	s_barrier
	s_setprio 3
	v_mfma_f32_16x16x32_bf16 v[2:5], v[178:181], v[226:229], v[2:5]
	v_mfma_f32_16x16x32_bf16 v[6:9], v[154:157], v[226:229], v[6:9]
	s_setprio 0
	s_add_u32 s30, s30, 0x40180
	s_addc_u32 s31, s31, 0
	s_add_u32 s68, s22, 0x200
	s_addc_u32 s69, s23, 0
	s_mov_b32 s70, 0
.LBB0_287:
	ds_read_b128 v[134:137], v198
	ds_read_b128 v[138:141], v198 offset:1024
	ds_read_b128 v[142:145], v198 offset:2048
	ds_read_b128 v[146:149], v198 offset:3072
	ds_read_b128 v[150:153], v199
	ds_read_b128 v[154:157], v199 offset:1024
	ds_read_b128 v[158:161], v199 offset:2048
	ds_read_b128 v[178:181], v199 offset:3072
	s_add_u32 s14, s30, 0xfffc0080
	s_addc_u32 s22, s31, -1
	s_cmp_eq_u32 s70, 12
	s_cselect_b32 s37, s54, s22
	s_cselect_b32 s36, s55, s14
	s_cselect_b32 s23, s56, s69
	s_cselect_b32 s22, s57, s68
	s_mov_b32 m0, s58
	v_lshl_add_u64 v[162:163], s[30:31], 0, v[170:171]
	ds_read_b128 v[182:185], v197
	ds_read_b128 v[190:193], v197 offset:1024
	ds_read_b128 v[200:203], v197 offset:2048
	ds_read_b128 v[204:207], v197 offset:3072
	ds_read_b128 v[208:211], v197 offset:4096
	ds_read_b128 v[212:215], v197 offset:5120
	ds_read_b128 v[216:219], v197 offset:6144
	ds_read_b128 v[222:225], v197 offset:7168
	global_load_lds_dwordx4 v[162:163], off
	v_lshl_add_u64 v[162:163], s[30:31], 0, v[172:173]
	s_mov_b32 m0, s59
	s_nop 0
	global_load_lds_dwordx4 v[162:163], off
	s_waitcnt vmcnt(8)
	s_waitcnt lgkmcnt(0)
	s_barrier
	s_setprio 1
	s_waitcnt lgkmcnt(0)
	v_mfma_f32_16x16x32_bf16 v[128:131], v[134:137], v[182:185], v[128:131]
	v_mfma_f32_16x16x32_bf16 v[124:127], v[142:145], v[182:185], v[124:127]
	v_mfma_f32_16x16x32_bf16 v[116:119], v[142:145], v[200:203], v[116:119]
	v_mfma_f32_16x16x32_bf16 v[120:123], v[134:137], v[200:203], v[120:123]
	v_mfma_f32_16x16x32_bf16 v[112:115], v[134:137], v[208:211], v[112:115]
	v_mfma_f32_16x16x32_bf16 v[108:111], v[142:145], v[208:211], v[108:111]
	v_mfma_f32_16x16x32_bf16 v[100:103], v[142:145], v[216:219], v[100:103]
	v_mfma_f32_16x16x32_bf16 v[104:107], v[134:137], v[216:219], v[104:107]
	v_mfma_f32_16x16x32_bf16 v[128:131], v[138:141], v[190:193], v[128:131]
	v_mfma_f32_16x16x32_bf16 v[124:127], v[146:149], v[190:193], v[124:127]
	v_mfma_f32_16x16x32_bf16 v[116:119], v[146:149], v[204:207], v[116:119]
	v_mfma_f32_16x16x32_bf16 v[120:123], v[138:141], v[204:207], v[120:123]
	v_mfma_f32_16x16x32_bf16 v[112:115], v[138:141], v[212:215], v[112:115]
	v_mfma_f32_16x16x32_bf16 v[108:111], v[146:149], v[212:215], v[108:111]
	v_mfma_f32_16x16x32_bf16 v[100:103], v[146:149], v[222:225], v[100:103]
	v_mfma_f32_16x16x32_bf16 v[104:107], v[138:141], v[222:225], v[104:107]
	s_setprio 0
	s_setprio 1
	v_mfma_f32_16x16x32_bf16 v[96:99], v[150:153], v[182:185], v[96:99]
	v_mfma_f32_16x16x32_bf16 v[92:95], v[158:161], v[182:185], v[92:95]
	v_mfma_f32_16x16x32_bf16 v[84:87], v[158:161], v[200:203], v[84:87]
	v_mfma_f32_16x16x32_bf16 v[88:91], v[150:153], v[200:203], v[88:91]
	v_mfma_f32_16x16x32_bf16 v[80:83], v[150:153], v[208:211], v[80:83]
	v_mfma_f32_16x16x32_bf16 v[76:79], v[158:161], v[208:211], v[76:79]
	v_mfma_f32_16x16x32_bf16 v[68:71], v[158:161], v[216:219], v[68:71]
	v_mfma_f32_16x16x32_bf16 v[72:75], v[150:153], v[216:219], v[72:75]
	v_mfma_f32_16x16x32_bf16 v[96:99], v[154:157], v[190:193], v[96:99]
	v_mfma_f32_16x16x32_bf16 v[92:95], v[178:181], v[190:193], v[92:95]
	v_mfma_f32_16x16x32_bf16 v[84:87], v[178:181], v[204:207], v[84:87]
	v_mfma_f32_16x16x32_bf16 v[88:91], v[154:157], v[204:207], v[88:91]
	v_mfma_f32_16x16x32_bf16 v[80:83], v[154:157], v[212:215], v[80:83]
	v_mfma_f32_16x16x32_bf16 v[76:79], v[178:181], v[212:215], v[76:79]
	s_barrier
	s_setprio 3
	v_mfma_f32_16x16x32_bf16 v[68:71], v[178:181], v[222:225], v[68:71]
	v_mfma_f32_16x16x32_bf16 v[72:75], v[154:157], v[222:225], v[72:75]
	s_setprio 0
	s_mov_b32 m0, s60
	v_lshl_add_u64 v[162:163], s[22:23], 0, v[34:35]
	s_add_u32 s72, s22, 0x40000
	ds_read_b128 v[182:185], v197 offset:16384
	ds_read_b128 v[190:193], v197 offset:17408
	ds_read_b128 v[200:203], v197 offset:18432
	ds_read_b128 v[204:207], v197 offset:19456
	ds_read_b128 v[208:211], v197 offset:20480
	ds_read_b128 v[212:215], v197 offset:21504
	ds_read_b128 v[216:219], v197 offset:22528
	ds_read_b128 v[222:225], v197 offset:23552
	global_load_lds_dwordx4 v[162:163], off
	v_lshl_add_u64 v[174:175], s[22:23], 0, v[164:165]
	s_mov_b32 m0, s61
	s_addc_u32 s73, s23, 0
	global_load_lds_dwordx4 v[174:175], off
	v_lshl_add_u64 v[194:195], s[72:73], 0, v[34:35]
	s_mov_b32 m0, s62
	v_lshl_add_u64 v[226:227], s[36:37], 0, v[166:167]
	global_load_lds_dwordx4 v[194:195], off
	v_lshl_add_u64 v[194:195], s[72:73], 0, v[164:165]
	s_mov_b32 m0, s63
	s_nop 0
	global_load_lds_dwordx4 v[194:195], off
	v_lshl_add_u64 v[194:195], s[36:37], 0, v[168:169]
	s_mov_b32 m0, s41
	s_nop 0
	global_load_lds_dwordx4 v[194:195], off
	s_mov_b32 m0, s42
	s_nop 0
	global_load_lds_dwordx4 v[226:227], off
	s_waitcnt vmcnt(8)
	s_waitcnt lgkmcnt(0)
	s_barrier
	s_setprio 1
	s_waitcnt lgkmcnt(0)
	v_mfma_f32_16x16x32_bf16 v[64:67], v[134:137], v[182:185], v[64:67]
	v_mfma_f32_16x16x32_bf16 v[60:63], v[142:145], v[182:185], v[60:63]
	v_mfma_f32_16x16x32_bf16 v[52:55], v[142:145], v[200:203], v[52:55]
	v_mfma_f32_16x16x32_bf16 v[56:59], v[134:137], v[200:203], v[56:59]
	v_mfma_f32_16x16x32_bf16 v[48:51], v[134:137], v[208:211], v[48:51]
	v_mfma_f32_16x16x32_bf16 v[44:47], v[142:145], v[208:211], v[44:47]
	v_mfma_f32_16x16x32_bf16 v[36:39], v[142:145], v[216:219], v[36:39]
	v_mfma_f32_16x16x32_bf16 v[40:43], v[134:137], v[216:219], v[40:43]
	v_mfma_f32_16x16x32_bf16 v[64:67], v[138:141], v[190:193], v[64:67]
	v_mfma_f32_16x16x32_bf16 v[60:63], v[146:149], v[190:193], v[60:63]
	v_mfma_f32_16x16x32_bf16 v[52:55], v[146:149], v[204:207], v[52:55]
	v_mfma_f32_16x16x32_bf16 v[56:59], v[138:141], v[204:207], v[56:59]
	v_mfma_f32_16x16x32_bf16 v[48:51], v[138:141], v[212:215], v[48:51]
	v_mfma_f32_16x16x32_bf16 v[44:47], v[146:149], v[212:215], v[44:47]
	v_mfma_f32_16x16x32_bf16 v[36:39], v[146:149], v[222:225], v[36:39]
	v_mfma_f32_16x16x32_bf16 v[40:43], v[138:141], v[222:225], v[40:43]
	s_setprio 0
	s_setprio 1
	v_mfma_f32_16x16x32_bf16 v[30:33], v[150:153], v[182:185], v[30:33]
	v_mfma_f32_16x16x32_bf16 v[26:29], v[158:161], v[182:185], v[26:29]
	v_mfma_f32_16x16x32_bf16 v[18:21], v[158:161], v[200:203], v[18:21]
	v_mfma_f32_16x16x32_bf16 v[22:25], v[150:153], v[200:203], v[22:25]
	v_mfma_f32_16x16x32_bf16 v[14:17], v[150:153], v[208:211], v[14:17]
	v_mfma_f32_16x16x32_bf16 v[10:13], v[158:161], v[208:211], v[10:13]
	v_mfma_f32_16x16x32_bf16 v[2:5], v[158:161], v[216:219], v[2:5]
	v_mfma_f32_16x16x32_bf16 v[6:9], v[150:153], v[216:219], v[6:9]
	v_mfma_f32_16x16x32_bf16 v[30:33], v[154:157], v[190:193], v[30:33]
	v_mfma_f32_16x16x32_bf16 v[26:29], v[178:181], v[190:193], v[26:29]
	v_mfma_f32_16x16x32_bf16 v[18:21], v[178:181], v[204:207], v[18:21]
	v_mfma_f32_16x16x32_bf16 v[22:25], v[154:157], v[204:207], v[22:25]
	v_mfma_f32_16x16x32_bf16 v[14:17], v[154:157], v[212:215], v[14:17]
	v_mfma_f32_16x16x32_bf16 v[10:13], v[178:181], v[212:215], v[10:13]
	s_barrier
	s_setprio 3
	v_mfma_f32_16x16x32_bf16 v[2:5], v[178:181], v[222:225], v[2:5]
	v_mfma_f32_16x16x32_bf16 v[6:9], v[154:157], v[222:225], v[6:9]
	s_setprio 0
	ds_read_b128 v[134:137], v132
	ds_read_b128 v[138:141], v132 offset:1024
	ds_read_b128 v[142:145], v132 offset:2048
	ds_read_b128 v[146:149], v132 offset:3072
	ds_read_b128 v[150:153], v133
	ds_read_b128 v[154:157], v133 offset:1024
	ds_read_b128 v[158:161], v133 offset:2048
	ds_read_b128 v[178:181], v133 offset:3072
	s_add_u32 s36, s36, 0x40000
	s_addc_u32 s37, s37, 0
	s_mov_b32 m0, s43
	v_lshl_add_u64 v[228:229], s[36:37], 0, v[168:169]
	ds_read_b128 v[182:185], v197 offset:32768
	ds_read_b128 v[190:193], v197 offset:33792
	ds_read_b128 v[200:203], v197 offset:34816
	ds_read_b128 v[204:207], v197 offset:35840
	ds_read_b128 v[208:211], v197 offset:36864
	ds_read_b128 v[212:215], v197 offset:37888
	ds_read_b128 v[216:219], v197 offset:38912
	ds_read_b128 v[222:225], v197 offset:39936
	global_load_lds_dwordx4 v[228:229], off
	v_lshl_add_u64 v[228:229], s[36:37], 0, v[166:167]
	s_mov_b32 m0, s44
	s_nop 0
	global_load_lds_dwordx4 v[228:229], off
	s_waitcnt vmcnt(8)
	s_waitcnt lgkmcnt(0)
	s_barrier
	s_setprio 1
	s_waitcnt lgkmcnt(0)
	v_mfma_f32_16x16x32_bf16 v[128:131], v[134:137], v[182:185], v[128:131]
	v_mfma_f32_16x16x32_bf16 v[124:127], v[142:145], v[182:185], v[124:127]
	v_mfma_f32_16x16x32_bf16 v[116:119], v[142:145], v[200:203], v[116:119]
	v_mfma_f32_16x16x32_bf16 v[120:123], v[134:137], v[200:203], v[120:123]
	v_mfma_f32_16x16x32_bf16 v[112:115], v[134:137], v[208:211], v[112:115]
	v_mfma_f32_16x16x32_bf16 v[108:111], v[142:145], v[208:211], v[108:111]
	v_mfma_f32_16x16x32_bf16 v[100:103], v[142:145], v[216:219], v[100:103]
	v_mfma_f32_16x16x32_bf16 v[104:107], v[134:137], v[216:219], v[104:107]
	v_mfma_f32_16x16x32_bf16 v[128:131], v[138:141], v[190:193], v[128:131]
	v_mfma_f32_16x16x32_bf16 v[124:127], v[146:149], v[190:193], v[124:127]
	v_mfma_f32_16x16x32_bf16 v[116:119], v[146:149], v[204:207], v[116:119]
	v_mfma_f32_16x16x32_bf16 v[120:123], v[138:141], v[204:207], v[120:123]
	v_mfma_f32_16x16x32_bf16 v[112:115], v[138:141], v[212:215], v[112:115]
	v_mfma_f32_16x16x32_bf16 v[108:111], v[146:149], v[212:215], v[108:111]
	v_mfma_f32_16x16x32_bf16 v[100:103], v[146:149], v[222:225], v[100:103]
	v_mfma_f32_16x16x32_bf16 v[104:107], v[138:141], v[222:225], v[104:107]
	s_setprio 0
	s_setprio 1
	v_mfma_f32_16x16x32_bf16 v[96:99], v[150:153], v[182:185], v[96:99]
	v_mfma_f32_16x16x32_bf16 v[92:95], v[158:161], v[182:185], v[92:95]
	v_mfma_f32_16x16x32_bf16 v[84:87], v[158:161], v[200:203], v[84:87]
	v_mfma_f32_16x16x32_bf16 v[88:91], v[150:153], v[200:203], v[88:91]
	v_mfma_f32_16x16x32_bf16 v[80:83], v[150:153], v[208:211], v[80:83]
	v_mfma_f32_16x16x32_bf16 v[76:79], v[158:161], v[208:211], v[76:79]
	v_mfma_f32_16x16x32_bf16 v[68:71], v[158:161], v[216:219], v[68:71]
	v_mfma_f32_16x16x32_bf16 v[72:75], v[150:153], v[216:219], v[72:75]
	v_mfma_f32_16x16x32_bf16 v[96:99], v[154:157], v[190:193], v[96:99]
	v_mfma_f32_16x16x32_bf16 v[92:95], v[178:181], v[190:193], v[92:95]
	v_mfma_f32_16x16x32_bf16 v[84:87], v[178:181], v[204:207], v[84:87]
	v_mfma_f32_16x16x32_bf16 v[88:91], v[154:157], v[204:207], v[88:91]
	v_mfma_f32_16x16x32_bf16 v[80:83], v[154:157], v[212:215], v[80:83]
	v_mfma_f32_16x16x32_bf16 v[76:79], v[178:181], v[212:215], v[76:79]
	s_barrier
	s_setprio 3
	v_mfma_f32_16x16x32_bf16 v[68:71], v[178:181], v[222:225], v[68:71]
	v_mfma_f32_16x16x32_bf16 v[72:75], v[154:157], v[222:225], v[72:75]
	s_setprio 0
	s_mov_b32 m0, s64
	v_lshl_add_u64 v[162:163], v[162:163], 0, s[18:19]
	s_add_u32 s22, s22, 0x40080
	ds_read_b128 v[182:185], v197 offset:49152
	ds_read_b128 v[190:193], v197 offset:50176
	ds_read_b128 v[200:203], v197 offset:51200
	ds_read_b128 v[204:207], v197 offset:52224
	ds_read_b128 v[208:211], v197 offset:53248
	ds_read_b128 v[212:215], v197 offset:54272
	ds_read_b128 v[216:219], v197 offset:55296
	ds_read_b128 v[222:225], v197 offset:56320
	global_load_lds_dwordx4 v[162:163], off
	v_lshl_add_u64 v[162:163], v[174:175], 0, s[18:19]
	s_mov_b32 m0, s65
	s_addc_u32 s23, s23, 0
	global_load_lds_dwordx4 v[162:163], off
	v_lshl_add_u64 v[162:163], s[22:23], 0, v[34:35]
	s_mov_b32 m0, s66
	s_nop 0
	global_load_lds_dwordx4 v[162:163], off
	v_lshl_add_u64 v[162:163], s[22:23], 0, v[164:165]
	s_mov_b32 m0, s67
	s_nop 0
	global_load_lds_dwordx4 v[162:163], off
	v_lshl_add_u64 v[162:163], v[194:195], 0, s[18:19]
	s_mov_b32 m0, s47
	s_nop 0
	global_load_lds_dwordx4 v[162:163], off
	v_lshl_add_u64 v[162:163], v[226:227], 0, s[18:19]
	s_mov_b32 m0, s48
	s_nop 0
	global_load_lds_dwordx4 v[162:163], off
	s_waitcnt vmcnt(8)
	s_waitcnt lgkmcnt(0)
	s_barrier
	s_setprio 1
	s_waitcnt lgkmcnt(0)
	v_mfma_f32_16x16x32_bf16 v[64:67], v[134:137], v[182:185], v[64:67]
	v_mfma_f32_16x16x32_bf16 v[60:63], v[142:145], v[182:185], v[60:63]
	v_mfma_f32_16x16x32_bf16 v[52:55], v[142:145], v[200:203], v[52:55]
	v_mfma_f32_16x16x32_bf16 v[56:59], v[134:137], v[200:203], v[56:59]
	v_mfma_f32_16x16x32_bf16 v[48:51], v[134:137], v[208:211], v[48:51]
	v_mfma_f32_16x16x32_bf16 v[44:47], v[142:145], v[208:211], v[44:47]
	v_mfma_f32_16x16x32_bf16 v[36:39], v[142:145], v[216:219], v[36:39]
	v_mfma_f32_16x16x32_bf16 v[40:43], v[134:137], v[216:219], v[40:43]
	v_mfma_f32_16x16x32_bf16 v[64:67], v[138:141], v[190:193], v[64:67]
	v_mfma_f32_16x16x32_bf16 v[60:63], v[146:149], v[190:193], v[60:63]
	v_mfma_f32_16x16x32_bf16 v[52:55], v[146:149], v[204:207], v[52:55]
	v_mfma_f32_16x16x32_bf16 v[56:59], v[138:141], v[204:207], v[56:59]
	v_mfma_f32_16x16x32_bf16 v[48:51], v[138:141], v[212:215], v[48:51]
	v_mfma_f32_16x16x32_bf16 v[44:47], v[146:149], v[212:215], v[44:47]
	v_mfma_f32_16x16x32_bf16 v[36:39], v[146:149], v[222:225], v[36:39]
	v_mfma_f32_16x16x32_bf16 v[40:43], v[138:141], v[222:225], v[40:43]
	s_setprio 0
	s_setprio 1
	v_mfma_f32_16x16x32_bf16 v[30:33], v[150:153], v[182:185], v[30:33]
	v_mfma_f32_16x16x32_bf16 v[26:29], v[158:161], v[182:185], v[26:29]
	v_mfma_f32_16x16x32_bf16 v[18:21], v[158:161], v[200:203], v[18:21]
	v_mfma_f32_16x16x32_bf16 v[22:25], v[150:153], v[200:203], v[22:25]
	v_mfma_f32_16x16x32_bf16 v[14:17], v[150:153], v[208:211], v[14:17]
	v_mfma_f32_16x16x32_bf16 v[10:13], v[158:161], v[208:211], v[10:13]
	v_mfma_f32_16x16x32_bf16 v[2:5], v[158:161], v[216:219], v[2:5]
	v_mfma_f32_16x16x32_bf16 v[6:9], v[150:153], v[216:219], v[6:9]
	v_mfma_f32_16x16x32_bf16 v[30:33], v[154:157], v[190:193], v[30:33]
	v_mfma_f32_16x16x32_bf16 v[26:29], v[178:181], v[190:193], v[26:29]
	v_mfma_f32_16x16x32_bf16 v[18:21], v[178:181], v[204:207], v[18:21]
	v_mfma_f32_16x16x32_bf16 v[22:25], v[154:157], v[204:207], v[22:25]
	v_mfma_f32_16x16x32_bf16 v[14:17], v[154:157], v[212:215], v[14:17]
	v_mfma_f32_16x16x32_bf16 v[10:13], v[178:181], v[212:215], v[10:13]
	s_barrier
	s_setprio 3
	v_mfma_f32_16x16x32_bf16 v[2:5], v[178:181], v[222:225], v[2:5]
	v_mfma_f32_16x16x32_bf16 v[6:9], v[154:157], v[222:225], v[6:9]
	s_setprio 0
	s_add_i32 s70, s70, 2
	s_add_u32 s30, s30, 0x100
	s_addc_u32 s31, s31, 0
	s_add_u32 s68, s68, 0x100
	s_addc_u32 s69, s69, 0
	s_cmp_gt_u32 s70, 13
	s_cbranch_scc0 .LBB0_287
	s_and_b64 vcc, exec, s[8:9]
	s_cbranch_vccz .LBB0_290
	s_barrier

.LBB0_540:
	s_lshl_b32 s14, s55, 19
	v_readlane_b32 s16, v253, 53
	v_readlane_b32 s17, v253, 54
	s_add_u32 s16, s16, s14
	s_addc_u32 s17, s17, 0
	s_and_b64 s[22:23], s[4:5], exec
	s_cselect_b32 s58, s17, s37
	s_cselect_b32 s59, s16, s36
	s_lshl_b32 s14, s54, 19
	s_add_u32 s22, s15, s14
	s_addc_u32 s23, s26, 0
	s_and_b64 s[40:41], s[4:5], exec
	s_cselect_b32 s60, s23, s31
	s_cselect_b32 s61, s22, s30
	s_add_i32 s64, 0, 0x10000
	v_add_u32_e32 v172, s64, v222
	s_add_i32 s66, 0, 0x14000
	v_add_u32_e32 v173, s66, v222
	ds_read_b128 v[160:163], v172
	ds_read_b128 v[152:155], v172 offset:1024
	ds_read_b128 v[156:159], v172 offset:2048
	ds_read_b128 v[148:151], v172 offset:3072
	ds_read_b128 v[144:147], v173
	ds_read_b128 v[136:139], v173 offset:1024
	ds_read_b128 v[140:143], v173 offset:2048
	ds_read_b128 v[132:135], v173 offset:3072
	s_add_u32 s40, s36, 0x40080
	s_addc_u32 s41, s37, 0
	s_add_i32 s62, s43, 0xc000
	v_lshl_add_u64 v[174:175], s[40:41], 0, v[194:195]
	s_mov_b32 m0, s62
	s_add_i32 s63, s43, 0xe000
	ds_read_b128 v[164:167], v223
	ds_read_b128 v[168:171], v223 offset:1024
	ds_read_b128 v[178:181], v223 offset:2048
	ds_read_b128 v[182:185], v223 offset:3072
	ds_read_b128 v[200:203], v223 offset:4096
	ds_read_b128 v[204:207], v223 offset:5120
	ds_read_b128 v[208:211], v223 offset:6144
	ds_read_b128 v[212:215], v223 offset:7168
	global_load_lds_dwordx4 v[174:175], off
	v_lshl_add_u64 v[174:175], s[40:41], 0, v[192:193]
	s_mov_b32 m0, s63
	s_nop 0
	global_load_lds_dwordx4 v[174:175], off
	s_waitcnt vmcnt(8)
	s_waitcnt lgkmcnt(0)
	s_barrier
	s_setprio 1
	s_waitcnt lgkmcnt(0)
	v_mfma_f32_16x16x32_bf16 v[128:131], v[160:163], v[164:167], 0
	v_mfma_f32_16x16x32_bf16 v[124:127], v[156:159], v[164:167], 0
	v_mfma_f32_16x16x32_bf16 v[116:119], v[156:159], v[178:181], 0
	v_mfma_f32_16x16x32_bf16 v[120:123], v[160:163], v[178:181], 0
	v_mfma_f32_16x16x32_bf16 v[112:115], v[160:163], v[200:203], 0
	v_mfma_f32_16x16x32_bf16 v[108:111], v[156:159], v[200:203], 0
	v_mfma_f32_16x16x32_bf16 v[100:103], v[156:159], v[208:211], 0
	v_mfma_f32_16x16x32_bf16 v[104:107], v[160:163], v[208:211], 0
	s_nop 0
	v_mfma_f32_16x16x32_bf16 v[128:131], v[152:155], v[168:171], v[128:131]
	v_mfma_f32_16x16x32_bf16 v[124:127], v[148:151], v[168:171], v[124:127]
	v_mfma_f32_16x16x32_bf16 v[116:119], v[148:151], v[182:185], v[116:119]
	v_mfma_f32_16x16x32_bf16 v[120:123], v[152:155], v[182:185], v[120:123]
	v_mfma_f32_16x16x32_bf16 v[112:115], v[152:155], v[204:207], v[112:115]
	v_mfma_f32_16x16x32_bf16 v[108:111], v[148:151], v[204:207], v[108:111]
	v_mfma_f32_16x16x32_bf16 v[100:103], v[148:151], v[212:215], v[100:103]
	v_mfma_f32_16x16x32_bf16 v[104:107], v[152:155], v[212:215], v[104:107]
	s_setprio 0
	s_setprio 1
	v_mfma_f32_16x16x32_bf16 v[96:99], v[144:147], v[164:167], 0
	v_mfma_f32_16x16x32_bf16 v[92:95], v[140:143], v[164:167], 0
	v_mfma_f32_16x16x32_bf16 v[84:87], v[140:143], v[178:181], 0
	v_mfma_f32_16x16x32_bf16 v[88:91], v[144:147], v[178:181], 0
	v_mfma_f32_16x16x32_bf16 v[80:83], v[144:147], v[200:203], 0
	v_mfma_f32_16x16x32_bf16 v[76:79], v[140:143], v[200:203], 0
	v_mfma_f32_16x16x32_bf16 v[68:71], v[140:143], v[208:211], 0
	v_mfma_f32_16x16x32_bf16 v[72:75], v[144:147], v[208:211], 0
	s_nop 0
	v_mfma_f32_16x16x32_bf16 v[96:99], v[136:139], v[168:171], v[96:99]
	v_mfma_f32_16x16x32_bf16 v[92:95], v[132:135], v[168:171], v[92:95]
	v_mfma_f32_16x16x32_bf16 v[84:87], v[132:135], v[182:185], v[84:87]
	v_mfma_f32_16x16x32_bf16 v[88:91], v[136:139], v[182:185], v[88:91]
	v_mfma_f32_16x16x32_bf16 v[80:83], v[136:139], v[204:207], v[80:83]
	v_mfma_f32_16x16x32_bf16 v[76:79], v[132:135], v[204:207], v[76:79]
	s_barrier
	s_setprio 3
	v_mfma_f32_16x16x32_bf16 v[68:71], v[132:135], v[212:215], v[68:71]
	v_mfma_f32_16x16x32_bf16 v[72:75], v[136:139], v[212:215], v[72:75]
	s_setprio 0
	v_lshl_add_u64 v[164:165], s[30:31], 0, v[34:35]
	s_add_i32 s64, s64, s42
	v_lshl_add_u64 v[166:167], v[164:165], 0, s[28:29]
	s_mov_b32 m0, s64
	s_add_i32 s65, s64, 0x2000
	ds_read_b128 v[178:181], v223 offset:16384
	ds_read_b128 v[182:185], v223 offset:17408
	ds_read_b128 v[200:203], v223 offset:18432
	ds_read_b128 v[204:207], v223 offset:19456
	ds_read_b128 v[208:211], v223 offset:20480
	ds_read_b128 v[212:215], v223 offset:21504
	ds_read_b128 v[216:219], v223 offset:22528
	ds_read_b128 v[224:227], v223 offset:23552
	global_load_lds_dwordx4 v[166:167], off
	v_lshl_add_u64 v[166:167], s[30:31], 0, v[190:191]
	s_add_u32 s40, s30, 0x40100
	v_lshl_add_u64 v[168:169], v[166:167], 0, s[28:29]
	s_mov_b32 m0, s65
	s_addc_u32 s41, s31, 0
	s_add_i32 s66, s66, s42
	global_load_lds_dwordx4 v[168:169], off
	v_lshl_add_u64 v[168:169], s[40:41], 0, v[34:35]
	s_mov_b32 m0, s66
	s_add_i32 s67, s66, 0x2000
	global_load_lds_dwordx4 v[168:169], off
	v_lshl_add_u64 v[168:169], s[40:41], 0, v[190:191]
	s_mov_b32 m0, s67
	s_nop 0
	global_load_lds_dwordx4 v[168:169], off
	v_lshl_add_u64 v[168:169], s[36:37], 0, v[194:195]
	v_lshl_add_u64 v[170:171], v[168:169], 0, s[28:29]
	s_mov_b32 m0, s43
	s_nop 0
	global_load_lds_dwordx4 v[170:171], off
	v_lshl_add_u64 v[170:171], s[36:37], 0, v[192:193]
	v_lshl_add_u64 v[174:175], v[170:171], 0, s[28:29]
	s_mov_b32 m0, s44
	s_nop 0
	global_load_lds_dwordx4 v[174:175], off
	s_waitcnt vmcnt(8)
	s_waitcnt lgkmcnt(0)
	s_barrier
	s_setprio 1
	s_waitcnt lgkmcnt(0)
	v_mfma_f32_16x16x32_bf16 v[64:67], v[160:163], v[178:181], 0
	v_mfma_f32_16x16x32_bf16 v[60:63], v[156:159], v[178:181], 0
	v_mfma_f32_16x16x32_bf16 v[52:55], v[156:159], v[200:203], 0
	v_mfma_f32_16x16x32_bf16 v[56:59], v[160:163], v[200:203], 0
	v_mfma_f32_16x16x32_bf16 v[48:51], v[160:163], v[208:211], 0
	v_mfma_f32_16x16x32_bf16 v[44:47], v[156:159], v[208:211], 0
	v_mfma_f32_16x16x32_bf16 v[36:39], v[156:159], v[216:219], 0
	v_mfma_f32_16x16x32_bf16 v[40:43], v[160:163], v[216:219], 0
	s_nop 0
	v_mfma_f32_16x16x32_bf16 v[64:67], v[152:155], v[182:185], v[64:67]
	v_mfma_f32_16x16x32_bf16 v[60:63], v[148:151], v[182:185], v[60:63]
	v_mfma_f32_16x16x32_bf16 v[52:55], v[148:151], v[204:207], v[52:55]
	v_mfma_f32_16x16x32_bf16 v[56:59], v[152:155], v[204:207], v[56:59]
	v_mfma_f32_16x16x32_bf16 v[48:51], v[152:155], v[212:215], v[48:51]
	v_mfma_f32_16x16x32_bf16 v[44:47], v[148:151], v[212:215], v[44:47]
	v_mfma_f32_16x16x32_bf16 v[36:39], v[148:151], v[224:227], v[36:39]
	v_mfma_f32_16x16x32_bf16 v[40:43], v[152:155], v[224:227], v[40:43]
	s_setprio 0
	s_setprio 1
	v_mfma_f32_16x16x32_bf16 v[30:33], v[144:147], v[178:181], 0
	v_mfma_f32_16x16x32_bf16 v[26:29], v[140:143], v[178:181], 0
	v_mfma_f32_16x16x32_bf16 v[18:21], v[140:143], v[200:203], 0
	v_mfma_f32_16x16x32_bf16 v[22:25], v[144:147], v[200:203], 0
	v_mfma_f32_16x16x32_bf16 v[14:17], v[144:147], v[208:211], 0
	v_mfma_f32_16x16x32_bf16 v[10:13], v[140:143], v[208:211], 0
	v_mfma_f32_16x16x32_bf16 v[2:5], v[140:143], v[216:219], 0
	v_mfma_f32_16x16x32_bf16 v[6:9], v[144:147], v[216:219], 0
	s_nop 0
	v_mfma_f32_16x16x32_bf16 v[30:33], v[136:139], v[182:185], v[30:33]
	v_mfma_f32_16x16x32_bf16 v[26:29], v[132:135], v[182:185], v[26:29]
	v_mfma_f32_16x16x32_bf16 v[18:21], v[132:135], v[204:207], v[18:21]
	v_mfma_f32_16x16x32_bf16 v[22:25], v[136:139], v[204:207], v[22:25]
	v_mfma_f32_16x16x32_bf16 v[14:17], v[136:139], v[212:215], v[14:17]
	v_mfma_f32_16x16x32_bf16 v[10:13], v[132:135], v[212:215], v[10:13]
	s_barrier
	s_setprio 3
	v_mfma_f32_16x16x32_bf16 v[2:5], v[132:135], v[224:227], v[2:5]
	v_mfma_f32_16x16x32_bf16 v[6:9], v[136:139], v[224:227], v[6:9]
	s_setprio 0
	s_add_i32 s68, 0, 0x18000
	s_add_i32 s70, 0, 0x1c000
	v_add_u32_e32 v132, s68, v222
	v_add_u32_e32 v133, s70, v222
	ds_read_b128 v[134:137], v132
	ds_read_b128 v[138:141], v132 offset:1024
	ds_read_b128 v[142:145], v132 offset:2048
	ds_read_b128 v[146:149], v132 offset:3072
	ds_read_b128 v[150:153], v133
	ds_read_b128 v[154:157], v133 offset:1024
	ds_read_b128 v[158:161], v133 offset:2048
	ds_read_b128 v[178:181], v133 offset:3072
	s_add_u32 s40, s36, 0x40100
	s_addc_u32 s41, s37, 0
	s_mov_b32 m0, s45
	v_lshl_add_u64 v[162:163], s[40:41], 0, v[194:195]
	ds_read_b128 v[182:185], v223 offset:32768
	ds_read_b128 v[200:203], v223 offset:33792
	ds_read_b128 v[204:207], v223 offset:34816
	ds_read_b128 v[208:211], v223 offset:35840
	ds_read_b128 v[212:215], v223 offset:36864
	ds_read_b128 v[216:219], v223 offset:37888
	ds_read_b128 v[224:227], v223 offset:38912
	ds_read_b128 v[228:231], v223 offset:39936
	global_load_lds_dwordx4 v[162:163], off
	v_lshl_add_u64 v[162:163], s[40:41], 0, v[192:193]
	s_mov_b32 m0, s46
	s_nop 0
	global_load_lds_dwordx4 v[162:163], off
	s_waitcnt vmcnt(8)
	s_waitcnt lgkmcnt(0)
	s_barrier
	s_setprio 1
	s_waitcnt lgkmcnt(0)
	v_mfma_f32_16x16x32_bf16 v[128:131], v[134:137], v[182:185], v[128:131]
	v_mfma_f32_16x16x32_bf16 v[124:127], v[142:145], v[182:185], v[124:127]
	v_mfma_f32_16x16x32_bf16 v[116:119], v[142:145], v[204:207], v[116:119]
	v_mfma_f32_16x16x32_bf16 v[120:123], v[134:137], v[204:207], v[120:123]
	v_mfma_f32_16x16x32_bf16 v[112:115], v[134:137], v[212:215], v[112:115]
	v_mfma_f32_16x16x32_bf16 v[108:111], v[142:145], v[212:215], v[108:111]
	v_mfma_f32_16x16x32_bf16 v[100:103], v[142:145], v[224:227], v[100:103]
	v_mfma_f32_16x16x32_bf16 v[104:107], v[134:137], v[224:227], v[104:107]
	v_mfma_f32_16x16x32_bf16 v[128:131], v[138:141], v[200:203], v[128:131]
	v_mfma_f32_16x16x32_bf16 v[124:127], v[146:149], v[200:203], v[124:127]
	v_mfma_f32_16x16x32_bf16 v[116:119], v[146:149], v[208:211], v[116:119]
	v_mfma_f32_16x16x32_bf16 v[120:123], v[138:141], v[208:211], v[120:123]
	v_mfma_f32_16x16x32_bf16 v[112:115], v[138:141], v[216:219], v[112:115]
	v_mfma_f32_16x16x32_bf16 v[108:111], v[146:149], v[216:219], v[108:111]
	v_mfma_f32_16x16x32_bf16 v[100:103], v[146:149], v[228:231], v[100:103]
	v_mfma_f32_16x16x32_bf16 v[104:107], v[138:141], v[228:231], v[104:107]
	s_setprio 0
	s_setprio 1
	v_mfma_f32_16x16x32_bf16 v[96:99], v[150:153], v[182:185], v[96:99]
	v_mfma_f32_16x16x32_bf16 v[92:95], v[158:161], v[182:185], v[92:95]
	v_mfma_f32_16x16x32_bf16 v[84:87], v[158:161], v[204:207], v[84:87]
	v_mfma_f32_16x16x32_bf16 v[88:91], v[150:153], v[204:207], v[88:91]
	v_mfma_f32_16x16x32_bf16 v[80:83], v[150:153], v[212:215], v[80:83]
	v_mfma_f32_16x16x32_bf16 v[76:79], v[158:161], v[212:215], v[76:79]
	v_mfma_f32_16x16x32_bf16 v[68:71], v[158:161], v[224:227], v[68:71]
	v_mfma_f32_16x16x32_bf16 v[72:75], v[150:153], v[224:227], v[72:75]
	v_mfma_f32_16x16x32_bf16 v[96:99], v[154:157], v[200:203], v[96:99]
	v_mfma_f32_16x16x32_bf16 v[92:95], v[178:181], v[200:203], v[92:95]
	v_mfma_f32_16x16x32_bf16 v[84:87], v[178:181], v[208:211], v[84:87]
	v_mfma_f32_16x16x32_bf16 v[88:91], v[154:157], v[208:211], v[88:91]
	v_mfma_f32_16x16x32_bf16 v[80:83], v[154:157], v[216:219], v[80:83]
	v_mfma_f32_16x16x32_bf16 v[76:79], v[178:181], v[216:219], v[76:79]
	s_barrier
	s_setprio 3
	v_mfma_f32_16x16x32_bf16 v[68:71], v[178:181], v[228:231], v[68:71]
	v_mfma_f32_16x16x32_bf16 v[72:75], v[154:157], v[228:231], v[72:75]
	s_setprio 0
	s_add_i32 s68, s68, s42
	s_mov_b64 s[24:25], 0x180
	s_add_i32 s69, s68, 0x2000
	v_lshl_add_u64 v[162:163], v[164:165], 0, s[24:25]
	s_mov_b32 m0, s68
	s_add_u32 s40, s30, 0x40180
	ds_read_b128 v[182:185], v223 offset:49152
	ds_read_b128 v[200:203], v223 offset:50176
	ds_read_b128 v[204:207], v223 offset:51200
	ds_read_b128 v[208:211], v223 offset:52224
	ds_read_b128 v[212:215], v223 offset:53248
	ds_read_b128 v[216:219], v223 offset:54272
	ds_read_b128 v[224:227], v223 offset:55296
	ds_read_b128 v[228:231], v223 offset:56320
	global_load_lds_dwordx4 v[162:163], off
	v_lshl_add_u64 v[162:163], v[166:167], 0, s[24:25]
	s_mov_b32 m0, s69
	s_addc_u32 s41, s31, 0
	s_add_i32 s70, s70, s42
	global_load_lds_dwordx4 v[162:163], off
	v_lshl_add_u64 v[162:163], s[40:41], 0, v[34:35]
	s_mov_b32 m0, s70
	s_add_i32 s71, s70, 0x2000
	global_load_lds_dwordx4 v[162:163], off
	v_lshl_add_u64 v[162:163], s[40:41], 0, v[190:191]
	s_mov_b32 m0, s71
	s_nop 0
	global_load_lds_dwordx4 v[162:163], off
	v_lshl_add_u64 v[162:163], v[168:169], 0, s[24:25]
	s_mov_b32 m0, s51
	s_nop 0
	global_load_lds_dwordx4 v[162:163], off
	v_lshl_add_u64 v[162:163], v[170:171], 0, s[24:25]
	s_mov_b32 m0, s52
	s_nop 0
	global_load_lds_dwordx4 v[162:163], off
	s_waitcnt vmcnt(8)
	s_waitcnt lgkmcnt(0)
	s_barrier
	s_setprio 1
	s_waitcnt lgkmcnt(0)
	v_mfma_f32_16x16x32_bf16 v[64:67], v[134:137], v[182:185], v[64:67]
	v_mfma_f32_16x16x32_bf16 v[60:63], v[142:145], v[182:185], v[60:63]
	v_mfma_f32_16x16x32_bf16 v[52:55], v[142:145], v[204:207], v[52:55]
	v_mfma_f32_16x16x32_bf16 v[56:59], v[134:137], v[204:207], v[56:59]
	v_mfma_f32_16x16x32_bf16 v[48:51], v[134:137], v[212:215], v[48:51]
	v_mfma_f32_16x16x32_bf16 v[44:47], v[142:145], v[212:215], v[44:47]
	v_mfma_f32_16x16x32_bf16 v[36:39], v[142:145], v[224:227], v[36:39]
	v_mfma_f32_16x16x32_bf16 v[40:43], v[134:137], v[224:227], v[40:43]
	v_mfma_f32_16x16x32_bf16 v[64:67], v[138:141], v[200:203], v[64:67]
	v_mfma_f32_16x16x32_bf16 v[60:63], v[146:149], v[200:203], v[60:63]
	v_mfma_f32_16x16x32_bf16 v[52:55], v[146:149], v[208:211], v[52:55]
	v_mfma_f32_16x16x32_bf16 v[56:59], v[138:141], v[208:211], v[56:59]
	v_mfma_f32_16x16x32_bf16 v[48:51], v[138:141], v[216:219], v[48:51]
	v_mfma_f32_16x16x32_bf16 v[44:47], v[146:149], v[216:219], v[44:47]
	v_mfma_f32_16x16x32_bf16 v[36:39], v[146:149], v[228:231], v[36:39]
	v_mfma_f32_16x16x32_bf16 v[40:43], v[138:141], v[228:231], v[40:43]
	s_setprio 0
	s_setprio 1
	v_mfma_f32_16x16x32_bf16 v[30:33], v[150:153], v[182:185], v[30:33]
	v_mfma_f32_16x16x32_bf16 v[26:29], v[158:161], v[182:185], v[26:29]
	v_mfma_f32_16x16x32_bf16 v[18:21], v[158:161], v[204:207], v[18:21]
	v_mfma_f32_16x16x32_bf16 v[22:25], v[150:153], v[204:207], v[22:25]
	v_mfma_f32_16x16x32_bf16 v[14:17], v[150:153], v[212:215], v[14:17]
	v_mfma_f32_16x16x32_bf16 v[10:13], v[158:161], v[212:215], v[10:13]
	v_mfma_f32_16x16x32_bf16 v[2:5], v[158:161], v[224:227], v[2:5]
	v_mfma_f32_16x16x32_bf16 v[6:9], v[150:153], v[224:227], v[6:9]
	v_mfma_f32_16x16x32_bf16 v[30:33], v[154:157], v[200:203], v[30:33]
	v_mfma_f32_16x16x32_bf16 v[26:29], v[178:181], v[200:203], v[26:29]
	v_mfma_f32_16x16x32_bf16 v[18:21], v[178:181], v[208:211], v[18:21]
	v_mfma_f32_16x16x32_bf16 v[22:25], v[154:157], v[208:211], v[22:25]
	v_mfma_f32_16x16x32_bf16 v[14:17], v[154:157], v[216:219], v[14:17]
	v_mfma_f32_16x16x32_bf16 v[10:13], v[178:181], v[216:219], v[10:13]
	s_barrier
	s_setprio 3
	v_mfma_f32_16x16x32_bf16 v[2:5], v[178:181], v[228:231], v[2:5]
	v_mfma_f32_16x16x32_bf16 v[6:9], v[154:157], v[228:231], v[6:9]
	s_setprio 0
	s_add_u32 s36, s36, 0x40180
	s_addc_u32 s37, s37, 0
	s_add_u32 s72, s30, 0x200
	s_addc_u32 s73, s31, 0
	s_mov_b32 s74, 0
.LBB0_541:
	ds_read_b128 v[134:137], v172
	ds_read_b128 v[138:141], v172 offset:1024
	ds_read_b128 v[142:145], v172 offset:2048
	ds_read_b128 v[146:149], v172 offset:3072
	ds_read_b128 v[150:153], v173
	ds_read_b128 v[154:157], v173 offset:1024
	ds_read_b128 v[158:161], v173 offset:2048
	ds_read_b128 v[162:165], v173 offset:3072
	s_add_u32 s14, s36, 0xfffc0080
	s_addc_u32 s30, s37, -1
	s_cmp_eq_u32 s74, 12
	s_cselect_b32 s41, s58, s30
	s_cselect_b32 s40, s59, s14
	s_cselect_b32 s31, s60, s73
	s_cselect_b32 s30, s61, s72
	s_mov_b32 m0, s62
	v_lshl_add_u64 v[170:171], s[36:37], 0, v[196:197]
	ds_read_b128 v[166:169], v223
	ds_read_b128 v[178:181], v223 offset:1024
	ds_read_b128 v[182:185], v223 offset:2048
	ds_read_b128 v[200:203], v223 offset:3072
	ds_read_b128 v[204:207], v223 offset:4096
	ds_read_b128 v[208:211], v223 offset:5120
	ds_read_b128 v[212:215], v223 offset:6144
	ds_read_b128 v[216:219], v223 offset:7168
	global_load_lds_dwordx4 v[170:171], off
	v_lshl_add_u64 v[170:171], s[36:37], 0, v[198:199]
	s_mov_b32 m0, s63
	s_nop 0
	global_load_lds_dwordx4 v[170:171], off
	s_waitcnt vmcnt(8)
	s_waitcnt lgkmcnt(0)
	s_barrier
	s_setprio 1
	s_waitcnt lgkmcnt(0)
	v_mfma_f32_16x16x32_bf16 v[128:131], v[134:137], v[166:169], v[128:131]
	v_mfma_f32_16x16x32_bf16 v[124:127], v[142:145], v[166:169], v[124:127]
	v_mfma_f32_16x16x32_bf16 v[116:119], v[142:145], v[182:185], v[116:119]
	v_mfma_f32_16x16x32_bf16 v[120:123], v[134:137], v[182:185], v[120:123]
	v_mfma_f32_16x16x32_bf16 v[112:115], v[134:137], v[204:207], v[112:115]
	v_mfma_f32_16x16x32_bf16 v[108:111], v[142:145], v[204:207], v[108:111]
	v_mfma_f32_16x16x32_bf16 v[100:103], v[142:145], v[212:215], v[100:103]
	v_mfma_f32_16x16x32_bf16 v[104:107], v[134:137], v[212:215], v[104:107]
	v_mfma_f32_16x16x32_bf16 v[128:131], v[138:141], v[178:181], v[128:131]
	v_mfma_f32_16x16x32_bf16 v[124:127], v[146:149], v[178:181], v[124:127]
	v_mfma_f32_16x16x32_bf16 v[116:119], v[146:149], v[200:203], v[116:119]
	v_mfma_f32_16x16x32_bf16 v[120:123], v[138:141], v[200:203], v[120:123]
	v_mfma_f32_16x16x32_bf16 v[112:115], v[138:141], v[208:211], v[112:115]
	v_mfma_f32_16x16x32_bf16 v[108:111], v[146:149], v[208:211], v[108:111]
	v_mfma_f32_16x16x32_bf16 v[100:103], v[146:149], v[216:219], v[100:103]
	v_mfma_f32_16x16x32_bf16 v[104:107], v[138:141], v[216:219], v[104:107]
	s_setprio 0
	s_setprio 1
	v_mfma_f32_16x16x32_bf16 v[96:99], v[150:153], v[166:169], v[96:99]
	v_mfma_f32_16x16x32_bf16 v[92:95], v[158:161], v[166:169], v[92:95]
	v_mfma_f32_16x16x32_bf16 v[84:87], v[158:161], v[182:185], v[84:87]
	v_mfma_f32_16x16x32_bf16 v[88:91], v[150:153], v[182:185], v[88:91]
	v_mfma_f32_16x16x32_bf16 v[80:83], v[150:153], v[204:207], v[80:83]
	v_mfma_f32_16x16x32_bf16 v[76:79], v[158:161], v[204:207], v[76:79]
	v_mfma_f32_16x16x32_bf16 v[68:71], v[158:161], v[212:215], v[68:71]
	v_mfma_f32_16x16x32_bf16 v[72:75], v[150:153], v[212:215], v[72:75]
	v_mfma_f32_16x16x32_bf16 v[96:99], v[154:157], v[178:181], v[96:99]
	v_mfma_f32_16x16x32_bf16 v[92:95], v[162:165], v[178:181], v[92:95]
	v_mfma_f32_16x16x32_bf16 v[84:87], v[162:165], v[200:203], v[84:87]
	v_mfma_f32_16x16x32_bf16 v[88:91], v[154:157], v[200:203], v[88:91]
	v_mfma_f32_16x16x32_bf16 v[80:83], v[154:157], v[208:211], v[80:83]
	v_mfma_f32_16x16x32_bf16 v[76:79], v[162:165], v[208:211], v[76:79]
	s_barrier
	s_setprio 3
	v_mfma_f32_16x16x32_bf16 v[68:71], v[162:165], v[216:219], v[68:71]
	v_mfma_f32_16x16x32_bf16 v[72:75], v[154:157], v[216:219], v[72:75]
	s_setprio 0
	s_mov_b32 m0, s64
	v_lshl_add_u64 v[170:171], s[30:31], 0, v[34:35]
	s_add_u32 s76, s30, 0x40000
	ds_read_b128 v[166:169], v223 offset:16384
	ds_read_b128 v[178:181], v223 offset:17408
	ds_read_b128 v[182:185], v223 offset:18432
	ds_read_b128 v[200:203], v223 offset:19456
	ds_read_b128 v[204:207], v223 offset:20480
	ds_read_b128 v[208:211], v223 offset:21504
	ds_read_b128 v[212:215], v223 offset:22528
	ds_read_b128 v[216:219], v223 offset:23552
	global_load_lds_dwordx4 v[170:171], off
	v_lshl_add_u64 v[174:175], s[30:31], 0, v[190:191]
	s_mov_b32 m0, s65
	s_addc_u32 s77, s31, 0
	global_load_lds_dwordx4 v[174:175], off
	v_lshl_add_u64 v[224:225], s[76:77], 0, v[34:35]
	s_mov_b32 m0, s66
	v_lshl_add_u64 v[226:227], s[40:41], 0, v[192:193]
	global_load_lds_dwordx4 v[224:225], off
	v_lshl_add_u64 v[224:225], s[76:77], 0, v[190:191]
	s_mov_b32 m0, s67
	s_nop 0
	global_load_lds_dwordx4 v[224:225], off
	v_lshl_add_u64 v[224:225], s[40:41], 0, v[194:195]
	s_mov_b32 m0, s43
	s_nop 0
	global_load_lds_dwordx4 v[224:225], off
	s_mov_b32 m0, s44
	s_nop 0
	global_load_lds_dwordx4 v[226:227], off
	s_waitcnt vmcnt(8)
	s_waitcnt lgkmcnt(0)
	s_barrier
	s_setprio 1
	s_waitcnt lgkmcnt(0)
	v_mfma_f32_16x16x32_bf16 v[64:67], v[134:137], v[166:169], v[64:67]
	v_mfma_f32_16x16x32_bf16 v[60:63], v[142:145], v[166:169], v[60:63]
	v_mfma_f32_16x16x32_bf16 v[52:55], v[142:145], v[182:185], v[52:55]
	v_mfma_f32_16x16x32_bf16 v[56:59], v[134:137], v[182:185], v[56:59]
	v_mfma_f32_16x16x32_bf16 v[48:51], v[134:137], v[204:207], v[48:51]
	v_mfma_f32_16x16x32_bf16 v[44:47], v[142:145], v[204:207], v[44:47]
	v_mfma_f32_16x16x32_bf16 v[36:39], v[142:145], v[212:215], v[36:39]
	v_mfma_f32_16x16x32_bf16 v[40:43], v[134:137], v[212:215], v[40:43]
	v_mfma_f32_16x16x32_bf16 v[64:67], v[138:141], v[178:181], v[64:67]
	v_mfma_f32_16x16x32_bf16 v[60:63], v[146:149], v[178:181], v[60:63]
	v_mfma_f32_16x16x32_bf16 v[52:55], v[146:149], v[200:203], v[52:55]
	v_mfma_f32_16x16x32_bf16 v[56:59], v[138:141], v[200:203], v[56:59]
	v_mfma_f32_16x16x32_bf16 v[48:51], v[138:141], v[208:211], v[48:51]
	v_mfma_f32_16x16x32_bf16 v[44:47], v[146:149], v[208:211], v[44:47]
	v_mfma_f32_16x16x32_bf16 v[36:39], v[146:149], v[216:219], v[36:39]
	v_mfma_f32_16x16x32_bf16 v[40:43], v[138:141], v[216:219], v[40:43]
	s_setprio 0
	s_setprio 1
	v_mfma_f32_16x16x32_bf16 v[30:33], v[150:153], v[166:169], v[30:33]
	v_mfma_f32_16x16x32_bf16 v[26:29], v[158:161], v[166:169], v[26:29]
	v_mfma_f32_16x16x32_bf16 v[18:21], v[158:161], v[182:185], v[18:21]
	v_mfma_f32_16x16x32_bf16 v[22:25], v[150:153], v[182:185], v[22:25]
	v_mfma_f32_16x16x32_bf16 v[14:17], v[150:153], v[204:207], v[14:17]
	v_mfma_f32_16x16x32_bf16 v[10:13], v[158:161], v[204:207], v[10:13]
	v_mfma_f32_16x16x32_bf16 v[2:5], v[158:161], v[212:215], v[2:5]
	v_mfma_f32_16x16x32_bf16 v[6:9], v[150:153], v[212:215], v[6:9]
	v_mfma_f32_16x16x32_bf16 v[30:33], v[154:157], v[178:181], v[30:33]
	v_mfma_f32_16x16x32_bf16 v[26:29], v[162:165], v[178:181], v[26:29]
	v_mfma_f32_16x16x32_bf16 v[18:21], v[162:165], v[200:203], v[18:21]
	v_mfma_f32_16x16x32_bf16 v[22:25], v[154:157], v[200:203], v[22:25]
	v_mfma_f32_16x16x32_bf16 v[14:17], v[154:157], v[208:211], v[14:17]
	v_mfma_f32_16x16x32_bf16 v[10:13], v[162:165], v[208:211], v[10:13]
	s_barrier
	s_setprio 3
	v_mfma_f32_16x16x32_bf16 v[2:5], v[162:165], v[216:219], v[2:5]
	v_mfma_f32_16x16x32_bf16 v[6:9], v[154:157], v[216:219], v[6:9]
	s_setprio 0
	ds_read_b128 v[134:137], v132
	ds_read_b128 v[138:141], v132 offset:1024
	ds_read_b128 v[142:145], v132 offset:2048
	ds_read_b128 v[146:149], v132 offset:3072
	ds_read_b128 v[150:153], v133
	ds_read_b128 v[154:157], v133 offset:1024
	ds_read_b128 v[158:161], v133 offset:2048
	ds_read_b128 v[162:165], v133 offset:3072
	s_add_u32 s40, s40, 0x40000
	s_addc_u32 s41, s41, 0
	s_mov_b32 m0, s45
	v_lshl_add_u64 v[228:229], s[40:41], 0, v[194:195]
	ds_read_b128 v[166:169], v223 offset:32768
	ds_read_b128 v[178:181], v223 offset:33792
	ds_read_b128 v[182:185], v223 offset:34816
	ds_read_b128 v[200:203], v223 offset:35840
	ds_read_b128 v[204:207], v223 offset:36864
	ds_read_b128 v[208:211], v223 offset:37888
	ds_read_b128 v[212:215], v223 offset:38912
	ds_read_b128 v[216:219], v223 offset:39936
	global_load_lds_dwordx4 v[228:229], off
	v_lshl_add_u64 v[228:229], s[40:41], 0, v[192:193]
	s_mov_b32 m0, s46
	s_nop 0
	global_load_lds_dwordx4 v[228:229], off
	s_waitcnt vmcnt(8)
	s_waitcnt lgkmcnt(0)
	s_barrier
	s_setprio 1
	s_waitcnt lgkmcnt(0)
	v_mfma_f32_16x16x32_bf16 v[128:131], v[134:137], v[166:169], v[128:131]
	v_mfma_f32_16x16x32_bf16 v[124:127], v[142:145], v[166:169], v[124:127]
	v_mfma_f32_16x16x32_bf16 v[116:119], v[142:145], v[182:185], v[116:119]
	v_mfma_f32_16x16x32_bf16 v[120:123], v[134:137], v[182:185], v[120:123]
	v_mfma_f32_16x16x32_bf16 v[112:115], v[134:137], v[204:207], v[112:115]
	v_mfma_f32_16x16x32_bf16 v[108:111], v[142:145], v[204:207], v[108:111]
	v_mfma_f32_16x16x32_bf16 v[100:103], v[142:145], v[212:215], v[100:103]
	v_mfma_f32_16x16x32_bf16 v[104:107], v[134:137], v[212:215], v[104:107]
	v_mfma_f32_16x16x32_bf16 v[128:131], v[138:141], v[178:181], v[128:131]
	v_mfma_f32_16x16x32_bf16 v[124:127], v[146:149], v[178:181], v[124:127]
	v_mfma_f32_16x16x32_bf16 v[116:119], v[146:149], v[200:203], v[116:119]
	v_mfma_f32_16x16x32_bf16 v[120:123], v[138:141], v[200:203], v[120:123]
	v_mfma_f32_16x16x32_bf16 v[112:115], v[138:141], v[208:211], v[112:115]
	v_mfma_f32_16x16x32_bf16 v[108:111], v[146:149], v[208:211], v[108:111]
	v_mfma_f32_16x16x32_bf16 v[100:103], v[146:149], v[216:219], v[100:103]
	v_mfma_f32_16x16x32_bf16 v[104:107], v[138:141], v[216:219], v[104:107]
	s_setprio 0
	s_setprio 1
	v_mfma_f32_16x16x32_bf16 v[96:99], v[150:153], v[166:169], v[96:99]
	v_mfma_f32_16x16x32_bf16 v[92:95], v[158:161], v[166:169], v[92:95]
	v_mfma_f32_16x16x32_bf16 v[84:87], v[158:161], v[182:185], v[84:87]
	v_mfma_f32_16x16x32_bf16 v[88:91], v[150:153], v[182:185], v[88:91]
	v_mfma_f32_16x16x32_bf16 v[80:83], v[150:153], v[204:207], v[80:83]
	v_mfma_f32_16x16x32_bf16 v[76:79], v[158:161], v[204:207], v[76:79]
	v_mfma_f32_16x16x32_bf16 v[68:71], v[158:161], v[212:215], v[68:71]
	v_mfma_f32_16x16x32_bf16 v[72:75], v[150:153], v[212:215], v[72:75]
	v_mfma_f32_16x16x32_bf16 v[96:99], v[154:157], v[178:181], v[96:99]
	v_mfma_f32_16x16x32_bf16 v[92:95], v[162:165], v[178:181], v[92:95]
	v_mfma_f32_16x16x32_bf16 v[84:87], v[162:165], v[200:203], v[84:87]
	v_mfma_f32_16x16x32_bf16 v[88:91], v[154:157], v[200:203], v[88:91]
	v_mfma_f32_16x16x32_bf16 v[80:83], v[154:157], v[208:211], v[80:83]
	v_mfma_f32_16x16x32_bf16 v[76:79], v[162:165], v[208:211], v[76:79]
	s_barrier
	s_setprio 3
	v_mfma_f32_16x16x32_bf16 v[68:71], v[162:165], v[216:219], v[68:71]
	v_mfma_f32_16x16x32_bf16 v[72:75], v[154:157], v[216:219], v[72:75]
	s_setprio 0
	s_mov_b32 m0, s68
	v_lshl_add_u64 v[170:171], v[170:171], 0, s[18:19]
	s_add_u32 s30, s30, 0x40080
	ds_read_b128 v[166:169], v223 offset:49152
	ds_read_b128 v[178:181], v223 offset:50176
	ds_read_b128 v[182:185], v223 offset:51200
	ds_read_b128 v[200:203], v223 offset:52224
	ds_read_b128 v[204:207], v223 offset:53248
	ds_read_b128 v[208:211], v223 offset:54272
	ds_read_b128 v[212:215], v223 offset:55296
	ds_read_b128 v[216:219], v223 offset:56320
	global_load_lds_dwordx4 v[170:171], off
	v_lshl_add_u64 v[170:171], v[174:175], 0, s[18:19]
	s_mov_b32 m0, s69
	s_addc_u32 s31, s31, 0
	global_load_lds_dwordx4 v[170:171], off
	v_lshl_add_u64 v[170:171], s[30:31], 0, v[34:35]
	s_mov_b32 m0, s70
	s_nop 0
	global_load_lds_dwordx4 v[170:171], off
	v_lshl_add_u64 v[170:171], s[30:31], 0, v[190:191]
	s_mov_b32 m0, s71
	s_nop 0
	global_load_lds_dwordx4 v[170:171], off
	v_lshl_add_u64 v[170:171], v[224:225], 0, s[18:19]
	s_mov_b32 m0, s51
	s_nop 0
	global_load_lds_dwordx4 v[170:171], off
	v_lshl_add_u64 v[170:171], v[226:227], 0, s[18:19]
	s_mov_b32 m0, s52
	s_nop 0
	global_load_lds_dwordx4 v[170:171], off
	s_waitcnt vmcnt(8)
	s_waitcnt lgkmcnt(0)
	s_barrier
	s_setprio 1
	s_waitcnt lgkmcnt(0)
	v_mfma_f32_16x16x32_bf16 v[64:67], v[134:137], v[166:169], v[64:67]
	v_mfma_f32_16x16x32_bf16 v[60:63], v[142:145], v[166:169], v[60:63]
	v_mfma_f32_16x16x32_bf16 v[52:55], v[142:145], v[182:185], v[52:55]
	v_mfma_f32_16x16x32_bf16 v[56:59], v[134:137], v[182:185], v[56:59]
	v_mfma_f32_16x16x32_bf16 v[48:51], v[134:137], v[204:207], v[48:51]
	v_mfma_f32_16x16x32_bf16 v[44:47], v[142:145], v[204:207], v[44:47]
	v_mfma_f32_16x16x32_bf16 v[36:39], v[142:145], v[212:215], v[36:39]
	v_mfma_f32_16x16x32_bf16 v[40:43], v[134:137], v[212:215], v[40:43]
	v_mfma_f32_16x16x32_bf16 v[64:67], v[138:141], v[178:181], v[64:67]
	v_mfma_f32_16x16x32_bf16 v[60:63], v[146:149], v[178:181], v[60:63]
	v_mfma_f32_16x16x32_bf16 v[52:55], v[146:149], v[200:203], v[52:55]
	v_mfma_f32_16x16x32_bf16 v[56:59], v[138:141], v[200:203], v[56:59]
	v_mfma_f32_16x16x32_bf16 v[48:51], v[138:141], v[208:211], v[48:51]
	v_mfma_f32_16x16x32_bf16 v[44:47], v[146:149], v[208:211], v[44:47]
	v_mfma_f32_16x16x32_bf16 v[36:39], v[146:149], v[216:219], v[36:39]
	v_mfma_f32_16x16x32_bf16 v[40:43], v[138:141], v[216:219], v[40:43]
	s_setprio 0
	s_setprio 1
	v_mfma_f32_16x16x32_bf16 v[30:33], v[150:153], v[166:169], v[30:33]
	v_mfma_f32_16x16x32_bf16 v[26:29], v[158:161], v[166:169], v[26:29]
	v_mfma_f32_16x16x32_bf16 v[18:21], v[158:161], v[182:185], v[18:21]
	v_mfma_f32_16x16x32_bf16 v[22:25], v[150:153], v[182:185], v[22:25]
	v_mfma_f32_16x16x32_bf16 v[14:17], v[150:153], v[204:207], v[14:17]
	v_mfma_f32_16x16x32_bf16 v[10:13], v[158:161], v[204:207], v[10:13]
	v_mfma_f32_16x16x32_bf16 v[2:5], v[158:161], v[212:215], v[2:5]
	v_mfma_f32_16x16x32_bf16 v[6:9], v[150:153], v[212:215], v[6:9]
	v_mfma_f32_16x16x32_bf16 v[30:33], v[154:157], v[178:181], v[30:33]
	v_mfma_f32_16x16x32_bf16 v[26:29], v[162:165], v[178:181], v[26:29]
	v_mfma_f32_16x16x32_bf16 v[18:21], v[162:165], v[200:203], v[18:21]
	v_mfma_f32_16x16x32_bf16 v[22:25], v[154:157], v[200:203], v[22:25]
	v_mfma_f32_16x16x32_bf16 v[14:17], v[154:157], v[208:211], v[14:17]
	v_mfma_f32_16x16x32_bf16 v[10:13], v[162:165], v[208:211], v[10:13]
	s_barrier
	s_setprio 3
	v_mfma_f32_16x16x32_bf16 v[2:5], v[162:165], v[216:219], v[2:5]
	v_mfma_f32_16x16x32_bf16 v[6:9], v[154:157], v[216:219], v[6:9]
	s_setprio 0
	s_add_i32 s74, s74, 2
	s_add_u32 s36, s36, 0x100
	s_addc_u32 s37, s37, 0
	s_add_u32 s72, s72, 0x100
	s_addc_u32 s73, s73, 0
	s_cmp_gt_u32 s74, 13
	s_cbranch_scc0 .LBB0_541
	v_readlane_b32 s74, v255, 3
	s_and_b64 vcc, exec, s[10:11]
	v_readlane_b32 s75, v255, 4
	s_mov_b32 s58, 0x19b00000
	v_readlane_b32 s59, v255, 10
	s_mov_b32 s60, 0xff61b1e6
	s_mov_b64 s[62:63], 0x800
	s_mov_b32 s64, 0x3b000000
	s_cbranch_vccz .LBB0_544
	s_barrier

.LBB0_819:
	s_add_u32 s81, s30, 0x200
	s_addc_u32 s82, s31, 0
	s_add_i32 s55, 0, 0x14000
	s_add_i32 s52, 0, 0x10000
	v_add_u32_e32 v199, s55, v167
	v_add_u32_e32 v200, s52, v167
	ds_read_b128 v[10:13], v199
	ds_read_b128 v[14:17], v199 offset:1024
	ds_read_b128 v[2:5], v199 offset:2048
	ds_read_b128 v[6:9], v199 offset:3072
	ds_read_b128 v[22:25], v200 offset:3072
	ds_read_b128 v[18:21], v200 offset:2048
	ds_read_b128 v[30:33], v200 offset:1024
	ds_read_b128 v[26:29], v200
	s_lshl_b32 s14, s80, 10
	s_add_i32 s83, s14, 0
	s_add_i32 s83, s83, 0x20400
	v_mov_b32_e32 v191, v35
	v_mov_b32_e32 v175, v35
	s_add_i32 s84, s69, 0xc000
	v_readlane_b32 s26, v253, 28
	s_mov_b32 m0, s84
	v_readlane_b32 s27, v253, 29
	s_add_i32 s53, s69, 0xe000
	ds_read_b128 v[202:205], v169
	ds_read_b128 v[206:209], v169 offset:1024
	ds_read_b128 v[222:225], v169 offset:2048
	ds_read_b128 v[226:229], v169 offset:3072
	ds_read_b128 v[230:233], v169 offset:4096
	ds_read_b128 v[234:237], v169 offset:5120
	ds_read_b128 v[238:241], v169 offset:6144
	ds_read_b128 v[242:245], v169 offset:7168
	global_load_lds_dwordx4 v190, s[26:27]
	s_mov_b32 m0, s53
	s_nop 0
	global_load_lds_dwordx4 v174, s[26:27]
	s_waitcnt vmcnt(8)
	s_waitcnt lgkmcnt(0)
	s_barrier
	s_setprio 1
	s_waitcnt lgkmcnt(0)
	v_mfma_f32_16x16x128_f8f6f4 v[160:163], v[26:33], v[202:209], 0
	v_mfma_f32_16x16x128_f8f6f4 v[156:159], v[18:25], v[202:209], 0
	v_mfma_f32_16x16x128_f8f6f4 v[148:151], v[18:25], v[222:229], 0
	v_mfma_f32_16x16x128_f8f6f4 v[152:155], v[26:33], v[222:229], 0
	v_mfma_f32_16x16x128_f8f6f4 v[144:147], v[26:33], v[230:237], 0
	v_mfma_f32_16x16x128_f8f6f4 v[140:143], v[18:25], v[230:237], 0
	v_mfma_f32_16x16x128_f8f6f4 v[132:135], v[18:25], v[238:245], 0
	v_mfma_f32_16x16x128_f8f6f4 v[136:139], v[26:33], v[238:245], 0
	s_setprio 0
	s_setprio 1
	v_mfma_f32_16x16x128_f8f6f4 v[128:131], v[10:17], v[202:209], 0
	v_mfma_f32_16x16x128_f8f6f4 v[124:127], v[2:9], v[202:209], 0
	v_mfma_f32_16x16x128_f8f6f4 v[116:119], v[2:9], v[222:229], 0
	v_mfma_f32_16x16x128_f8f6f4 v[120:123], v[10:17], v[222:229], 0
	v_mfma_f32_16x16x128_f8f6f4 v[112:115], v[10:17], v[230:237], 0
	v_mfma_f32_16x16x128_f8f6f4 v[108:111], v[2:9], v[230:237], 0
	v_mfma_f32_16x16x128_f8f6f4 v[100:103], v[2:9], v[238:245], 0
	s_barrier
	s_setprio 3
	v_mfma_f32_16x16x128_f8f6f4 v[104:107], v[10:17], v[238:245], 0
	s_setprio 0
	s_add_i32 s52, s52, s68
	v_lshl_add_u64 v[194:195], s[30:31], 0, v[170:171]
	s_add_i32 s85, s52, 0x2000
	v_lshl_add_u64 v[178:179], v[194:195], 0, s[28:29]
	s_mov_b32 m0, s52
	v_lshl_add_u64 v[196:197], s[30:31], 0, v[172:173]
	s_add_u32 s36, s30, 0x20100
	ds_read_b128 v[202:205], v169 offset:16384
	ds_read_b128 v[206:209], v169 offset:17408
	ds_read_b128 v[222:225], v169 offset:18432
	ds_read_b128 v[226:229], v169 offset:19456
	ds_read_b128 v[230:233], v169 offset:20480
	ds_read_b128 v[234:237], v169 offset:21504
	ds_read_b128 v[238:241], v169 offset:22528
	ds_read_b128 v[242:245], v169 offset:23552
	global_load_lds_dwordx4 v[178:179], off
	v_lshl_add_u64 v[178:179], v[196:197], 0, s[28:29]
	s_mov_b32 m0, s85
	s_addc_u32 s37, s31, 0
	s_add_i32 s55, s55, s68
	global_load_lds_dwordx4 v[178:179], off
	v_lshl_add_u64 v[178:179], s[36:37], 0, v[170:171]
	s_mov_b32 m0, s55
	s_add_i32 s65, s55, 0x2000
	global_load_lds_dwordx4 v[178:179], off
	v_lshl_add_u64 v[178:179], s[36:37], 0, v[172:173]
	s_mov_b32 m0, s65
	v_readlane_b32 s26, v253, 37
	global_load_lds_dwordx4 v[178:179], off
	s_mov_b32 m0, s69
	v_readlane_b32 s27, v253, 38
	s_nop 4
	global_load_lds_dwordx4 v34, s[26:27]
	s_mov_b32 m0, s70
	s_nop 0
	global_load_lds_dwordx4 v192, s[26:27]
	s_waitcnt vmcnt(8)
	s_waitcnt lgkmcnt(0)
	s_barrier
	s_setprio 1
	s_waitcnt lgkmcnt(0)
	v_mfma_f32_16x16x128_f8f6f4 v[96:99], v[26:33], v[202:209], 0
	v_mfma_f32_16x16x128_f8f6f4 v[92:95], v[18:25], v[202:209], 0
	v_mfma_f32_16x16x128_f8f6f4 v[84:87], v[18:25], v[222:229], 0
	v_mfma_f32_16x16x128_f8f6f4 v[88:91], v[26:33], v[222:229], 0
	v_mfma_f32_16x16x128_f8f6f4 v[80:83], v[26:33], v[230:237], 0
	v_mfma_f32_16x16x128_f8f6f4 v[76:79], v[18:25], v[230:237], 0
	v_mfma_f32_16x16x128_f8f6f4 v[68:71], v[18:25], v[238:245], 0
	v_mfma_f32_16x16x128_f8f6f4 v[72:75], v[26:33], v[238:245], 0
	s_setprio 0
	s_setprio 1
	v_mfma_f32_16x16x128_f8f6f4 v[64:67], v[10:17], v[202:209], 0
	v_mfma_f32_16x16x128_f8f6f4 v[60:63], v[2:9], v[202:209], 0
	v_mfma_f32_16x16x128_f8f6f4 v[52:55], v[2:9], v[222:229], 0
	v_mfma_f32_16x16x128_f8f6f4 v[56:59], v[10:17], v[222:229], 0
	v_mfma_f32_16x16x128_f8f6f4 v[48:51], v[10:17], v[230:237], 0
	v_mfma_f32_16x16x128_f8f6f4 v[44:47], v[2:9], v[230:237], 0
	v_mfma_f32_16x16x128_f8f6f4 v[36:39], v[2:9], v[238:245], 0
	s_barrier
	s_setprio 3
	v_mfma_f32_16x16x128_f8f6f4 v[40:43], v[10:17], v[238:245], 0
	s_setprio 0
	s_add_i32 s54, 0, 0x18000
	s_add_i32 s51, 0, 0x1c000
	v_add_u32_e32 v201, s54, v167
	v_add_u32_e32 v202, s51, v167
	ds_read_b128 v[26:29], v201
	ds_read_b128 v[30:33], v201 offset:1024
	ds_read_b128 v[18:21], v201 offset:2048
	ds_read_b128 v[22:25], v201 offset:3072
	ds_read_b128 v[10:13], v202
	ds_read_b128 v[14:17], v202 offset:1024
	ds_read_b128 v[2:5], v202 offset:2048
	ds_read_b128 v[6:9], v202 offset:3072
	s_mov_b32 m0, s71
	ds_read_b128 v[204:207], v169 offset:32768
	ds_read_b128 v[208:211], v169 offset:33792
	ds_read_b128 v[222:225], v169 offset:34816
	ds_read_b128 v[226:229], v169 offset:35840
	ds_read_b128 v[230:233], v169 offset:36864
	ds_read_b128 v[234:237], v169 offset:37888
	ds_read_b128 v[238:241], v169 offset:38912
	ds_read_b128 v[242:245], v169 offset:39936
	global_load_lds_dwordx4 v189, s[26:27]
	s_mov_b32 m0, s72
	s_nop 0
	global_load_lds_dwordx4 v198, s[26:27]
	s_waitcnt vmcnt(8)
	s_waitcnt lgkmcnt(0)
	s_barrier
	s_setprio 1
	s_waitcnt lgkmcnt(0)
	v_mfma_f32_16x16x128_f8f6f4 v[160:163], v[26:33], v[204:211], v[160:163]
	v_mfma_f32_16x16x128_f8f6f4 v[156:159], v[18:25], v[204:211], v[156:159]
	v_mfma_f32_16x16x128_f8f6f4 v[148:151], v[18:25], v[222:229], v[148:151]
	v_mfma_f32_16x16x128_f8f6f4 v[152:155], v[26:33], v[222:229], v[152:155]
	v_mfma_f32_16x16x128_f8f6f4 v[144:147], v[26:33], v[230:237], v[144:147]
	v_mfma_f32_16x16x128_f8f6f4 v[140:143], v[18:25], v[230:237], v[140:143]
	v_mfma_f32_16x16x128_f8f6f4 v[132:135], v[18:25], v[238:245], v[132:135]
	v_mfma_f32_16x16x128_f8f6f4 v[136:139], v[26:33], v[238:245], v[136:139]
	s_setprio 0
	s_setprio 1
	v_mfma_f32_16x16x128_f8f6f4 v[128:131], v[10:17], v[204:211], v[128:131]
	v_mfma_f32_16x16x128_f8f6f4 v[124:127], v[2:9], v[204:211], v[124:127]
	v_mfma_f32_16x16x128_f8f6f4 v[116:119], v[2:9], v[222:229], v[116:119]
	v_mfma_f32_16x16x128_f8f6f4 v[120:123], v[10:17], v[222:229], v[120:123]
	v_mfma_f32_16x16x128_f8f6f4 v[112:115], v[10:17], v[230:237], v[112:115]
	v_mfma_f32_16x16x128_f8f6f4 v[108:111], v[2:9], v[230:237], v[108:111]
	v_mfma_f32_16x16x128_f8f6f4 v[100:103], v[2:9], v[238:245], v[100:103]
	s_barrier
	s_setprio 3
	v_mfma_f32_16x16x128_f8f6f4 v[104:107], v[10:17], v[238:245], v[104:107]
	s_setprio 0
	s_add_i32 s54, s54, s68
	s_mov_b64 s[26:27], 0x180
	s_add_i32 s50, s54, 0x2000
	v_lshl_add_u64 v[178:179], v[194:195], 0, s[26:27]
	s_mov_b32 m0, s54
	s_add_u32 s30, s30, 0x20180
	ds_read_b128 v[204:207], v169 offset:49152
	ds_read_b128 v[208:211], v169 offset:50176
	ds_read_b128 v[222:225], v169 offset:51200
	ds_read_b128 v[226:229], v169 offset:52224
	ds_read_b128 v[230:233], v169 offset:53248
	ds_read_b128 v[234:237], v169 offset:54272
	ds_read_b128 v[238:241], v169 offset:55296
	ds_read_b128 v[242:245], v169 offset:56320
	global_load_lds_dwordx4 v[178:179], off
	v_lshl_add_u64 v[178:179], v[196:197], 0, s[26:27]
	s_mov_b32 m0, s50
	s_addc_u32 s31, s31, 0
	s_add_i32 s51, s51, s68
	global_load_lds_dwordx4 v[178:179], off
	v_lshl_add_u64 v[178:179], s[30:31], 0, v[170:171]
	s_mov_b32 m0, s51
	s_add_i32 s64, s51, 0x2000
	global_load_lds_dwordx4 v[178:179], off
	v_lshl_add_u64 v[178:179], s[30:31], 0, v[172:173]
	s_mov_b32 m0, s64
	v_readlane_b32 s26, v253, 39
	global_load_lds_dwordx4 v[178:179], off
	s_mov_b32 m0, s75
	v_readlane_b32 s27, v253, 40
	s_nop 4
	global_load_lds_dwordx4 v34, s[26:27]
	s_mov_b32 m0, s76
	s_nop 0
	global_load_lds_dwordx4 v192, s[26:27]
	s_waitcnt vmcnt(8)
	s_waitcnt lgkmcnt(0)
	s_barrier
	s_setprio 1
	s_waitcnt lgkmcnt(0)
	v_mfma_f32_16x16x128_f8f6f4 v[96:99], v[26:33], v[204:211], v[96:99]
	v_mfma_f32_16x16x128_f8f6f4 v[92:95], v[18:25], v[204:211], v[92:95]
	v_mfma_f32_16x16x128_f8f6f4 v[84:87], v[18:25], v[222:229], v[84:87]
	v_mfma_f32_16x16x128_f8f6f4 v[88:91], v[26:33], v[222:229], v[88:91]
	v_mfma_f32_16x16x128_f8f6f4 v[80:83], v[26:33], v[230:237], v[80:83]
	v_mfma_f32_16x16x128_f8f6f4 v[76:79], v[18:25], v[230:237], v[76:79]
	v_mfma_f32_16x16x128_f8f6f4 v[68:71], v[18:25], v[238:245], v[68:71]
	v_mfma_f32_16x16x128_f8f6f4 v[72:75], v[26:33], v[238:245], v[72:75]
	s_setprio 0
	s_setprio 1
	v_mfma_f32_16x16x128_f8f6f4 v[64:67], v[10:17], v[204:211], v[64:67]
	v_mfma_f32_16x16x128_f8f6f4 v[60:63], v[2:9], v[204:211], v[60:63]
	v_mfma_f32_16x16x128_f8f6f4 v[52:55], v[2:9], v[222:229], v[52:55]
	v_mfma_f32_16x16x128_f8f6f4 v[56:59], v[10:17], v[222:229], v[56:59]
	v_mfma_f32_16x16x128_f8f6f4 v[48:51], v[10:17], v[230:237], v[48:51]
	v_mfma_f32_16x16x128_f8f6f4 v[44:47], v[2:9], v[230:237], v[44:47]
	v_mfma_f32_16x16x128_f8f6f4 v[36:39], v[2:9], v[238:245], v[36:39]
	s_barrier
	s_setprio 3
	v_mfma_f32_16x16x128_f8f6f4 v[40:43], v[10:17], v[238:245], v[40:43]
	s_setprio 0
	v_lshl_add_u64 v[18:19], s[26:27], 0, v[174:175]
	v_lshl_add_u64 v[20:21], s[26:27], 0, v[190:191]
	s_mov_b32 s63, 0
	s_mov_b64 s[30:31], 0
	s_branch .LBB0_821
.LBB0_820:
	ds_read_b128 v[204:207], v200
	ds_read_b128 v[208:211], v200 offset:1024
	ds_read_b128 v[222:225], v200 offset:2048
	ds_read_b128 v[226:229], v200 offset:3072
	ds_read_b128 v[10:13], v199
	ds_read_b128 v[14:17], v199 offset:1024
	ds_read_b128 v[2:5], v199 offset:2048
	ds_read_b128 v[6:9], v199 offset:3072
	s_add_u32 s14, s30, 0x200
	s_addc_u32 s86, s31, 0
	s_and_b64 s[40:41], s[36:37], exec
	s_cselect_b32 s14, 0, s14
	s_cselect_b32 s41, 0, s86
	s_add_u32 s40, s20, s14
	s_addc_u32 s41, s21, s41
	s_add_u32 s14, s81, s30
	s_addc_u32 s86, s82, s31
	s_and_b64 s[36:37], s[36:37], exec
	s_cselect_b32 s37, s23, s86
	s_cselect_b32 s36, s22, s14
	s_mov_b32 m0, s84
	v_lshl_add_u64 v[30:31], v[20:21], 0, s[30:31]
	ds_read_b128 v[22:25], v169
	ds_read_b128 v[26:29], v169 offset:1024
	ds_read_b128 v[230:233], v169 offset:2048
	ds_read_b128 v[234:237], v169 offset:3072
	ds_read_b128 v[238:241], v169 offset:4096
	ds_read_b128 v[242:245], v169 offset:5120
	ds_read_b128 v[178:181], v169 offset:6144
	ds_read_b128 v[182:185], v169 offset:7168
	global_load_lds_dwordx4 v[30:31], off
	v_lshl_add_u64 v[30:31], v[18:19], 0, s[30:31]
	s_mov_b32 m0, s53
	s_nop 0
	global_load_lds_dwordx4 v[30:31], off
	s_waitcnt vmcnt(8)
	s_waitcnt lgkmcnt(0)
	s_barrier
	s_setprio 1
	s_waitcnt lgkmcnt(0)
	v_mfma_f32_16x16x128_f8f6f4 v[160:163], v[204:211], v[22:29], v[160:163]
	v_mfma_f32_16x16x128_f8f6f4 v[156:159], v[222:229], v[22:29], v[156:159]
	v_mfma_f32_16x16x128_f8f6f4 v[148:151], v[222:229], v[230:237], v[148:151]
	v_mfma_f32_16x16x128_f8f6f4 v[152:155], v[204:211], v[230:237], v[152:155]
	v_mfma_f32_16x16x128_f8f6f4 v[144:147], v[204:211], v[238:245], v[144:147]
	v_mfma_f32_16x16x128_f8f6f4 v[140:143], v[222:229], v[238:245], v[140:143]
	v_mfma_f32_16x16x128_f8f6f4 v[132:135], v[222:229], v[178:185], v[132:135]
	v_mfma_f32_16x16x128_f8f6f4 v[136:139], v[204:211], v[178:185], v[136:139]
	s_setprio 0
	s_setprio 1
	v_mfma_f32_16x16x128_f8f6f4 v[128:131], v[10:17], v[22:29], v[128:131]
	v_mfma_f32_16x16x128_f8f6f4 v[124:127], v[2:9], v[22:29], v[124:127]
	v_mfma_f32_16x16x128_f8f6f4 v[116:119], v[2:9], v[230:237], v[116:119]
	v_mfma_f32_16x16x128_f8f6f4 v[120:123], v[10:17], v[230:237], v[120:123]
	v_mfma_f32_16x16x128_f8f6f4 v[112:115], v[10:17], v[238:245], v[112:115]
	v_mfma_f32_16x16x128_f8f6f4 v[108:111], v[2:9], v[238:245], v[108:111]
	v_mfma_f32_16x16x128_f8f6f4 v[100:103], v[2:9], v[178:185], v[100:103]
	s_barrier
	s_setprio 3
	v_mfma_f32_16x16x128_f8f6f4 v[104:107], v[10:17], v[178:185], v[104:107]
	s_setprio 0
	s_mov_b32 m0, s52
	v_lshl_add_u64 v[22:23], s[36:37], 0, v[170:171]
	s_add_u32 s86, s36, 0x20000
	ds_read_b128 v[178:181], v169 offset:16384
	ds_read_b128 v[182:185], v169 offset:17408
	ds_read_b128 v[230:233], v169 offset:18432
	ds_read_b128 v[234:237], v169 offset:19456
	ds_read_b128 v[238:241], v169 offset:20480
	ds_read_b128 v[242:245], v169 offset:21504
	ds_read_b128 v[212:215], v169 offset:22528
	ds_read_b128 v[216:219], v169 offset:23552
	global_load_lds_dwordx4 v[22:23], off
	v_lshl_add_u64 v[24:25], s[36:37], 0, v[172:173]
	s_mov_b32 m0, s85
	s_addc_u32 s87, s37, 0
	global_load_lds_dwordx4 v[24:25], off
	v_lshl_add_u64 v[26:27], s[86:87], 0, v[170:171]
	s_mov_b32 m0, s55
	v_mov_b32_e32 v193, v35
	global_load_lds_dwordx4 v[26:27], off
	v_lshl_add_u64 v[26:27], s[86:87], 0, v[172:173]
	s_mov_b32 m0, s65
	v_lshl_add_u64 v[28:29], s[40:41], 0, v[34:35]
	global_load_lds_dwordx4 v[26:27], off
	s_mov_b32 m0, s69
	v_lshl_add_u64 v[26:27], s[40:41], 0, v[192:193]
	global_load_lds_dwordx4 v34, s[40:41]
	s_mov_b32 m0, s70
	s_nop 0
	global_load_lds_dwordx4 v192, s[40:41]
	s_waitcnt vmcnt(8)
	s_waitcnt lgkmcnt(0)
	s_barrier
	s_setprio 1
	s_waitcnt lgkmcnt(0)
	v_mfma_f32_16x16x128_f8f6f4 v[96:99], v[204:211], v[178:185], v[96:99]
	v_mfma_f32_16x16x128_f8f6f4 v[92:95], v[222:229], v[178:185], v[92:95]
	v_mfma_f32_16x16x128_f8f6f4 v[84:87], v[222:229], v[230:237], v[84:87]
	v_mfma_f32_16x16x128_f8f6f4 v[88:91], v[204:211], v[230:237], v[88:91]
	v_mfma_f32_16x16x128_f8f6f4 v[80:83], v[204:211], v[238:245], v[80:83]
	v_mfma_f32_16x16x128_f8f6f4 v[76:79], v[222:229], v[238:245], v[76:79]
	v_mfma_f32_16x16x128_f8f6f4 v[68:71], v[222:229], v[212:219], v[68:71]
	v_mfma_f32_16x16x128_f8f6f4 v[72:75], v[204:211], v[212:219], v[72:75]
	s_setprio 0
	s_setprio 1
	v_mfma_f32_16x16x128_f8f6f4 v[64:67], v[10:17], v[178:185], v[64:67]
	v_mfma_f32_16x16x128_f8f6f4 v[60:63], v[2:9], v[178:185], v[60:63]
	v_mfma_f32_16x16x128_f8f6f4 v[52:55], v[2:9], v[230:237], v[52:55]
	v_mfma_f32_16x16x128_f8f6f4 v[56:59], v[10:17], v[230:237], v[56:59]
	v_mfma_f32_16x16x128_f8f6f4 v[48:51], v[10:17], v[238:245], v[48:51]
	v_mfma_f32_16x16x128_f8f6f4 v[44:47], v[2:9], v[238:245], v[44:47]
	v_mfma_f32_16x16x128_f8f6f4 v[36:39], v[2:9], v[212:219], v[36:39]
	s_barrier
	s_setprio 3
	v_mfma_f32_16x16x128_f8f6f4 v[40:43], v[10:17], v[212:219], v[40:43]
	s_setprio 0
	ds_read_b128 v[178:181], v201
	ds_read_b128 v[182:185], v201 offset:1024
	ds_read_b128 v[204:207], v201 offset:2048
	ds_read_b128 v[208:211], v201 offset:3072
	ds_read_b128 v[10:13], v202
	ds_read_b128 v[14:17], v202 offset:1024
	ds_read_b128 v[2:5], v202 offset:2048
	ds_read_b128 v[6:9], v202 offset:3072
	s_mov_b32 m0, s71
	ds_read_b128 v[212:215], v169 offset:32768
	ds_read_b128 v[216:219], v169 offset:33792
	ds_read_b128 v[222:225], v169 offset:34816
	ds_read_b128 v[226:229], v169 offset:35840
	ds_read_b128 v[230:233], v169 offset:36864
	ds_read_b128 v[234:237], v169 offset:37888
	ds_read_b128 v[238:241], v169 offset:38912
	ds_read_b128 v[242:245], v169 offset:39936
	global_load_lds_dwordx4 v189, s[40:41]
	s_mov_b32 m0, s72
	s_nop 0
	global_load_lds_dwordx4 v198, s[40:41]
	s_waitcnt vmcnt(8)
	s_waitcnt lgkmcnt(0)
	s_barrier
	s_setprio 1
	s_waitcnt lgkmcnt(0)
	v_mfma_f32_16x16x128_f8f6f4 v[160:163], v[178:185], v[212:219], v[160:163]
	v_mfma_f32_16x16x128_f8f6f4 v[156:159], v[204:211], v[212:219], v[156:159]
	v_mfma_f32_16x16x128_f8f6f4 v[148:151], v[204:211], v[222:229], v[148:151]
	v_mfma_f32_16x16x128_f8f6f4 v[152:155], v[178:185], v[222:229], v[152:155]
	v_mfma_f32_16x16x128_f8f6f4 v[144:147], v[178:185], v[230:237], v[144:147]
	v_mfma_f32_16x16x128_f8f6f4 v[140:143], v[204:211], v[230:237], v[140:143]
	v_mfma_f32_16x16x128_f8f6f4 v[132:135], v[204:211], v[238:245], v[132:135]
	v_mfma_f32_16x16x128_f8f6f4 v[136:139], v[178:185], v[238:245], v[136:139]
	s_setprio 0
	s_setprio 1
	v_mfma_f32_16x16x128_f8f6f4 v[128:131], v[10:17], v[212:219], v[128:131]
	v_mfma_f32_16x16x128_f8f6f4 v[124:127], v[2:9], v[212:219], v[124:127]
	v_mfma_f32_16x16x128_f8f6f4 v[116:119], v[2:9], v[222:229], v[116:119]
	v_mfma_f32_16x16x128_f8f6f4 v[120:123], v[10:17], v[222:229], v[120:123]
	v_mfma_f32_16x16x128_f8f6f4 v[112:115], v[10:17], v[230:237], v[112:115]
	v_mfma_f32_16x16x128_f8f6f4 v[108:111], v[2:9], v[230:237], v[108:111]
	v_mfma_f32_16x16x128_f8f6f4 v[100:103], v[2:9], v[238:245], v[100:103]
	s_barrier
	s_setprio 3
	v_mfma_f32_16x16x128_f8f6f4 v[104:107], v[10:17], v[238:245], v[104:107]
	s_setprio 0
	s_mov_b32 m0, s54
	v_lshl_add_u64 v[22:23], v[22:23], 0, s[18:19]
	s_add_u32 s36, s36, 0x20080
	ds_read_b128 v[212:215], v169 offset:49152
	ds_read_b128 v[216:219], v169 offset:50176
	ds_read_b128 v[222:225], v169 offset:51200
	ds_read_b128 v[226:229], v169 offset:52224
	ds_read_b128 v[230:233], v169 offset:53248
	ds_read_b128 v[234:237], v169 offset:54272
	ds_read_b128 v[238:241], v169 offset:55296
	ds_read_b128 v[242:245], v169 offset:56320
	global_load_lds_dwordx4 v[22:23], off
	v_lshl_add_u64 v[22:23], v[24:25], 0, s[18:19]
	s_mov_b32 m0, s50
	s_addc_u32 s37, s37, 0
	global_load_lds_dwordx4 v[22:23], off
	v_lshl_add_u64 v[22:23], s[36:37], 0, v[170:171]
	s_mov_b32 m0, s51
	s_nop 0
	global_load_lds_dwordx4 v[22:23], off
	v_lshl_add_u64 v[22:23], s[36:37], 0, v[172:173]
	s_mov_b32 m0, s64
	s_nop 0
	global_load_lds_dwordx4 v[22:23], off
	v_lshl_add_u64 v[22:23], v[28:29], 0, s[18:19]
	s_mov_b32 m0, s75
	s_nop 0
	global_load_lds_dwordx4 v[22:23], off
	v_lshl_add_u64 v[22:23], v[26:27], 0, s[18:19]
	s_mov_b32 m0, s76
	s_nop 0
	global_load_lds_dwordx4 v[22:23], off
	s_waitcnt vmcnt(8)
	s_waitcnt lgkmcnt(0)
	s_barrier
	s_setprio 1
	s_waitcnt lgkmcnt(0)
	v_mfma_f32_16x16x128_f8f6f4 v[96:99], v[178:185], v[212:219], v[96:99]
	v_mfma_f32_16x16x128_f8f6f4 v[92:95], v[204:211], v[212:219], v[92:95]
	v_mfma_f32_16x16x128_f8f6f4 v[84:87], v[204:211], v[222:229], v[84:87]
	v_mfma_f32_16x16x128_f8f6f4 v[88:91], v[178:185], v[222:229], v[88:91]
	v_mfma_f32_16x16x128_f8f6f4 v[80:83], v[178:185], v[230:237], v[80:83]
	v_mfma_f32_16x16x128_f8f6f4 v[76:79], v[204:211], v[230:237], v[76:79]
	v_mfma_f32_16x16x128_f8f6f4 v[68:71], v[204:211], v[238:245], v[68:71]
	v_mfma_f32_16x16x128_f8f6f4 v[72:75], v[178:185], v[238:245], v[72:75]
	s_setprio 0
	s_setprio 1
	v_mfma_f32_16x16x128_f8f6f4 v[64:67], v[10:17], v[212:219], v[64:67]
	v_mfma_f32_16x16x128_f8f6f4 v[60:63], v[2:9], v[212:219], v[60:63]
	v_mfma_f32_16x16x128_f8f6f4 v[52:55], v[2:9], v[222:229], v[52:55]
	v_mfma_f32_16x16x128_f8f6f4 v[56:59], v[10:17], v[222:229], v[56:59]
	v_mfma_f32_16x16x128_f8f6f4 v[48:51], v[10:17], v[230:237], v[48:51]
	v_mfma_f32_16x16x128_f8f6f4 v[44:47], v[2:9], v[230:237], v[44:47]
	v_mfma_f32_16x16x128_f8f6f4 v[36:39], v[2:9], v[238:245], v[36:39]
	s_barrier
	s_setprio 3
	v_mfma_f32_16x16x128_f8f6f4 v[40:43], v[10:17], v[238:245], v[40:43]
	s_setprio 0
	s_add_i32 s63, s63, 2
	s_add_u32 s30, s30, 0x100
	s_addc_u32 s31, s31, 0
	s_cmp_gt_u32 s63, 5
	s_cbranch_scc1 .LBB0_823

.LBB0_899:
	s_mul_i32 s14, s81, 0xe0000
	s_add_u32 s40, s44, s14
	s_addc_u32 s41, s45, 0
	s_and_b64 s[6:7], s[6:7], exec
	s_cselect_b32 s52, s41, s43
	s_cselect_b32 s53, s40, s42
	s_add_i32 s54, 0, 0x10000
	s_add_i32 s65, 0, 0x14000
	v_add_u32_e32 v34, s54, v167
	v_add_u32_e32 v206, s65, v167
	ds_read_b128 v[26:29], v34
	ds_read_b128 v[30:33], v34 offset:1024
	ds_read_b128 v[18:21], v34 offset:2048
	ds_read_b128 v[22:25], v34 offset:3072
	ds_read_b128 v[10:13], v206
	ds_read_b128 v[14:17], v206 offset:1024
	ds_read_b128 v[2:5], v206 offset:2048
	ds_read_b128 v[6:9], v206 offset:3072
	s_add_u32 s6, s42, 0x70080
	s_addc_u32 s7, s43, 0
	s_add_i32 s84, s72, 0xc000
	v_lshl_add_u64 v[216:217], s[6:7], 0, v[174:175]
	s_mov_b32 m0, s84
	s_add_i32 s85, s72, 0xe000
	ds_read_b128 v[178:181], v189
	ds_read_b128 v[182:185], v189 offset:1024
	ds_read_b128 v[198:201], v189 offset:2048
	ds_read_b128 v[202:205], v189 offset:3072
	ds_read_b128 v[208:211], v189 offset:4096
	ds_read_b128 v[212:215], v189 offset:5120
	ds_read_b128 v[222:225], v189 offset:6144
	ds_read_b128 v[226:229], v189 offset:7168
	global_load_lds_dwordx4 v[216:217], off
	v_lshl_add_u64 v[216:217], s[6:7], 0, v[170:171]
	s_mov_b32 m0, s85
	s_nop 0
	global_load_lds_dwordx4 v[216:217], off
	s_waitcnt vmcnt(8)
	s_waitcnt lgkmcnt(0)
	s_barrier
	s_setprio 1
	s_waitcnt lgkmcnt(0)
	v_mfma_f32_16x16x128_f8f6f4 v[160:163], v[26:33], v[178:185], 0
	v_mfma_f32_16x16x128_f8f6f4 v[156:159], v[18:25], v[178:185], 0
	v_mfma_f32_16x16x128_f8f6f4 v[148:151], v[18:25], v[198:205], 0
	v_mfma_f32_16x16x128_f8f6f4 v[152:155], v[26:33], v[198:205], 0
	v_mfma_f32_16x16x128_f8f6f4 v[144:147], v[26:33], v[208:215], 0
	v_mfma_f32_16x16x128_f8f6f4 v[140:143], v[18:25], v[208:215], 0
	v_mfma_f32_16x16x128_f8f6f4 v[132:135], v[18:25], v[222:229], 0
	v_mfma_f32_16x16x128_f8f6f4 v[136:139], v[26:33], v[222:229], 0
	s_setprio 0
	s_setprio 1
	v_mfma_f32_16x16x128_f8f6f4 v[128:131], v[10:17], v[178:185], 0
	v_mfma_f32_16x16x128_f8f6f4 v[124:127], v[2:9], v[178:185], 0
	v_mfma_f32_16x16x128_f8f6f4 v[116:119], v[2:9], v[198:205], 0
	v_mfma_f32_16x16x128_f8f6f4 v[120:123], v[10:17], v[198:205], 0
	v_mfma_f32_16x16x128_f8f6f4 v[112:115], v[10:17], v[208:215], 0
	v_mfma_f32_16x16x128_f8f6f4 v[108:111], v[2:9], v[208:215], 0
	v_mfma_f32_16x16x128_f8f6f4 v[100:103], v[2:9], v[222:229], 0
	s_barrier
	s_setprio 3
	v_mfma_f32_16x16x128_f8f6f4 v[104:107], v[10:17], v[222:229], 0
	s_setprio 0
	v_lshl_add_u64 v[198:199], v[196:197], 0, v[172:173]
	s_add_i32 s54, s54, s71
	v_lshl_add_u64 v[200:201], v[198:199], 0, s[28:29]
	s_mov_b32 m0, s54
	ds_read_b128 v[178:181], v189 offset:16384
	ds_read_b128 v[182:185], v189 offset:17408
	ds_read_b128 v[208:211], v189 offset:18432
	ds_read_b128 v[212:215], v189 offset:19456
	ds_read_b128 v[222:225], v189 offset:20480
	ds_read_b128 v[226:229], v189 offset:21504
	ds_read_b128 v[230:233], v189 offset:22528
	ds_read_b128 v[234:237], v189 offset:23552
	global_load_lds_dwordx4 v[200:201], off
	v_lshl_add_u64 v[200:201], v[196:197], 0, v[168:169]
	s_add_i32 s55, s54, 0x2000
	v_lshl_add_u64 v[202:203], v[200:201], 0, s[28:29]
	s_mov_b32 m0, s55
	s_mov_b64 s[6:7], 0x70100
	global_load_lds_dwordx4 v[202:203], off
	v_lshl_add_u64 v[202:203], v[196:197], 0, s[6:7]
	s_add_i32 s65, s65, s71
	v_lshl_add_u64 v[204:205], v[202:203], 0, v[172:173]
	s_mov_b32 m0, s65
	s_add_i32 s67, s65, 0x2000
	global_load_lds_dwordx4 v[204:205], off
	v_lshl_add_u64 v[202:203], v[202:203], 0, v[168:169]
	s_mov_b32 m0, s67
	s_nop 0
	global_load_lds_dwordx4 v[202:203], off
	v_lshl_add_u64 v[202:203], s[42:43], 0, v[174:175]
	v_lshl_add_u64 v[204:205], v[202:203], 0, s[28:29]
	s_mov_b32 m0, s72
	s_nop 0
	global_load_lds_dwordx4 v[204:205], off
	v_lshl_add_u64 v[204:205], s[42:43], 0, v[170:171]
	v_lshl_add_u64 v[216:217], v[204:205], 0, s[28:29]
	s_mov_b32 m0, s73
	s_nop 0
	global_load_lds_dwordx4 v[216:217], off
	s_waitcnt vmcnt(8)
	s_waitcnt lgkmcnt(0)
	s_barrier
	s_setprio 1
	s_waitcnt lgkmcnt(0)
	v_mfma_f32_16x16x128_f8f6f4 v[96:99], v[26:33], v[178:185], 0
	v_mfma_f32_16x16x128_f8f6f4 v[92:95], v[18:25], v[178:185], 0
	v_mfma_f32_16x16x128_f8f6f4 v[84:87], v[18:25], v[208:215], 0
	v_mfma_f32_16x16x128_f8f6f4 v[88:91], v[26:33], v[208:215], 0
	v_mfma_f32_16x16x128_f8f6f4 v[80:83], v[26:33], v[222:229], 0
	v_mfma_f32_16x16x128_f8f6f4 v[76:79], v[18:25], v[222:229], 0
	v_mfma_f32_16x16x128_f8f6f4 v[68:71], v[18:25], v[230:237], 0
	v_mfma_f32_16x16x128_f8f6f4 v[72:75], v[26:33], v[230:237], 0
	s_setprio 0
	s_setprio 1
	v_mfma_f32_16x16x128_f8f6f4 v[64:67], v[10:17], v[178:185], 0
	v_mfma_f32_16x16x128_f8f6f4 v[60:63], v[2:9], v[178:185], 0
	v_mfma_f32_16x16x128_f8f6f4 v[52:55], v[2:9], v[208:215], 0
	v_mfma_f32_16x16x128_f8f6f4 v[56:59], v[10:17], v[208:215], 0
	v_mfma_f32_16x16x128_f8f6f4 v[48:51], v[10:17], v[222:229], 0
	v_mfma_f32_16x16x128_f8f6f4 v[44:47], v[2:9], v[222:229], 0
	v_mfma_f32_16x16x128_f8f6f4 v[36:39], v[2:9], v[230:237], 0
	s_barrier
	s_setprio 3
	v_mfma_f32_16x16x128_f8f6f4 v[40:43], v[10:17], v[230:237], 0
	s_setprio 0
	s_add_i32 s50, 0, 0x18000
	s_add_i32 s63, 0, 0x1c000
	v_add_u32_e32 v207, s50, v167
	v_add_u32_e32 v208, s63, v167
	ds_read_b128 v[26:29], v207
	ds_read_b128 v[30:33], v207 offset:1024
	ds_read_b128 v[18:21], v207 offset:2048
	ds_read_b128 v[22:25], v207 offset:3072
	ds_read_b128 v[10:13], v208
	ds_read_b128 v[14:17], v208 offset:1024
	ds_read_b128 v[2:5], v208 offset:2048
	ds_read_b128 v[6:9], v208 offset:3072
	s_add_u32 s6, s42, 0x70100
	s_addc_u32 s7, s43, 0
	s_mov_b32 m0, s74
	v_lshl_add_u64 v[218:219], s[6:7], 0, v[174:175]
	ds_read_b128 v[178:181], v189 offset:32768
	ds_read_b128 v[182:185], v189 offset:33792
	ds_read_b128 v[210:213], v189 offset:34816
	ds_read_b128 v[214:217], v189 offset:35840
	ds_read_b128 v[222:225], v189 offset:36864
	ds_read_b128 v[226:229], v189 offset:37888
	ds_read_b128 v[230:233], v189 offset:38912
	ds_read_b128 v[234:237], v189 offset:39936
	global_load_lds_dwordx4 v[218:219], off
	v_lshl_add_u64 v[218:219], s[6:7], 0, v[170:171]
	s_mov_b32 m0, s75
	s_nop 0
	global_load_lds_dwordx4 v[218:219], off
	s_waitcnt vmcnt(8)
	s_waitcnt lgkmcnt(0)
	s_barrier
	s_setprio 1
	s_waitcnt lgkmcnt(0)
	v_mfma_f32_16x16x128_f8f6f4 v[160:163], v[26:33], v[178:185], v[160:163]
	v_mfma_f32_16x16x128_f8f6f4 v[156:159], v[18:25], v[178:185], v[156:159]
	v_mfma_f32_16x16x128_f8f6f4 v[148:151], v[18:25], v[210:217], v[148:151]
	v_mfma_f32_16x16x128_f8f6f4 v[152:155], v[26:33], v[210:217], v[152:155]
	v_mfma_f32_16x16x128_f8f6f4 v[144:147], v[26:33], v[222:229], v[144:147]
	v_mfma_f32_16x16x128_f8f6f4 v[140:143], v[18:25], v[222:229], v[140:143]
	v_mfma_f32_16x16x128_f8f6f4 v[132:135], v[18:25], v[230:237], v[132:135]
	v_mfma_f32_16x16x128_f8f6f4 v[136:139], v[26:33], v[230:237], v[136:139]
	s_setprio 0
	s_setprio 1
	v_mfma_f32_16x16x128_f8f6f4 v[128:131], v[10:17], v[178:185], v[128:131]
	v_mfma_f32_16x16x128_f8f6f4 v[124:127], v[2:9], v[178:185], v[124:127]
	v_mfma_f32_16x16x128_f8f6f4 v[116:119], v[2:9], v[210:217], v[116:119]
	v_mfma_f32_16x16x128_f8f6f4 v[120:123], v[10:17], v[210:217], v[120:123]
	v_mfma_f32_16x16x128_f8f6f4 v[112:115], v[10:17], v[222:229], v[112:115]
	v_mfma_f32_16x16x128_f8f6f4 v[108:111], v[2:9], v[222:229], v[108:111]
	v_mfma_f32_16x16x128_f8f6f4 v[100:103], v[2:9], v[230:237], v[100:103]
	s_barrier
	s_setprio 3
	v_mfma_f32_16x16x128_f8f6f4 v[104:107], v[10:17], v[230:237], v[104:107]
	s_setprio 0
	s_mov_b64 s[6:7], 0x180
	s_add_i32 s50, s50, s71
	v_lshl_add_u64 v[198:199], v[198:199], 0, s[6:7]
	s_mov_b32 m0, s50
	s_add_i32 s51, s50, 0x2000
	ds_read_b128 v[178:181], v189 offset:49152
	ds_read_b128 v[182:185], v189 offset:50176
	ds_read_b128 v[210:213], v189 offset:51200
	ds_read_b128 v[214:217], v189 offset:52224
	ds_read_b128 v[222:225], v189 offset:53248
	ds_read_b128 v[226:229], v189 offset:54272
	ds_read_b128 v[230:233], v189 offset:55296
	ds_read_b128 v[234:237], v189 offset:56320
	global_load_lds_dwordx4 v[198:199], off
	v_lshl_add_u64 v[198:199], v[200:201], 0, s[6:7]
	s_mov_b32 m0, s51
	s_add_i32 s63, s63, s71
	global_load_lds_dwordx4 v[198:199], off
	v_lshl_add_u64 v[198:199], v[196:197], 0, s[26:27]
	v_lshl_add_u64 v[200:201], v[198:199], 0, v[172:173]
	s_mov_b32 m0, s63
	s_add_i32 s64, s63, 0x2000
	global_load_lds_dwordx4 v[200:201], off
	v_lshl_add_u64 v[198:199], v[198:199], 0, v[168:169]
	s_mov_b32 m0, s64
	s_nop 0
	global_load_lds_dwordx4 v[198:199], off
	v_lshl_add_u64 v[198:199], v[202:203], 0, s[6:7]
	s_mov_b32 m0, s77
	s_nop 0
	global_load_lds_dwordx4 v[198:199], off
	v_lshl_add_u64 v[198:199], v[204:205], 0, s[6:7]
	s_mov_b32 m0, s78
	s_nop 0
	global_load_lds_dwordx4 v[198:199], off
	s_waitcnt vmcnt(8)
	s_waitcnt lgkmcnt(0)
	s_barrier
	s_setprio 1
	s_waitcnt lgkmcnt(0)
	v_mfma_f32_16x16x128_f8f6f4 v[96:99], v[26:33], v[178:185], v[96:99]
	v_mfma_f32_16x16x128_f8f6f4 v[92:95], v[18:25], v[178:185], v[92:95]
	v_mfma_f32_16x16x128_f8f6f4 v[84:87], v[18:25], v[210:217], v[84:87]
	v_mfma_f32_16x16x128_f8f6f4 v[88:91], v[26:33], v[210:217], v[88:91]
	v_mfma_f32_16x16x128_f8f6f4 v[80:83], v[26:33], v[222:229], v[80:83]
	v_mfma_f32_16x16x128_f8f6f4 v[76:79], v[18:25], v[222:229], v[76:79]
	v_mfma_f32_16x16x128_f8f6f4 v[68:71], v[18:25], v[230:237], v[68:71]
	v_mfma_f32_16x16x128_f8f6f4 v[72:75], v[26:33], v[230:237], v[72:75]
	s_setprio 0
	s_setprio 1
	v_mfma_f32_16x16x128_f8f6f4 v[64:67], v[10:17], v[178:185], v[64:67]
	v_mfma_f32_16x16x128_f8f6f4 v[60:63], v[2:9], v[178:185], v[60:63]
	v_mfma_f32_16x16x128_f8f6f4 v[52:55], v[2:9], v[210:217], v[52:55]
	v_mfma_f32_16x16x128_f8f6f4 v[56:59], v[10:17], v[210:217], v[56:59]
	v_mfma_f32_16x16x128_f8f6f4 v[48:51], v[10:17], v[222:229], v[48:51]
	v_mfma_f32_16x16x128_f8f6f4 v[44:47], v[2:9], v[222:229], v[44:47]
	v_mfma_f32_16x16x128_f8f6f4 v[36:39], v[2:9], v[230:237], v[36:39]
	s_barrier
	s_setprio 3
	v_mfma_f32_16x16x128_f8f6f4 v[40:43], v[10:17], v[230:237], v[40:43]
	s_setprio 0
	s_mov_b64 s[6:7], 0x200
	v_lshl_add_u64 v[18:19], v[196:197], 0, s[6:7]
	s_mov_b32 s86, 0
.LBB0_900:
	ds_read_b128 v[2:5], v34
	ds_read_b128 v[6:9], v34 offset:1024
	ds_read_b128 v[10:13], v34 offset:2048
	ds_read_b128 v[14:17], v34 offset:3072
	ds_read_b128 v[178:181], v206
	ds_read_b128 v[182:185], v206 offset:1024
	ds_read_b128 v[196:199], v206 offset:2048
	ds_read_b128 v[200:203], v206 offset:3072
	s_add_u32 s6, s42, 0x200
	s_addc_u32 s7, s43, 0
	s_cmp_eq_u32 s86, 24
	s_cselect_b64 vcc, -1, 0
	s_cselect_b32 s7, s52, s7
	s_cselect_b32 s6, s53, s6
	v_cndmask_b32_e32 v21, v19, v195, vcc
	v_cndmask_b32_e32 v20, v18, v194, vcc
	s_mov_b32 m0, s84
	v_lshl_add_u64 v[30:31], s[42:43], 0, v[190:191]
	ds_read_b128 v[22:25], v189
	ds_read_b128 v[26:29], v189 offset:1024
	ds_read_b128 v[210:213], v189 offset:2048
	ds_read_b128 v[214:217], v189 offset:3072
	ds_read_b128 v[222:225], v189 offset:4096
	ds_read_b128 v[226:229], v189 offset:5120
	ds_read_b128 v[230:233], v189 offset:6144
	ds_read_b128 v[234:237], v189 offset:7168
	global_load_lds_dwordx4 v[30:31], off
	v_lshl_add_u64 v[30:31], s[42:43], 0, v[192:193]
	s_mov_b32 m0, s85
	s_nop 0
	global_load_lds_dwordx4 v[30:31], off
	s_waitcnt vmcnt(8)
	s_waitcnt lgkmcnt(0)
	s_barrier
	s_setprio 1
	s_waitcnt lgkmcnt(0)
	v_mfma_f32_16x16x128_f8f6f4 v[160:163], v[2:9], v[22:29], v[160:163]
	v_mfma_f32_16x16x128_f8f6f4 v[156:159], v[10:17], v[22:29], v[156:159]
	v_mfma_f32_16x16x128_f8f6f4 v[148:151], v[10:17], v[210:217], v[148:151]
	v_mfma_f32_16x16x128_f8f6f4 v[152:155], v[2:9], v[210:217], v[152:155]
	v_mfma_f32_16x16x128_f8f6f4 v[144:147], v[2:9], v[222:229], v[144:147]
	v_mfma_f32_16x16x128_f8f6f4 v[140:143], v[10:17], v[222:229], v[140:143]
	v_mfma_f32_16x16x128_f8f6f4 v[132:135], v[10:17], v[230:237], v[132:135]
	v_mfma_f32_16x16x128_f8f6f4 v[136:139], v[2:9], v[230:237], v[136:139]
	s_setprio 0
	s_setprio 1
	v_mfma_f32_16x16x128_f8f6f4 v[128:131], v[178:185], v[22:29], v[128:131]
	v_mfma_f32_16x16x128_f8f6f4 v[124:127], v[196:203], v[22:29], v[124:127]
	v_mfma_f32_16x16x128_f8f6f4 v[116:119], v[196:203], v[210:217], v[116:119]
	v_mfma_f32_16x16x128_f8f6f4 v[120:123], v[178:185], v[210:217], v[120:123]
	v_mfma_f32_16x16x128_f8f6f4 v[112:115], v[178:185], v[222:229], v[112:115]
	v_mfma_f32_16x16x128_f8f6f4 v[108:111], v[196:203], v[222:229], v[108:111]
	v_mfma_f32_16x16x128_f8f6f4 v[100:103], v[196:203], v[230:237], v[100:103]
	s_barrier
	s_setprio 3
	v_mfma_f32_16x16x128_f8f6f4 v[104:107], v[178:185], v[230:237], v[104:107]
	s_setprio 0
	s_mov_b32 m0, s54
	v_lshl_add_u64 v[22:23], v[20:21], 0, v[172:173]
	ds_read_b128 v[210:213], v189 offset:16384
	ds_read_b128 v[214:217], v189 offset:17408
	ds_read_b128 v[222:225], v189 offset:18432
	ds_read_b128 v[226:229], v189 offset:19456
	ds_read_b128 v[230:233], v189 offset:20480
	ds_read_b128 v[234:237], v189 offset:21504
	ds_read_b128 v[238:241], v189 offset:22528
	ds_read_b128 v[242:245], v189 offset:23552
	global_load_lds_dwordx4 v[22:23], off
	v_lshl_add_u64 v[24:25], v[20:21], 0, v[168:169]
	s_mov_b32 m0, s55
	v_lshl_add_u64 v[26:27], v[20:21], 0, s[2:3]
	global_load_lds_dwordx4 v[24:25], off
	v_lshl_add_u64 v[28:29], v[26:27], 0, v[172:173]
	s_mov_b32 m0, s65
	v_lshl_add_u64 v[26:27], v[26:27], 0, v[168:169]
	global_load_lds_dwordx4 v[28:29], off
	s_mov_b32 m0, s67
	v_lshl_add_u64 v[28:29], s[6:7], 0, v[170:171]
	global_load_lds_dwordx4 v[26:27], off
	v_lshl_add_u64 v[26:27], s[6:7], 0, v[174:175]
	s_mov_b32 m0, s72
	s_nop 0
	global_load_lds_dwordx4 v[26:27], off
	s_mov_b32 m0, s73
	s_nop 0
	global_load_lds_dwordx4 v[28:29], off
	s_waitcnt vmcnt(8)
	s_waitcnt lgkmcnt(0)
	s_barrier
	s_setprio 1
	s_waitcnt lgkmcnt(0)
	v_mfma_f32_16x16x128_f8f6f4 v[96:99], v[2:9], v[210:217], v[96:99]
	v_mfma_f32_16x16x128_f8f6f4 v[92:95], v[10:17], v[210:217], v[92:95]
	v_mfma_f32_16x16x128_f8f6f4 v[84:87], v[10:17], v[222:229], v[84:87]
	v_mfma_f32_16x16x128_f8f6f4 v[88:91], v[2:9], v[222:229], v[88:91]
	v_mfma_f32_16x16x128_f8f6f4 v[80:83], v[2:9], v[230:237], v[80:83]
	v_mfma_f32_16x16x128_f8f6f4 v[76:79], v[10:17], v[230:237], v[76:79]
	v_mfma_f32_16x16x128_f8f6f4 v[68:71], v[10:17], v[238:245], v[68:71]
	v_mfma_f32_16x16x128_f8f6f4 v[72:75], v[2:9], v[238:245], v[72:75]
	s_setprio 0
	s_setprio 1
	v_mfma_f32_16x16x128_f8f6f4 v[64:67], v[178:185], v[210:217], v[64:67]
	v_mfma_f32_16x16x128_f8f6f4 v[60:63], v[196:203], v[210:217], v[60:63]
	v_mfma_f32_16x16x128_f8f6f4 v[52:55], v[196:203], v[222:229], v[52:55]
	v_mfma_f32_16x16x128_f8f6f4 v[56:59], v[178:185], v[222:229], v[56:59]
	v_mfma_f32_16x16x128_f8f6f4 v[48:51], v[178:185], v[230:237], v[48:51]
	v_mfma_f32_16x16x128_f8f6f4 v[44:47], v[196:203], v[230:237], v[44:47]
	v_mfma_f32_16x16x128_f8f6f4 v[36:39], v[196:203], v[238:245], v[36:39]
	s_barrier
	s_setprio 3
	v_mfma_f32_16x16x128_f8f6f4 v[40:43], v[178:185], v[238:245], v[40:43]
	s_setprio 0
	ds_read_b128 v[178:181], v207
	ds_read_b128 v[182:185], v207 offset:1024
	ds_read_b128 v[196:199], v207 offset:2048
	ds_read_b128 v[200:203], v207 offset:3072
	ds_read_b128 v[10:13], v208
	ds_read_b128 v[14:17], v208 offset:1024
	ds_read_b128 v[2:5], v208 offset:2048
	ds_read_b128 v[6:9], v208 offset:3072
	s_add_u32 s6, s6, 0x70000
	s_addc_u32 s7, s7, 0
	s_mov_b32 m0, s74
	v_lshl_add_u64 v[30:31], s[6:7], 0, v[174:175]
	ds_read_b128 v[210:213], v189 offset:32768
	ds_read_b128 v[214:217], v189 offset:33792
	ds_read_b128 v[222:225], v189 offset:34816
	ds_read_b128 v[226:229], v189 offset:35840
	ds_read_b128 v[230:233], v189 offset:36864
	ds_read_b128 v[234:237], v189 offset:37888
	ds_read_b128 v[238:241], v189 offset:38912
	ds_read_b128 v[242:245], v189 offset:39936
	global_load_lds_dwordx4 v[30:31], off
	v_lshl_add_u64 v[30:31], s[6:7], 0, v[170:171]
	s_mov_b32 m0, s75
	s_nop 0
	global_load_lds_dwordx4 v[30:31], off
	s_waitcnt vmcnt(8)
	s_waitcnt lgkmcnt(0)
	s_barrier
	s_setprio 1
	s_waitcnt lgkmcnt(0)
	v_mfma_f32_16x16x128_f8f6f4 v[160:163], v[178:185], v[210:217], v[160:163]
	v_mfma_f32_16x16x128_f8f6f4 v[156:159], v[196:203], v[210:217], v[156:159]
	v_mfma_f32_16x16x128_f8f6f4 v[148:151], v[196:203], v[222:229], v[148:151]
	v_mfma_f32_16x16x128_f8f6f4 v[152:155], v[178:185], v[222:229], v[152:155]
	v_mfma_f32_16x16x128_f8f6f4 v[144:147], v[178:185], v[230:237], v[144:147]
	v_mfma_f32_16x16x128_f8f6f4 v[140:143], v[196:203], v[230:237], v[140:143]
	v_mfma_f32_16x16x128_f8f6f4 v[132:135], v[196:203], v[238:245], v[132:135]
	v_mfma_f32_16x16x128_f8f6f4 v[136:139], v[178:185], v[238:245], v[136:139]
	s_setprio 0
	s_setprio 1
	v_mfma_f32_16x16x128_f8f6f4 v[128:131], v[10:17], v[210:217], v[128:131]
	v_mfma_f32_16x16x128_f8f6f4 v[124:127], v[2:9], v[210:217], v[124:127]
	v_mfma_f32_16x16x128_f8f6f4 v[116:119], v[2:9], v[222:229], v[116:119]
	v_mfma_f32_16x16x128_f8f6f4 v[120:123], v[10:17], v[222:229], v[120:123]
	v_mfma_f32_16x16x128_f8f6f4 v[112:115], v[10:17], v[230:237], v[112:115]
	v_mfma_f32_16x16x128_f8f6f4 v[108:111], v[2:9], v[230:237], v[108:111]
	v_mfma_f32_16x16x128_f8f6f4 v[100:103], v[2:9], v[238:245], v[100:103]
	s_barrier
	s_setprio 3
	v_mfma_f32_16x16x128_f8f6f4 v[104:107], v[10:17], v[238:245], v[104:107]
	s_setprio 0
	s_mov_b32 m0, s50
	v_lshl_add_u64 v[22:23], v[22:23], 0, s[18:19]
	ds_read_b128 v[210:213], v189 offset:49152
	ds_read_b128 v[214:217], v189 offset:50176
	ds_read_b128 v[222:225], v189 offset:51200
	ds_read_b128 v[226:229], v189 offset:52224
	ds_read_b128 v[230:233], v189 offset:53248
	ds_read_b128 v[234:237], v189 offset:54272
	ds_read_b128 v[238:241], v189 offset:55296
	ds_read_b128 v[242:245], v189 offset:56320
	global_load_lds_dwordx4 v[22:23], off
	v_lshl_add_u64 v[22:23], v[24:25], 0, s[18:19]
	s_mov_b32 m0, s51
	v_lshl_add_u64 v[20:21], v[20:21], 0, s[34:35]
	global_load_lds_dwordx4 v[22:23], off
	v_lshl_add_u64 v[22:23], v[20:21], 0, v[172:173]
	s_mov_b32 m0, s63
	v_lshl_add_u64 v[20:21], v[20:21], 0, v[168:169]
	global_load_lds_dwordx4 v[22:23], off
	s_mov_b32 m0, s64
	s_nop 0
	global_load_lds_dwordx4 v[20:21], off
	v_lshl_add_u64 v[20:21], v[26:27], 0, s[18:19]
	s_mov_b32 m0, s77
	s_nop 0
	global_load_lds_dwordx4 v[20:21], off
	v_lshl_add_u64 v[20:21], v[28:29], 0, s[18:19]
	s_mov_b32 m0, s78
	s_nop 0
	global_load_lds_dwordx4 v[20:21], off
	s_waitcnt vmcnt(8)
	s_waitcnt lgkmcnt(0)
	s_barrier
	s_setprio 1
	s_waitcnt lgkmcnt(0)
	v_mfma_f32_16x16x128_f8f6f4 v[96:99], v[178:185], v[210:217], v[96:99]
	v_mfma_f32_16x16x128_f8f6f4 v[92:95], v[196:203], v[210:217], v[92:95]
	v_mfma_f32_16x16x128_f8f6f4 v[84:87], v[196:203], v[222:229], v[84:87]
	v_mfma_f32_16x16x128_f8f6f4 v[88:91], v[178:185], v[222:229], v[88:91]
	v_mfma_f32_16x16x128_f8f6f4 v[80:83], v[178:185], v[230:237], v[80:83]
	v_mfma_f32_16x16x128_f8f6f4 v[76:79], v[196:203], v[230:237], v[76:79]
	v_mfma_f32_16x16x128_f8f6f4 v[68:71], v[196:203], v[238:245], v[68:71]
	v_mfma_f32_16x16x128_f8f6f4 v[72:75], v[178:185], v[238:245], v[72:75]
	s_setprio 0
	s_setprio 1
	v_mfma_f32_16x16x128_f8f6f4 v[64:67], v[10:17], v[210:217], v[64:67]
	v_mfma_f32_16x16x128_f8f6f4 v[60:63], v[2:9], v[210:217], v[60:63]
	v_mfma_f32_16x16x128_f8f6f4 v[52:55], v[2:9], v[222:229], v[52:55]
	v_mfma_f32_16x16x128_f8f6f4 v[56:59], v[10:17], v[222:229], v[56:59]
	v_mfma_f32_16x16x128_f8f6f4 v[48:51], v[10:17], v[230:237], v[48:51]
	v_mfma_f32_16x16x128_f8f6f4 v[44:47], v[2:9], v[230:237], v[44:47]
	v_mfma_f32_16x16x128_f8f6f4 v[36:39], v[2:9], v[238:245], v[36:39]
	s_barrier
	s_setprio 3
	v_mfma_f32_16x16x128_f8f6f4 v[40:43], v[10:17], v[238:245], v[40:43]
	s_setprio 0
	s_add_i32 s86, s86, 2
	s_add_u32 s42, s42, 0x100
	s_addc_u32 s43, s43, 0
	s_cmp_gt_u32 s86, 25
	v_lshl_add_u64 v[18:19], v[18:19], 0, s[28:29]
	s_cbranch_scc0 .LBB0_900
	s_and_b64 vcc, exec, s[36:37]
	s_mov_b64 s[84:85], s[24:25]
	s_cbranch_vccz .LBB0_903
	s_barrier

.LBB0_953:
	s_add_u32 s95, s30, 0x200
	s_addc_u32 s96, s31, 0
	s_add_i32 s65, 0, 0x14000
	s_add_i32 s67, 0, 0x10000
	v_add_u32_e32 v199, s65, v167
	v_add_u32_e32 v200, s67, v167
	ds_read_b128 v[10:13], v199
	ds_read_b128 v[14:17], v199 offset:1024
	ds_read_b128 v[2:5], v199 offset:2048
	ds_read_b128 v[6:9], v199 offset:3072
	ds_read_b128 v[22:25], v200 offset:3072
	ds_read_b128 v[18:21], v200 offset:2048
	ds_read_b128 v[30:33], v200 offset:1024
	ds_read_b128 v[26:29], v200
	s_lshl_b32 s14, s94, 10
	s_add_i32 s97, s14, 0
	s_add_i32 s97, s97, 0x20400
	v_mov_b32_e32 v191, v35
	v_mov_b32_e32 v175, v35
	s_add_i32 s83, s52, 0xc000
	v_readlane_b32 s26, v253, 28
	s_mov_b32 m0, s83
	v_readlane_b32 s27, v253, 29
	s_add_i32 s53, s52, 0xe000
	ds_read_b128 v[178:181], v169
	ds_read_b128 v[182:185], v169 offset:1024
	ds_read_b128 v[202:205], v169 offset:2048
	ds_read_b128 v[206:209], v169 offset:3072
	ds_read_b128 v[210:213], v169 offset:4096
	ds_read_b128 v[214:217], v169 offset:5120
	ds_read_b128 v[222:225], v169 offset:6144
	ds_read_b128 v[226:229], v169 offset:7168
	global_load_lds_dwordx4 v190, s[26:27]
	s_mov_b32 m0, s53
	s_nop 0
	global_load_lds_dwordx4 v174, s[26:27]
	s_waitcnt vmcnt(8)
	s_waitcnt lgkmcnt(0)
	s_barrier
	s_setprio 1
	s_waitcnt lgkmcnt(0)
	v_mfma_f32_16x16x128_f8f6f4 v[160:163], v[26:33], v[178:185], 0
	v_mfma_f32_16x16x128_f8f6f4 v[156:159], v[18:25], v[178:185], 0
	v_mfma_f32_16x16x128_f8f6f4 v[148:151], v[18:25], v[202:209], 0
	v_mfma_f32_16x16x128_f8f6f4 v[152:155], v[26:33], v[202:209], 0
	v_mfma_f32_16x16x128_f8f6f4 v[144:147], v[26:33], v[210:217], 0
	v_mfma_f32_16x16x128_f8f6f4 v[140:143], v[18:25], v[210:217], 0
	v_mfma_f32_16x16x128_f8f6f4 v[132:135], v[18:25], v[222:229], 0
	v_mfma_f32_16x16x128_f8f6f4 v[136:139], v[26:33], v[222:229], 0
	s_setprio 0
	s_setprio 1
	v_mfma_f32_16x16x128_f8f6f4 v[128:131], v[10:17], v[178:185], 0
	v_mfma_f32_16x16x128_f8f6f4 v[124:127], v[2:9], v[178:185], 0
	v_mfma_f32_16x16x128_f8f6f4 v[116:119], v[2:9], v[202:209], 0
	v_mfma_f32_16x16x128_f8f6f4 v[120:123], v[10:17], v[202:209], 0
	v_mfma_f32_16x16x128_f8f6f4 v[112:115], v[10:17], v[210:217], 0
	v_mfma_f32_16x16x128_f8f6f4 v[108:111], v[2:9], v[210:217], 0
	v_mfma_f32_16x16x128_f8f6f4 v[100:103], v[2:9], v[222:229], 0
	s_barrier
	s_setprio 3
	v_mfma_f32_16x16x128_f8f6f4 v[104:107], v[10:17], v[222:229], 0
	s_setprio 0
	v_lshl_add_u64 v[194:195], s[30:31], 0, v[170:171]
	s_add_i32 s67, s67, s82
	v_lshl_add_u64 v[196:197], v[194:195], 0, s[28:29]
	s_mov_b32 m0, s67
	s_add_i32 s55, s67, 0x2000
	ds_read_b128 v[178:181], v169 offset:16384
	ds_read_b128 v[182:185], v169 offset:17408
	ds_read_b128 v[202:205], v169 offset:18432
	ds_read_b128 v[206:209], v169 offset:19456
	ds_read_b128 v[210:213], v169 offset:20480
	ds_read_b128 v[214:217], v169 offset:21504
	ds_read_b128 v[222:225], v169 offset:22528
	ds_read_b128 v[226:229], v169 offset:23552
	global_load_lds_dwordx4 v[196:197], off
	v_lshl_add_u64 v[196:197], s[30:31], 0, v[172:173]
	s_add_u32 s46, s30, 0x20100
	v_lshl_add_u64 v[218:219], v[196:197], 0, s[28:29]
	s_mov_b32 m0, s55
	s_addc_u32 s47, s31, 0
	s_add_i32 s65, s65, s82
	global_load_lds_dwordx4 v[218:219], off
	v_lshl_add_u64 v[218:219], s[46:47], 0, v[170:171]
	s_mov_b32 m0, s65
	s_add_i32 s54, s65, 0x2000
	global_load_lds_dwordx4 v[218:219], off
	v_lshl_add_u64 v[218:219], s[46:47], 0, v[172:173]
	s_mov_b32 m0, s54
	v_readlane_b32 s26, v253, 37
	global_load_lds_dwordx4 v[218:219], off
	s_mov_b32 m0, s52
	v_readlane_b32 s27, v253, 38
	s_nop 4
	global_load_lds_dwordx4 v34, s[26:27]
	s_mov_b32 m0, s84
	s_nop 0
	global_load_lds_dwordx4 v192, s[26:27]
	s_waitcnt vmcnt(8)
	s_waitcnt lgkmcnt(0)
	s_barrier
	s_setprio 1
	s_waitcnt lgkmcnt(0)
	v_mfma_f32_16x16x128_f8f6f4 v[96:99], v[26:33], v[178:185], 0
	v_mfma_f32_16x16x128_f8f6f4 v[92:95], v[18:25], v[178:185], 0
	v_mfma_f32_16x16x128_f8f6f4 v[84:87], v[18:25], v[202:209], 0
	v_mfma_f32_16x16x128_f8f6f4 v[88:91], v[26:33], v[202:209], 0
	v_mfma_f32_16x16x128_f8f6f4 v[80:83], v[26:33], v[210:217], 0
	v_mfma_f32_16x16x128_f8f6f4 v[76:79], v[18:25], v[210:217], 0
	v_mfma_f32_16x16x128_f8f6f4 v[68:71], v[18:25], v[222:229], 0
	v_mfma_f32_16x16x128_f8f6f4 v[72:75], v[26:33], v[222:229], 0
	s_setprio 0
	s_setprio 1
	v_mfma_f32_16x16x128_f8f6f4 v[64:67], v[10:17], v[178:185], 0
	v_mfma_f32_16x16x128_f8f6f4 v[60:63], v[2:9], v[178:185], 0
	v_mfma_f32_16x16x128_f8f6f4 v[52:55], v[2:9], v[202:209], 0
	v_mfma_f32_16x16x128_f8f6f4 v[56:59], v[10:17], v[202:209], 0
	v_mfma_f32_16x16x128_f8f6f4 v[48:51], v[10:17], v[210:217], 0
	v_mfma_f32_16x16x128_f8f6f4 v[44:47], v[2:9], v[210:217], 0
	v_mfma_f32_16x16x128_f8f6f4 v[36:39], v[2:9], v[222:229], 0
	s_barrier
	s_setprio 3
	v_mfma_f32_16x16x128_f8f6f4 v[40:43], v[10:17], v[222:229], 0
	s_setprio 0
	s_add_i32 s50, 0, 0x18000
	s_add_i32 s64, 0, 0x1c000
	v_add_u32_e32 v201, s50, v167
	v_add_u32_e32 v202, s64, v167
	ds_read_b128 v[26:29], v201
	ds_read_b128 v[30:33], v201 offset:1024
	ds_read_b128 v[18:21], v201 offset:2048
	ds_read_b128 v[22:25], v201 offset:3072
	ds_read_b128 v[10:13], v202
	ds_read_b128 v[14:17], v202 offset:1024
	ds_read_b128 v[2:5], v202 offset:2048
	ds_read_b128 v[6:9], v202 offset:3072
	s_mov_b32 m0, s85
	ds_read_b128 v[178:181], v169 offset:32768
	ds_read_b128 v[182:185], v169 offset:33792
	ds_read_b128 v[204:207], v169 offset:34816
	ds_read_b128 v[208:211], v169 offset:35840
	ds_read_b128 v[212:215], v169 offset:36864
	ds_read_b128 v[216:219], v169 offset:37888
	ds_read_b128 v[222:225], v169 offset:38912
	ds_read_b128 v[226:229], v169 offset:39936
	global_load_lds_dwordx4 v189, s[26:27]
	s_mov_b32 m0, s86
	s_nop 0
	global_load_lds_dwordx4 v198, s[26:27]
	s_waitcnt vmcnt(8)
	s_waitcnt lgkmcnt(0)
	s_barrier
	s_setprio 1
	s_waitcnt lgkmcnt(0)
	v_mfma_f32_16x16x128_f8f6f4 v[160:163], v[26:33], v[178:185], v[160:163]
	v_mfma_f32_16x16x128_f8f6f4 v[156:159], v[18:25], v[178:185], v[156:159]
	v_mfma_f32_16x16x128_f8f6f4 v[148:151], v[18:25], v[204:211], v[148:151]
	v_mfma_f32_16x16x128_f8f6f4 v[152:155], v[26:33], v[204:211], v[152:155]
	v_mfma_f32_16x16x128_f8f6f4 v[144:147], v[26:33], v[212:219], v[144:147]
	v_mfma_f32_16x16x128_f8f6f4 v[140:143], v[18:25], v[212:219], v[140:143]
	v_mfma_f32_16x16x128_f8f6f4 v[132:135], v[18:25], v[222:229], v[132:135]
	v_mfma_f32_16x16x128_f8f6f4 v[136:139], v[26:33], v[222:229], v[136:139]
	s_setprio 0
	s_setprio 1
	v_mfma_f32_16x16x128_f8f6f4 v[128:131], v[10:17], v[178:185], v[128:131]
	v_mfma_f32_16x16x128_f8f6f4 v[124:127], v[2:9], v[178:185], v[124:127]
	v_mfma_f32_16x16x128_f8f6f4 v[116:119], v[2:9], v[204:211], v[116:119]
	v_mfma_f32_16x16x128_f8f6f4 v[120:123], v[10:17], v[204:211], v[120:123]
	v_mfma_f32_16x16x128_f8f6f4 v[112:115], v[10:17], v[212:219], v[112:115]
	v_mfma_f32_16x16x128_f8f6f4 v[108:111], v[2:9], v[212:219], v[108:111]
	v_mfma_f32_16x16x128_f8f6f4 v[100:103], v[2:9], v[222:229], v[100:103]
	s_barrier
	s_setprio 3
	v_mfma_f32_16x16x128_f8f6f4 v[104:107], v[10:17], v[222:229], v[104:107]
	s_setprio 0
	s_add_i32 s50, s50, s82
	s_mov_b64 s[26:27], 0x180
	s_add_i32 s51, s50, 0x2000
	v_lshl_add_u64 v[194:195], v[194:195], 0, s[26:27]
	s_mov_b32 m0, s50
	s_add_u32 s30, s30, 0x20180
	ds_read_b128 v[178:181], v169 offset:49152
	ds_read_b128 v[182:185], v169 offset:50176
	ds_read_b128 v[204:207], v169 offset:51200
	ds_read_b128 v[208:211], v169 offset:52224
	ds_read_b128 v[212:215], v169 offset:53248
	ds_read_b128 v[216:219], v169 offset:54272
	ds_read_b128 v[222:225], v169 offset:55296
	ds_read_b128 v[226:229], v169 offset:56320
	global_load_lds_dwordx4 v[194:195], off
	v_lshl_add_u64 v[194:195], v[196:197], 0, s[26:27]
	s_mov_b32 m0, s51
	s_addc_u32 s31, s31, 0
	s_add_i32 s64, s64, s82
	global_load_lds_dwordx4 v[194:195], off
	v_lshl_add_u64 v[194:195], s[30:31], 0, v[170:171]
	s_mov_b32 m0, s64
	s_add_i32 s63, s64, 0x2000
	global_load_lds_dwordx4 v[194:195], off
	v_lshl_add_u64 v[194:195], s[30:31], 0, v[172:173]
	s_mov_b32 m0, s63
	v_readlane_b32 s26, v253, 39
	global_load_lds_dwordx4 v[194:195], off
	s_mov_b32 m0, s90
	v_readlane_b32 s27, v253, 40
	s_nop 4
	global_load_lds_dwordx4 v34, s[26:27]
	s_mov_b32 m0, s91
	s_nop 0
	global_load_lds_dwordx4 v192, s[26:27]
	s_waitcnt vmcnt(8)
	s_waitcnt lgkmcnt(0)
	s_barrier
	s_setprio 1
	s_waitcnt lgkmcnt(0)
	v_mfma_f32_16x16x128_f8f6f4 v[96:99], v[26:33], v[178:185], v[96:99]
	v_mfma_f32_16x16x128_f8f6f4 v[92:95], v[18:25], v[178:185], v[92:95]
	v_mfma_f32_16x16x128_f8f6f4 v[84:87], v[18:25], v[204:211], v[84:87]
	v_mfma_f32_16x16x128_f8f6f4 v[88:91], v[26:33], v[204:211], v[88:91]
	v_mfma_f32_16x16x128_f8f6f4 v[80:83], v[26:33], v[212:219], v[80:83]
	v_mfma_f32_16x16x128_f8f6f4 v[76:79], v[18:25], v[212:219], v[76:79]
	v_mfma_f32_16x16x128_f8f6f4 v[68:71], v[18:25], v[222:229], v[68:71]
	v_mfma_f32_16x16x128_f8f6f4 v[72:75], v[26:33], v[222:229], v[72:75]
	s_setprio 0
	s_setprio 1
	v_mfma_f32_16x16x128_f8f6f4 v[64:67], v[10:17], v[178:185], v[64:67]
	v_mfma_f32_16x16x128_f8f6f4 v[60:63], v[2:9], v[178:185], v[60:63]
	v_mfma_f32_16x16x128_f8f6f4 v[52:55], v[2:9], v[204:211], v[52:55]
	v_mfma_f32_16x16x128_f8f6f4 v[56:59], v[10:17], v[204:211], v[56:59]
	v_mfma_f32_16x16x128_f8f6f4 v[48:51], v[10:17], v[212:219], v[48:51]
	v_mfma_f32_16x16x128_f8f6f4 v[44:47], v[2:9], v[212:219], v[44:47]
	v_mfma_f32_16x16x128_f8f6f4 v[36:39], v[2:9], v[222:229], v[36:39]
	s_barrier
	s_setprio 3
	v_mfma_f32_16x16x128_f8f6f4 v[40:43], v[10:17], v[222:229], v[40:43]
	s_setprio 0
	v_lshl_add_u64 v[18:19], s[26:27], 0, v[174:175]
	v_lshl_add_u64 v[20:21], s[26:27], 0, v[190:191]
	s_mov_b32 s75, 0
	s_mov_b64 s[30:31], 0
	s_branch .LBB0_955
.LBB0_954:
	ds_read_b128 v[178:181], v200
	ds_read_b128 v[182:185], v200 offset:1024
	ds_read_b128 v[204:207], v200 offset:2048
	ds_read_b128 v[208:211], v200 offset:3072
	ds_read_b128 v[10:13], v199
	ds_read_b128 v[14:17], v199 offset:1024
	ds_read_b128 v[2:5], v199 offset:2048
	ds_read_b128 v[6:9], v199 offset:3072
	s_add_u32 s14, s30, 0x200
	s_addc_u32 vcc_lo, s31, 0
	s_and_b64 s[48:49], s[46:47], exec
	s_cselect_b32 s14, 0, s14
	s_cselect_b32 s49, 0, vcc_lo
	s_add_u32 s48, s20, s14
	s_addc_u32 s49, s21, s49
	s_add_u32 s14, s95, s30
	s_addc_u32 vcc_lo, s96, s31
	s_and_b64 s[46:47], s[46:47], exec
	s_cselect_b32 s47, s43, vcc_lo
	s_cselect_b32 s46, s42, s14
	s_mov_b32 m0, s83
	v_lshl_add_u64 v[30:31], v[20:21], 0, s[30:31]
	ds_read_b128 v[22:25], v169
	ds_read_b128 v[26:29], v169 offset:1024
	ds_read_b128 v[212:215], v169 offset:2048
	ds_read_b128 v[216:219], v169 offset:3072
	ds_read_b128 v[222:225], v169 offset:4096
	ds_read_b128 v[226:229], v169 offset:5120
	ds_read_b128 v[230:233], v169 offset:6144
	ds_read_b128 v[234:237], v169 offset:7168
	global_load_lds_dwordx4 v[30:31], off
	v_lshl_add_u64 v[30:31], v[18:19], 0, s[30:31]
	s_mov_b32 m0, s53
	s_nop 0
	global_load_lds_dwordx4 v[30:31], off
	s_waitcnt vmcnt(8)
	s_waitcnt lgkmcnt(0)
	s_barrier
	s_setprio 1
	s_waitcnt lgkmcnt(0)
	v_mfma_f32_16x16x128_f8f6f4 v[160:163], v[178:185], v[22:29], v[160:163]
	v_mfma_f32_16x16x128_f8f6f4 v[156:159], v[204:211], v[22:29], v[156:159]
	v_mfma_f32_16x16x128_f8f6f4 v[148:151], v[204:211], v[212:219], v[148:151]
	v_mfma_f32_16x16x128_f8f6f4 v[152:155], v[178:185], v[212:219], v[152:155]
	v_mfma_f32_16x16x128_f8f6f4 v[144:147], v[178:185], v[222:229], v[144:147]
	v_mfma_f32_16x16x128_f8f6f4 v[140:143], v[204:211], v[222:229], v[140:143]
	v_mfma_f32_16x16x128_f8f6f4 v[132:135], v[204:211], v[230:237], v[132:135]
	v_mfma_f32_16x16x128_f8f6f4 v[136:139], v[178:185], v[230:237], v[136:139]
	s_setprio 0
	s_setprio 1
	v_mfma_f32_16x16x128_f8f6f4 v[128:131], v[10:17], v[22:29], v[128:131]
	v_mfma_f32_16x16x128_f8f6f4 v[124:127], v[2:9], v[22:29], v[124:127]
	v_mfma_f32_16x16x128_f8f6f4 v[116:119], v[2:9], v[212:219], v[116:119]
	v_mfma_f32_16x16x128_f8f6f4 v[120:123], v[10:17], v[212:219], v[120:123]
	v_mfma_f32_16x16x128_f8f6f4 v[112:115], v[10:17], v[222:229], v[112:115]
	v_mfma_f32_16x16x128_f8f6f4 v[108:111], v[2:9], v[222:229], v[108:111]
	v_mfma_f32_16x16x128_f8f6f4 v[100:103], v[2:9], v[230:237], v[100:103]
	s_barrier
	s_setprio 3
	v_mfma_f32_16x16x128_f8f6f4 v[104:107], v[10:17], v[230:237], v[104:107]
	s_setprio 0
	s_mov_b32 m0, s67
	v_lshl_add_u64 v[22:23], s[46:47], 0, v[170:171]
	s_add_u32 vcc_lo, s46, 0x20000
	ds_read_b128 v[212:215], v169 offset:16384
	ds_read_b128 v[216:219], v169 offset:17408
	ds_read_b128 v[222:225], v169 offset:18432
	ds_read_b128 v[226:229], v169 offset:19456
	ds_read_b128 v[230:233], v169 offset:20480
	ds_read_b128 v[234:237], v169 offset:21504
	ds_read_b128 v[238:241], v169 offset:22528
	ds_read_b128 v[242:245], v169 offset:23552
	global_load_lds_dwordx4 v[22:23], off
	v_lshl_add_u64 v[24:25], s[46:47], 0, v[172:173]
	s_mov_b32 m0, s55
	s_addc_u32 vcc_hi, s47, 0
	global_load_lds_dwordx4 v[24:25], off
	v_lshl_add_u64 v[26:27], vcc, 0, v[170:171]
	s_mov_b32 m0, s65
	v_mov_b32_e32 v193, v35
	global_load_lds_dwordx4 v[26:27], off
	v_lshl_add_u64 v[26:27], vcc, 0, v[172:173]
	s_mov_b32 m0, s54
	v_lshl_add_u64 v[28:29], s[48:49], 0, v[34:35]
	global_load_lds_dwordx4 v[26:27], off
	s_mov_b32 m0, s52
	v_lshl_add_u64 v[26:27], s[48:49], 0, v[192:193]
	global_load_lds_dwordx4 v34, s[48:49]
	s_mov_b32 m0, s84
	s_nop 0
	global_load_lds_dwordx4 v192, s[48:49]
	s_waitcnt vmcnt(8)
	s_waitcnt lgkmcnt(0)
	s_barrier
	s_setprio 1
	s_waitcnt lgkmcnt(0)
	v_mfma_f32_16x16x128_f8f6f4 v[96:99], v[178:185], v[212:219], v[96:99]
	v_mfma_f32_16x16x128_f8f6f4 v[92:95], v[204:211], v[212:219], v[92:95]
	v_mfma_f32_16x16x128_f8f6f4 v[84:87], v[204:211], v[222:229], v[84:87]
	v_mfma_f32_16x16x128_f8f6f4 v[88:91], v[178:185], v[222:229], v[88:91]
	v_mfma_f32_16x16x128_f8f6f4 v[80:83], v[178:185], v[230:237], v[80:83]
	v_mfma_f32_16x16x128_f8f6f4 v[76:79], v[204:211], v[230:237], v[76:79]
	v_mfma_f32_16x16x128_f8f6f4 v[68:71], v[204:211], v[238:245], v[68:71]
	v_mfma_f32_16x16x128_f8f6f4 v[72:75], v[178:185], v[238:245], v[72:75]
	s_setprio 0
	s_setprio 1
	v_mfma_f32_16x16x128_f8f6f4 v[64:67], v[10:17], v[212:219], v[64:67]
	v_mfma_f32_16x16x128_f8f6f4 v[60:63], v[2:9], v[212:219], v[60:63]
	v_mfma_f32_16x16x128_f8f6f4 v[52:55], v[2:9], v[222:229], v[52:55]
	v_mfma_f32_16x16x128_f8f6f4 v[56:59], v[10:17], v[222:229], v[56:59]
	v_mfma_f32_16x16x128_f8f6f4 v[48:51], v[10:17], v[230:237], v[48:51]
	v_mfma_f32_16x16x128_f8f6f4 v[44:47], v[2:9], v[230:237], v[44:47]
	v_mfma_f32_16x16x128_f8f6f4 v[36:39], v[2:9], v[238:245], v[36:39]
	s_barrier
	s_setprio 3
	v_mfma_f32_16x16x128_f8f6f4 v[40:43], v[10:17], v[238:245], v[40:43]
	s_setprio 0
	ds_read_b128 v[178:181], v201
	ds_read_b128 v[182:185], v201 offset:1024
	ds_read_b128 v[204:207], v201 offset:2048
	ds_read_b128 v[208:211], v201 offset:3072
	ds_read_b128 v[10:13], v202
	ds_read_b128 v[14:17], v202 offset:1024
	ds_read_b128 v[2:5], v202 offset:2048
	ds_read_b128 v[6:9], v202 offset:3072
	s_mov_b32 m0, s85
	ds_read_b128 v[212:215], v169 offset:32768
	ds_read_b128 v[216:219], v169 offset:33792
	ds_read_b128 v[222:225], v169 offset:34816
	ds_read_b128 v[226:229], v169 offset:35840
	ds_read_b128 v[230:233], v169 offset:36864
	ds_read_b128 v[234:237], v169 offset:37888
	ds_read_b128 v[238:241], v169 offset:38912
	ds_read_b128 v[242:245], v169 offset:39936
	global_load_lds_dwordx4 v189, s[48:49]
	s_mov_b32 m0, s86
	s_nop 0
	global_load_lds_dwordx4 v198, s[48:49]
	s_waitcnt vmcnt(8)
	s_waitcnt lgkmcnt(0)
	s_barrier
	s_setprio 1
	s_waitcnt lgkmcnt(0)
	v_mfma_f32_16x16x128_f8f6f4 v[160:163], v[178:185], v[212:219], v[160:163]
	v_mfma_f32_16x16x128_f8f6f4 v[156:159], v[204:211], v[212:219], v[156:159]
	v_mfma_f32_16x16x128_f8f6f4 v[148:151], v[204:211], v[222:229], v[148:151]
	v_mfma_f32_16x16x128_f8f6f4 v[152:155], v[178:185], v[222:229], v[152:155]
	v_mfma_f32_16x16x128_f8f6f4 v[144:147], v[178:185], v[230:237], v[144:147]
	v_mfma_f32_16x16x128_f8f6f4 v[140:143], v[204:211], v[230:237], v[140:143]
	v_mfma_f32_16x16x128_f8f6f4 v[132:135], v[204:211], v[238:245], v[132:135]
	v_mfma_f32_16x16x128_f8f6f4 v[136:139], v[178:185], v[238:245], v[136:139]
	s_setprio 0
	s_setprio 1
	v_mfma_f32_16x16x128_f8f6f4 v[128:131], v[10:17], v[212:219], v[128:131]
	v_mfma_f32_16x16x128_f8f6f4 v[124:127], v[2:9], v[212:219], v[124:127]
	v_mfma_f32_16x16x128_f8f6f4 v[116:119], v[2:9], v[222:229], v[116:119]
	v_mfma_f32_16x16x128_f8f6f4 v[120:123], v[10:17], v[222:229], v[120:123]
	v_mfma_f32_16x16x128_f8f6f4 v[112:115], v[10:17], v[230:237], v[112:115]
	v_mfma_f32_16x16x128_f8f6f4 v[108:111], v[2:9], v[230:237], v[108:111]
	v_mfma_f32_16x16x128_f8f6f4 v[100:103], v[2:9], v[238:245], v[100:103]
	s_barrier
	s_setprio 3
	v_mfma_f32_16x16x128_f8f6f4 v[104:107], v[10:17], v[238:245], v[104:107]
	s_setprio 0
	s_mov_b32 m0, s50
	v_lshl_add_u64 v[22:23], v[22:23], 0, s[18:19]
	s_add_u32 s46, s46, 0x20080
	ds_read_b128 v[212:215], v169 offset:49152
	ds_read_b128 v[216:219], v169 offset:50176
	ds_read_b128 v[222:225], v169 offset:51200
	ds_read_b128 v[226:229], v169 offset:52224
	ds_read_b128 v[230:233], v169 offset:53248
	ds_read_b128 v[234:237], v169 offset:54272
	ds_read_b128 v[238:241], v169 offset:55296
	ds_read_b128 v[242:245], v169 offset:56320
	global_load_lds_dwordx4 v[22:23], off
	v_lshl_add_u64 v[22:23], v[24:25], 0, s[18:19]
	s_mov_b32 m0, s51
	s_addc_u32 s47, s47, 0
	global_load_lds_dwordx4 v[22:23], off
	v_lshl_add_u64 v[22:23], s[46:47], 0, v[170:171]
	s_mov_b32 m0, s64
	s_nop 0
	global_load_lds_dwordx4 v[22:23], off
	v_lshl_add_u64 v[22:23], s[46:47], 0, v[172:173]
	s_mov_b32 m0, s63
	s_nop 0
	global_load_lds_dwordx4 v[22:23], off
	v_lshl_add_u64 v[22:23], v[28:29], 0, s[18:19]
	s_mov_b32 m0, s90
	s_nop 0
	global_load_lds_dwordx4 v[22:23], off
	v_lshl_add_u64 v[22:23], v[26:27], 0, s[18:19]
	s_mov_b32 m0, s91
	s_nop 0
	global_load_lds_dwordx4 v[22:23], off
	s_waitcnt vmcnt(8)
	s_waitcnt lgkmcnt(0)
	s_barrier
	s_setprio 1
	s_waitcnt lgkmcnt(0)
	v_mfma_f32_16x16x128_f8f6f4 v[96:99], v[178:185], v[212:219], v[96:99]
	v_mfma_f32_16x16x128_f8f6f4 v[92:95], v[204:211], v[212:219], v[92:95]
	v_mfma_f32_16x16x128_f8f6f4 v[84:87], v[204:211], v[222:229], v[84:87]
	v_mfma_f32_16x16x128_f8f6f4 v[88:91], v[178:185], v[222:229], v[88:91]
	v_mfma_f32_16x16x128_f8f6f4 v[80:83], v[178:185], v[230:237], v[80:83]
	v_mfma_f32_16x16x128_f8f6f4 v[76:79], v[204:211], v[230:237], v[76:79]
	v_mfma_f32_16x16x128_f8f6f4 v[68:71], v[204:211], v[238:245], v[68:71]
	v_mfma_f32_16x16x128_f8f6f4 v[72:75], v[178:185], v[238:245], v[72:75]
	s_setprio 0
	s_setprio 1
	v_mfma_f32_16x16x128_f8f6f4 v[64:67], v[10:17], v[212:219], v[64:67]
	v_mfma_f32_16x16x128_f8f6f4 v[60:63], v[2:9], v[212:219], v[60:63]
	v_mfma_f32_16x16x128_f8f6f4 v[52:55], v[2:9], v[222:229], v[52:55]
	v_mfma_f32_16x16x128_f8f6f4 v[56:59], v[10:17], v[222:229], v[56:59]
	v_mfma_f32_16x16x128_f8f6f4 v[48:51], v[10:17], v[230:237], v[48:51]
	v_mfma_f32_16x16x128_f8f6f4 v[44:47], v[2:9], v[230:237], v[44:47]
	v_mfma_f32_16x16x128_f8f6f4 v[36:39], v[2:9], v[238:245], v[36:39]
	s_barrier
	s_setprio 3
	v_mfma_f32_16x16x128_f8f6f4 v[40:43], v[10:17], v[238:245], v[40:43]
	s_setprio 0
	s_add_i32 s75, s75, 2
	s_add_u32 s30, s30, 0x100
	s_addc_u32 s31, s31, 0
	s_cmp_gt_u32 s75, 5
	s_cbranch_scc1 .LBB0_957

.LBB0_1086:
	s_lshl_b32 s10, s51, 18
	s_add_u32 s10, s20, s10
	s_addc_u32 s11, s21, 0
	s_and_b64 s[16:17], s[4:5], exec
	s_cselect_b32 s54, s11, s31
	s_cselect_b32 s55, s10, s30
	s_lshl_b32 s14, s50, 18
	s_add_u32 s16, s15, s14
	s_addc_u32 s17, s26, 0
	s_and_b64 s[36:37], s[4:5], exec
	s_cselect_b32 s56, s17, s23
	s_cselect_b32 s57, s16, s22
	s_add_i32 s60, 0, 0x10000
	s_add_i32 s62, 0, 0x14000
	v_add_u32_e32 v198, s60, v196
	v_add_u32_e32 v199, s62, v196
	ds_read_b128 v[26:29], v198
	ds_read_b128 v[30:33], v198 offset:1024
	ds_read_b128 v[18:21], v198 offset:2048
	ds_read_b128 v[22:25], v198 offset:3072
	ds_read_b128 v[10:13], v199
	ds_read_b128 v[14:17], v199 offset:1024
	ds_read_b128 v[2:5], v199 offset:2048
	ds_read_b128 v[6:9], v199 offset:3072
	s_add_u32 s36, s30, 0x20080
	s_addc_u32 s37, s31, 0
	s_add_i32 s58, s41, 0xc000
	v_lshl_add_u64 v[174:175], s[36:37], 0, v[168:169]
	s_mov_b32 m0, s58
	s_add_i32 s59, s41, 0xe000
	ds_read_b128 v[200:203], v197
	ds_read_b128 v[204:207], v197 offset:1024
	ds_read_b128 v[222:225], v197 offset:2048
	ds_read_b128 v[226:229], v197 offset:3072
	ds_read_b128 v[230:233], v197 offset:4096
	ds_read_b128 v[234:237], v197 offset:5120
	ds_read_b128 v[238:241], v197 offset:6144
	ds_read_b128 v[242:245], v197 offset:7168
	global_load_lds_dwordx4 v[174:175], off
	v_lshl_add_u64 v[174:175], s[36:37], 0, v[166:167]
	s_mov_b32 m0, s59
	s_nop 0
	global_load_lds_dwordx4 v[174:175], off
	s_waitcnt vmcnt(8)
	s_waitcnt lgkmcnt(0)
	s_barrier
	s_setprio 1
	s_waitcnt lgkmcnt(0)
	v_mfma_f32_16x16x128_f8f6f4 v[160:163], v[26:33], v[200:207], 0
	v_mfma_f32_16x16x128_f8f6f4 v[156:159], v[18:25], v[200:207], 0
	v_mfma_f32_16x16x128_f8f6f4 v[148:151], v[18:25], v[222:229], 0
	v_mfma_f32_16x16x128_f8f6f4 v[152:155], v[26:33], v[222:229], 0
	v_mfma_f32_16x16x128_f8f6f4 v[144:147], v[26:33], v[230:237], 0
	v_mfma_f32_16x16x128_f8f6f4 v[140:143], v[18:25], v[230:237], 0
	v_mfma_f32_16x16x128_f8f6f4 v[132:135], v[18:25], v[238:245], 0
	v_mfma_f32_16x16x128_f8f6f4 v[136:139], v[26:33], v[238:245], 0
	s_setprio 0
	s_setprio 1
	v_mfma_f32_16x16x128_f8f6f4 v[128:131], v[10:17], v[200:207], 0
	v_mfma_f32_16x16x128_f8f6f4 v[124:127], v[2:9], v[200:207], 0
	v_mfma_f32_16x16x128_f8f6f4 v[116:119], v[2:9], v[222:229], 0
	v_mfma_f32_16x16x128_f8f6f4 v[120:123], v[10:17], v[222:229], 0
	v_mfma_f32_16x16x128_f8f6f4 v[112:115], v[10:17], v[230:237], 0
	v_mfma_f32_16x16x128_f8f6f4 v[108:111], v[2:9], v[230:237], 0
	v_mfma_f32_16x16x128_f8f6f4 v[100:103], v[2:9], v[238:245], 0
	s_barrier
	s_setprio 3
	v_mfma_f32_16x16x128_f8f6f4 v[104:107], v[10:17], v[238:245], 0
	s_setprio 0
	s_add_i32 s60, s60, s40
	v_lshl_add_u64 v[174:175], s[22:23], 0, v[34:35]
	s_add_i32 s61, s60, 0x2000
	v_lshl_add_u64 v[178:179], v[174:175], 0, s[28:29]
	s_mov_b32 m0, s60
	v_lshl_add_u64 v[190:191], s[22:23], 0, v[164:165]
	s_add_u32 s36, s22, 0x20100
	ds_read_b128 v[200:203], v197 offset:16384
	ds_read_b128 v[204:207], v197 offset:17408
	ds_read_b128 v[222:225], v197 offset:18432
	ds_read_b128 v[226:229], v197 offset:19456
	ds_read_b128 v[230:233], v197 offset:20480
	ds_read_b128 v[234:237], v197 offset:21504
	ds_read_b128 v[238:241], v197 offset:22528
	ds_read_b128 v[242:245], v197 offset:23552
	global_load_lds_dwordx4 v[178:179], off
	v_lshl_add_u64 v[178:179], v[190:191], 0, s[28:29]
	s_mov_b32 m0, s61
	s_addc_u32 s37, s23, 0
	s_add_i32 s62, s62, s40
	global_load_lds_dwordx4 v[178:179], off
	v_lshl_add_u64 v[178:179], s[36:37], 0, v[34:35]
	s_mov_b32 m0, s62
	s_add_i32 s63, s62, 0x2000
	global_load_lds_dwordx4 v[178:179], off
	v_lshl_add_u64 v[178:179], s[36:37], 0, v[164:165]
	s_mov_b32 m0, s63
	v_lshl_add_u64 v[192:193], s[30:31], 0, v[168:169]
	global_load_lds_dwordx4 v[178:179], off
	v_lshl_add_u64 v[178:179], v[192:193], 0, s[28:29]
	s_mov_b32 m0, s41
	v_lshl_add_u64 v[194:195], s[30:31], 0, v[166:167]
	global_load_lds_dwordx4 v[178:179], off
	v_lshl_add_u64 v[178:179], v[194:195], 0, s[28:29]
	s_mov_b32 m0, s42
	s_nop 0
	global_load_lds_dwordx4 v[178:179], off
	s_waitcnt vmcnt(8)
	s_waitcnt lgkmcnt(0)
	s_barrier
	s_setprio 1
	s_waitcnt lgkmcnt(0)
	v_mfma_f32_16x16x128_f8f6f4 v[96:99], v[26:33], v[200:207], 0
	v_mfma_f32_16x16x128_f8f6f4 v[92:95], v[18:25], v[200:207], 0
	v_mfma_f32_16x16x128_f8f6f4 v[84:87], v[18:25], v[222:229], 0
	v_mfma_f32_16x16x128_f8f6f4 v[88:91], v[26:33], v[222:229], 0
	v_mfma_f32_16x16x128_f8f6f4 v[80:83], v[26:33], v[230:237], 0
	v_mfma_f32_16x16x128_f8f6f4 v[76:79], v[18:25], v[230:237], 0
	v_mfma_f32_16x16x128_f8f6f4 v[68:71], v[18:25], v[238:245], 0
	v_mfma_f32_16x16x128_f8f6f4 v[72:75], v[26:33], v[238:245], 0
	s_setprio 0
	s_setprio 1
	v_mfma_f32_16x16x128_f8f6f4 v[64:67], v[10:17], v[200:207], 0
	v_mfma_f32_16x16x128_f8f6f4 v[60:63], v[2:9], v[200:207], 0
	v_mfma_f32_16x16x128_f8f6f4 v[52:55], v[2:9], v[222:229], 0
	v_mfma_f32_16x16x128_f8f6f4 v[56:59], v[10:17], v[222:229], 0
	v_mfma_f32_16x16x128_f8f6f4 v[48:51], v[10:17], v[230:237], 0
	v_mfma_f32_16x16x128_f8f6f4 v[44:47], v[2:9], v[230:237], 0
	v_mfma_f32_16x16x128_f8f6f4 v[36:39], v[2:9], v[238:245], 0
	s_barrier
	s_setprio 3
	v_mfma_f32_16x16x128_f8f6f4 v[40:43], v[10:17], v[238:245], 0
	s_setprio 0
	s_add_i32 s64, 0, 0x18000
	s_add_i32 s66, 0, 0x1c000
	v_add_u32_e32 v200, s64, v196
	v_add_u32_e32 v201, s66, v196
	ds_read_b128 v[26:29], v200
	ds_read_b128 v[30:33], v200 offset:1024
	ds_read_b128 v[18:21], v200 offset:2048
	ds_read_b128 v[22:25], v200 offset:3072
	ds_read_b128 v[10:13], v201
	ds_read_b128 v[14:17], v201 offset:1024
	ds_read_b128 v[2:5], v201 offset:2048
	ds_read_b128 v[6:9], v201 offset:3072
	s_add_u32 s36, s30, 0x20100
	s_addc_u32 s37, s31, 0
	s_mov_b32 m0, s43
	v_lshl_add_u64 v[178:179], s[36:37], 0, v[168:169]
	ds_read_b128 v[202:205], v197 offset:32768
	ds_read_b128 v[206:209], v197 offset:33792
	ds_read_b128 v[222:225], v197 offset:34816
	ds_read_b128 v[226:229], v197 offset:35840
	ds_read_b128 v[230:233], v197 offset:36864
	ds_read_b128 v[234:237], v197 offset:37888
	ds_read_b128 v[238:241], v197 offset:38912
	ds_read_b128 v[242:245], v197 offset:39936
	global_load_lds_dwordx4 v[178:179], off
	v_lshl_add_u64 v[178:179], s[36:37], 0, v[166:167]
	s_mov_b32 m0, s44
	s_nop 0
	global_load_lds_dwordx4 v[178:179], off
	s_waitcnt vmcnt(8)
	s_waitcnt lgkmcnt(0)
	s_barrier
	s_setprio 1
	s_waitcnt lgkmcnt(0)
	v_mfma_f32_16x16x128_f8f6f4 v[160:163], v[26:33], v[202:209], v[160:163]
	v_mfma_f32_16x16x128_f8f6f4 v[156:159], v[18:25], v[202:209], v[156:159]
	v_mfma_f32_16x16x128_f8f6f4 v[148:151], v[18:25], v[222:229], v[148:151]
	v_mfma_f32_16x16x128_f8f6f4 v[152:155], v[26:33], v[222:229], v[152:155]
	v_mfma_f32_16x16x128_f8f6f4 v[144:147], v[26:33], v[230:237], v[144:147]
	v_mfma_f32_16x16x128_f8f6f4 v[140:143], v[18:25], v[230:237], v[140:143]
	v_mfma_f32_16x16x128_f8f6f4 v[132:135], v[18:25], v[238:245], v[132:135]
	v_mfma_f32_16x16x128_f8f6f4 v[136:139], v[26:33], v[238:245], v[136:139]
	s_setprio 0
	s_setprio 1
	v_mfma_f32_16x16x128_f8f6f4 v[128:131], v[10:17], v[202:209], v[128:131]
	v_mfma_f32_16x16x128_f8f6f4 v[124:127], v[2:9], v[202:209], v[124:127]
	v_mfma_f32_16x16x128_f8f6f4 v[116:119], v[2:9], v[222:229], v[116:119]
	v_mfma_f32_16x16x128_f8f6f4 v[120:123], v[10:17], v[222:229], v[120:123]
	v_mfma_f32_16x16x128_f8f6f4 v[112:115], v[10:17], v[230:237], v[112:115]
	v_mfma_f32_16x16x128_f8f6f4 v[108:111], v[2:9], v[230:237], v[108:111]
	v_mfma_f32_16x16x128_f8f6f4 v[100:103], v[2:9], v[238:245], v[100:103]
	s_barrier
	s_setprio 3
	v_mfma_f32_16x16x128_f8f6f4 v[104:107], v[10:17], v[238:245], v[104:107]
	s_setprio 0
	s_add_i32 s64, s64, s40
	s_mov_b64 s[24:25], 0x180
	s_add_i32 s65, s64, 0x2000
	v_lshl_add_u64 v[174:175], v[174:175], 0, s[24:25]
	s_mov_b32 m0, s64
	s_add_u32 s36, s22, 0x20180
	ds_read_b128 v[202:205], v197 offset:49152
	ds_read_b128 v[206:209], v197 offset:50176
	ds_read_b128 v[222:225], v197 offset:51200
	ds_read_b128 v[226:229], v197 offset:52224
	ds_read_b128 v[230:233], v197 offset:53248
	ds_read_b128 v[234:237], v197 offset:54272
	ds_read_b128 v[238:241], v197 offset:55296
	ds_read_b128 v[242:245], v197 offset:56320
	global_load_lds_dwordx4 v[174:175], off
	v_lshl_add_u64 v[174:175], v[190:191], 0, s[24:25]
	s_mov_b32 m0, s65
	s_addc_u32 s37, s23, 0
	s_add_i32 s66, s66, s40
	global_load_lds_dwordx4 v[174:175], off
	v_lshl_add_u64 v[174:175], s[36:37], 0, v[34:35]
	s_mov_b32 m0, s66
	s_add_i32 s67, s66, 0x2000
	global_load_lds_dwordx4 v[174:175], off
	v_lshl_add_u64 v[174:175], s[36:37], 0, v[164:165]
	s_mov_b32 m0, s67
	s_nop 0
	global_load_lds_dwordx4 v[174:175], off
	v_lshl_add_u64 v[174:175], v[192:193], 0, s[24:25]
	s_mov_b32 m0, s47
	s_nop 0
	global_load_lds_dwordx4 v[174:175], off
	v_lshl_add_u64 v[174:175], v[194:195], 0, s[24:25]
	s_mov_b32 m0, s48
	s_nop 0
	global_load_lds_dwordx4 v[174:175], off
	s_waitcnt vmcnt(8)
	s_waitcnt lgkmcnt(0)
	s_barrier
	s_setprio 1
	s_waitcnt lgkmcnt(0)
	v_mfma_f32_16x16x128_f8f6f4 v[96:99], v[26:33], v[202:209], v[96:99]
	v_mfma_f32_16x16x128_f8f6f4 v[92:95], v[18:25], v[202:209], v[92:95]
	v_mfma_f32_16x16x128_f8f6f4 v[84:87], v[18:25], v[222:229], v[84:87]
	v_mfma_f32_16x16x128_f8f6f4 v[88:91], v[26:33], v[222:229], v[88:91]
	v_mfma_f32_16x16x128_f8f6f4 v[80:83], v[26:33], v[230:237], v[80:83]
	v_mfma_f32_16x16x128_f8f6f4 v[76:79], v[18:25], v[230:237], v[76:79]
	v_mfma_f32_16x16x128_f8f6f4 v[68:71], v[18:25], v[238:245], v[68:71]
	v_mfma_f32_16x16x128_f8f6f4 v[72:75], v[26:33], v[238:245], v[72:75]
	s_setprio 0
	s_setprio 1
	v_mfma_f32_16x16x128_f8f6f4 v[64:67], v[10:17], v[202:209], v[64:67]
	v_mfma_f32_16x16x128_f8f6f4 v[60:63], v[2:9], v[202:209], v[60:63]
	v_mfma_f32_16x16x128_f8f6f4 v[52:55], v[2:9], v[222:229], v[52:55]
	v_mfma_f32_16x16x128_f8f6f4 v[56:59], v[10:17], v[222:229], v[56:59]
	v_mfma_f32_16x16x128_f8f6f4 v[48:51], v[10:17], v[230:237], v[48:51]
	v_mfma_f32_16x16x128_f8f6f4 v[44:47], v[2:9], v[230:237], v[44:47]
	v_mfma_f32_16x16x128_f8f6f4 v[36:39], v[2:9], v[238:245], v[36:39]
	s_barrier
	s_setprio 3
	v_mfma_f32_16x16x128_f8f6f4 v[40:43], v[10:17], v[238:245], v[40:43]
	s_setprio 0
	s_add_u32 s30, s30, 0x20180
	s_addc_u32 s31, s31, 0
	s_add_u32 s68, s22, 0x200
	s_addc_u32 s69, s23, 0
	s_mov_b32 s70, 0
.LBB0_1087:
	ds_read_b128 v[2:5], v198
	ds_read_b128 v[6:9], v198 offset:1024
	ds_read_b128 v[10:13], v198 offset:2048
	ds_read_b128 v[14:17], v198 offset:3072
	ds_read_b128 v[18:21], v199
	ds_read_b128 v[22:25], v199 offset:1024
	ds_read_b128 v[26:29], v199 offset:2048
	ds_read_b128 v[30:33], v199 offset:3072
	s_add_u32 s14, s30, 0xfffe0080
	s_addc_u32 s22, s31, -1
	s_cmp_eq_u32 s70, 4
	s_cselect_b32 s37, s54, s22
	s_cselect_b32 s36, s55, s14
	s_cselect_b32 s23, s56, s69
	s_cselect_b32 s22, s57, s68
	s_mov_b32 m0, s58
	v_lshl_add_u64 v[174:175], s[30:31], 0, v[170:171]
	ds_read_b128 v[202:205], v197
	ds_read_b128 v[206:209], v197 offset:1024
	ds_read_b128 v[222:225], v197 offset:2048
	ds_read_b128 v[226:229], v197 offset:3072
	ds_read_b128 v[230:233], v197 offset:4096
	ds_read_b128 v[234:237], v197 offset:5120
	ds_read_b128 v[238:241], v197 offset:6144
	ds_read_b128 v[242:245], v197 offset:7168
	global_load_lds_dwordx4 v[174:175], off
	v_lshl_add_u64 v[174:175], s[30:31], 0, v[172:173]
	s_mov_b32 m0, s59
	s_nop 0
	global_load_lds_dwordx4 v[174:175], off
	s_waitcnt vmcnt(8)
	s_waitcnt lgkmcnt(0)
	s_barrier
	s_setprio 1
	s_waitcnt lgkmcnt(0)
	v_mfma_f32_16x16x128_f8f6f4 v[160:163], v[2:9], v[202:209], v[160:163]
	v_mfma_f32_16x16x128_f8f6f4 v[156:159], v[10:17], v[202:209], v[156:159]
	v_mfma_f32_16x16x128_f8f6f4 v[148:151], v[10:17], v[222:229], v[148:151]
	v_mfma_f32_16x16x128_f8f6f4 v[152:155], v[2:9], v[222:229], v[152:155]
	v_mfma_f32_16x16x128_f8f6f4 v[144:147], v[2:9], v[230:237], v[144:147]
	v_mfma_f32_16x16x128_f8f6f4 v[140:143], v[10:17], v[230:237], v[140:143]
	v_mfma_f32_16x16x128_f8f6f4 v[132:135], v[10:17], v[238:245], v[132:135]
	v_mfma_f32_16x16x128_f8f6f4 v[136:139], v[2:9], v[238:245], v[136:139]
	s_setprio 0
	s_setprio 1
	v_mfma_f32_16x16x128_f8f6f4 v[128:131], v[18:25], v[202:209], v[128:131]
	v_mfma_f32_16x16x128_f8f6f4 v[124:127], v[26:33], v[202:209], v[124:127]
	v_mfma_f32_16x16x128_f8f6f4 v[116:119], v[26:33], v[222:229], v[116:119]
	v_mfma_f32_16x16x128_f8f6f4 v[120:123], v[18:25], v[222:229], v[120:123]
	v_mfma_f32_16x16x128_f8f6f4 v[112:115], v[18:25], v[230:237], v[112:115]
	v_mfma_f32_16x16x128_f8f6f4 v[108:111], v[26:33], v[230:237], v[108:111]
	v_mfma_f32_16x16x128_f8f6f4 v[100:103], v[26:33], v[238:245], v[100:103]
	s_barrier
	s_setprio 3
	v_mfma_f32_16x16x128_f8f6f4 v[104:107], v[18:25], v[238:245], v[104:107]
	s_setprio 0
	s_mov_b32 m0, s60
	v_lshl_add_u64 v[174:175], s[22:23], 0, v[34:35]
	s_add_u32 s72, s22, 0x20000
	ds_read_b128 v[202:205], v197 offset:16384
	ds_read_b128 v[206:209], v197 offset:17408
	ds_read_b128 v[222:225], v197 offset:18432
	ds_read_b128 v[226:229], v197 offset:19456
	ds_read_b128 v[230:233], v197 offset:20480
	ds_read_b128 v[234:237], v197 offset:21504
	ds_read_b128 v[238:241], v197 offset:22528
	ds_read_b128 v[242:245], v197 offset:23552
	global_load_lds_dwordx4 v[174:175], off
	v_lshl_add_u64 v[190:191], s[22:23], 0, v[164:165]
	s_mov_b32 m0, s61
	s_addc_u32 s73, s23, 0
	global_load_lds_dwordx4 v[190:191], off
	v_lshl_add_u64 v[178:179], s[72:73], 0, v[34:35]
	s_mov_b32 m0, s62
	v_lshl_add_u64 v[192:193], s[36:37], 0, v[168:169]
	global_load_lds_dwordx4 v[178:179], off
	v_lshl_add_u64 v[178:179], s[72:73], 0, v[164:165]
	s_mov_b32 m0, s63
	v_lshl_add_u64 v[194:195], s[36:37], 0, v[166:167]
	global_load_lds_dwordx4 v[178:179], off
	s_mov_b32 m0, s41
	s_nop 0
	global_load_lds_dwordx4 v[192:193], off
	s_mov_b32 m0, s42
	s_nop 0
	global_load_lds_dwordx4 v[194:195], off
	s_waitcnt vmcnt(8)
	s_waitcnt lgkmcnt(0)
	s_barrier
	s_setprio 1
	s_waitcnt lgkmcnt(0)
	v_mfma_f32_16x16x128_f8f6f4 v[96:99], v[2:9], v[202:209], v[96:99]
	v_mfma_f32_16x16x128_f8f6f4 v[92:95], v[10:17], v[202:209], v[92:95]
	v_mfma_f32_16x16x128_f8f6f4 v[84:87], v[10:17], v[222:229], v[84:87]
	v_mfma_f32_16x16x128_f8f6f4 v[88:91], v[2:9], v[222:229], v[88:91]
	v_mfma_f32_16x16x128_f8f6f4 v[80:83], v[2:9], v[230:237], v[80:83]
	v_mfma_f32_16x16x128_f8f6f4 v[76:79], v[10:17], v[230:237], v[76:79]
	v_mfma_f32_16x16x128_f8f6f4 v[68:71], v[10:17], v[238:245], v[68:71]
	v_mfma_f32_16x16x128_f8f6f4 v[72:75], v[2:9], v[238:245], v[72:75]
	s_setprio 0
	s_setprio 1
	v_mfma_f32_16x16x128_f8f6f4 v[64:67], v[18:25], v[202:209], v[64:67]
	v_mfma_f32_16x16x128_f8f6f4 v[60:63], v[26:33], v[202:209], v[60:63]
	v_mfma_f32_16x16x128_f8f6f4 v[52:55], v[26:33], v[222:229], v[52:55]
	v_mfma_f32_16x16x128_f8f6f4 v[56:59], v[18:25], v[222:229], v[56:59]
	v_mfma_f32_16x16x128_f8f6f4 v[48:51], v[18:25], v[230:237], v[48:51]
	v_mfma_f32_16x16x128_f8f6f4 v[44:47], v[26:33], v[230:237], v[44:47]
	v_mfma_f32_16x16x128_f8f6f4 v[36:39], v[26:33], v[238:245], v[36:39]
	s_barrier
	s_setprio 3
	v_mfma_f32_16x16x128_f8f6f4 v[40:43], v[18:25], v[238:245], v[40:43]
	s_setprio 0
	ds_read_b128 v[26:29], v200
	ds_read_b128 v[30:33], v200 offset:1024
	ds_read_b128 v[18:21], v200 offset:2048
	ds_read_b128 v[22:25], v200 offset:3072
	ds_read_b128 v[10:13], v201
	ds_read_b128 v[14:17], v201 offset:1024
	ds_read_b128 v[2:5], v201 offset:2048
	ds_read_b128 v[6:9], v201 offset:3072
	s_add_u32 s36, s36, 0x20000
	s_addc_u32 s37, s37, 0
	s_mov_b32 m0, s43
	v_lshl_add_u64 v[178:179], s[36:37], 0, v[168:169]
	ds_read_b128 v[202:205], v197 offset:32768
	ds_read_b128 v[206:209], v197 offset:33792
	ds_read_b128 v[222:225], v197 offset:34816
	ds_read_b128 v[226:229], v197 offset:35840
	ds_read_b128 v[230:233], v197 offset:36864
	ds_read_b128 v[234:237], v197 offset:37888
	ds_read_b128 v[238:241], v197 offset:38912
	ds_read_b128 v[242:245], v197 offset:39936
	global_load_lds_dwordx4 v[178:179], off
	v_lshl_add_u64 v[178:179], s[36:37], 0, v[166:167]
	s_mov_b32 m0, s44
	s_nop 0
	global_load_lds_dwordx4 v[178:179], off
	s_waitcnt vmcnt(8)
	s_waitcnt lgkmcnt(0)
	s_barrier
	s_setprio 1
	s_waitcnt lgkmcnt(0)
	v_mfma_f32_16x16x128_f8f6f4 v[160:163], v[26:33], v[202:209], v[160:163]
	v_mfma_f32_16x16x128_f8f6f4 v[156:159], v[18:25], v[202:209], v[156:159]
	v_mfma_f32_16x16x128_f8f6f4 v[148:151], v[18:25], v[222:229], v[148:151]
	v_mfma_f32_16x16x128_f8f6f4 v[152:155], v[26:33], v[222:229], v[152:155]
	v_mfma_f32_16x16x128_f8f6f4 v[144:147], v[26:33], v[230:237], v[144:147]
	v_mfma_f32_16x16x128_f8f6f4 v[140:143], v[18:25], v[230:237], v[140:143]
	v_mfma_f32_16x16x128_f8f6f4 v[132:135], v[18:25], v[238:245], v[132:135]
	v_mfma_f32_16x16x128_f8f6f4 v[136:139], v[26:33], v[238:245], v[136:139]
	s_setprio 0
	s_setprio 1
	v_mfma_f32_16x16x128_f8f6f4 v[128:131], v[10:17], v[202:209], v[128:131]
	v_mfma_f32_16x16x128_f8f6f4 v[124:127], v[2:9], v[202:209], v[124:127]
	v_mfma_f32_16x16x128_f8f6f4 v[116:119], v[2:9], v[222:229], v[116:119]
	v_mfma_f32_16x16x128_f8f6f4 v[120:123], v[10:17], v[222:229], v[120:123]
	v_mfma_f32_16x16x128_f8f6f4 v[112:115], v[10:17], v[230:237], v[112:115]
	v_mfma_f32_16x16x128_f8f6f4 v[108:111], v[2:9], v[230:237], v[108:111]
	v_mfma_f32_16x16x128_f8f6f4 v[100:103], v[2:9], v[238:245], v[100:103]
	s_barrier
	s_setprio 3
	v_mfma_f32_16x16x128_f8f6f4 v[104:107], v[10:17], v[238:245], v[104:107]
	s_setprio 0
	s_mov_b32 m0, s64
	v_lshl_add_u64 v[174:175], v[174:175], 0, s[18:19]
	s_add_u32 s22, s22, 0x20080
	ds_read_b128 v[202:205], v197 offset:49152
	ds_read_b128 v[206:209], v197 offset:50176
	ds_read_b128 v[222:225], v197 offset:51200
	ds_read_b128 v[226:229], v197 offset:52224
	ds_read_b128 v[230:233], v197 offset:53248
	ds_read_b128 v[234:237], v197 offset:54272
	ds_read_b128 v[238:241], v197 offset:55296
	ds_read_b128 v[242:245], v197 offset:56320
	global_load_lds_dwordx4 v[174:175], off
	v_lshl_add_u64 v[174:175], v[190:191], 0, s[18:19]
	s_mov_b32 m0, s65
	s_addc_u32 s23, s23, 0
	global_load_lds_dwordx4 v[174:175], off
	v_lshl_add_u64 v[174:175], s[22:23], 0, v[34:35]
	s_mov_b32 m0, s66
	s_nop 0
	global_load_lds_dwordx4 v[174:175], off
	v_lshl_add_u64 v[174:175], s[22:23], 0, v[164:165]
	s_mov_b32 m0, s67
	s_nop 0
	global_load_lds_dwordx4 v[174:175], off
	v_lshl_add_u64 v[174:175], v[192:193], 0, s[18:19]
	s_mov_b32 m0, s47
	s_nop 0
	global_load_lds_dwordx4 v[174:175], off
	v_lshl_add_u64 v[174:175], v[194:195], 0, s[18:19]
	s_mov_b32 m0, s48
	s_nop 0
	global_load_lds_dwordx4 v[174:175], off
	s_waitcnt vmcnt(8)
	s_waitcnt lgkmcnt(0)
	s_barrier
	s_setprio 1
	s_waitcnt lgkmcnt(0)
	v_mfma_f32_16x16x128_f8f6f4 v[96:99], v[26:33], v[202:209], v[96:99]
	v_mfma_f32_16x16x128_f8f6f4 v[92:95], v[18:25], v[202:209], v[92:95]
	v_mfma_f32_16x16x128_f8f6f4 v[84:87], v[18:25], v[222:229], v[84:87]
	v_mfma_f32_16x16x128_f8f6f4 v[88:91], v[26:33], v[222:229], v[88:91]
	v_mfma_f32_16x16x128_f8f6f4 v[80:83], v[26:33], v[230:237], v[80:83]
	v_mfma_f32_16x16x128_f8f6f4 v[76:79], v[18:25], v[230:237], v[76:79]
	v_mfma_f32_16x16x128_f8f6f4 v[68:71], v[18:25], v[238:245], v[68:71]
	v_mfma_f32_16x16x128_f8f6f4 v[72:75], v[26:33], v[238:245], v[72:75]
	s_setprio 0
	s_setprio 1
	v_mfma_f32_16x16x128_f8f6f4 v[64:67], v[10:17], v[202:209], v[64:67]
	v_mfma_f32_16x16x128_f8f6f4 v[60:63], v[2:9], v[202:209], v[60:63]
	v_mfma_f32_16x16x128_f8f6f4 v[52:55], v[2:9], v[222:229], v[52:55]
	v_mfma_f32_16x16x128_f8f6f4 v[56:59], v[10:17], v[222:229], v[56:59]
	v_mfma_f32_16x16x128_f8f6f4 v[48:51], v[10:17], v[230:237], v[48:51]
	v_mfma_f32_16x16x128_f8f6f4 v[44:47], v[2:9], v[230:237], v[44:47]
	v_mfma_f32_16x16x128_f8f6f4 v[36:39], v[2:9], v[238:245], v[36:39]
	s_barrier
	s_setprio 3
	v_mfma_f32_16x16x128_f8f6f4 v[40:43], v[10:17], v[238:245], v[40:43]
	s_setprio 0
	s_add_i32 s70, s70, 2
	s_add_u32 s30, s30, 0x100
	s_addc_u32 s31, s31, 0
	s_add_u32 s68, s68, 0x100
	s_addc_u32 s69, s69, 0
	s_cmp_gt_u32 s70, 5
	s_cbranch_scc0 .LBB0_1087

.LBB0_1160:
	s_add_u32 s22, s30, 0x100
	s_addc_u32 s23, s31, 0
	s_add_i32 s65, 0, 0x10000
	s_cmp_eq_u32 s64, 18
	s_cselect_b32 s41, s58, s23
	s_cselect_b32 s40, s59, s22
	s_cselect_b32 s37, s60, s63
	s_cselect_b32 s36, s61, s62
	s_add_i32 s66, 0, 0x14000
	v_add_u32_e32 v2, s65, v222
	v_add_u32_e32 v6, s66, v222
	ds_read_b128 v[26:29], v2
	ds_read_b128 v[30:33], v2 offset:1024
	ds_read_b128 v[18:21], v2 offset:2048
	ds_read_b128 v[22:25], v2 offset:3072
	ds_read_b128 v[10:13], v6
	ds_read_b128 v[14:17], v6 offset:1024
	ds_read_b128 v[2:5], v6 offset:2048
	ds_read_b128 v[6:9], v6 offset:3072
	v_lshl_add_u64 v[174:175], s[30:31], 0, v[170:171]
	s_add_i32 m0, s43, 0xc000
	ds_read_b128 v[190:193], v223
	ds_read_b128 v[194:197], v223 offset:1024
	ds_read_b128 v[198:201], v223 offset:2048
	ds_read_b128 v[202:205], v223 offset:3072
	ds_read_b128 v[224:227], v223 offset:4096
	ds_read_b128 v[228:231], v223 offset:5120
	ds_read_b128 v[232:235], v223 offset:6144
	ds_read_b128 v[236:239], v223 offset:7168
	global_load_lds_dwordx4 v[174:175], off
	v_lshl_add_u64 v[174:175], s[30:31], 0, v[172:173]
	s_add_i32 m0, s43, 0xe000
	s_nop 0
	global_load_lds_dwordx4 v[174:175], off
	s_waitcnt vmcnt(8)
	s_waitcnt lgkmcnt(0)
	s_barrier
	s_setprio 1
	s_waitcnt lgkmcnt(0)
	v_mfma_f32_16x16x128_f8f6f4 v[160:163], v[26:33], v[190:197], v[160:163]
	v_mfma_f32_16x16x128_f8f6f4 v[156:159], v[18:25], v[190:197], v[156:159]
	v_mfma_f32_16x16x128_f8f6f4 v[140:143], v[18:25], v[198:205], v[140:143]
	v_mfma_f32_16x16x128_f8f6f4 v[144:147], v[26:33], v[198:205], v[144:147]
	v_mfma_f32_16x16x128_f8f6f4 v[132:135], v[26:33], v[224:231], v[132:135]
	v_mfma_f32_16x16x128_f8f6f4 v[124:127], v[18:25], v[224:231], v[124:127]
	v_mfma_f32_16x16x128_f8f6f4 v[108:111], v[18:25], v[232:239], v[108:111]
	v_mfma_f32_16x16x128_f8f6f4 v[116:119], v[26:33], v[232:239], v[116:119]
	s_setprio 0
	s_setprio 1
	v_mfma_f32_16x16x128_f8f6f4 v[152:155], v[10:17], v[190:197], v[152:155]
	v_mfma_f32_16x16x128_f8f6f4 v[148:151], v[2:9], v[190:197], v[148:151]
	v_mfma_f32_16x16x128_f8f6f4 v[128:131], v[2:9], v[198:205], v[128:131]
	v_mfma_f32_16x16x128_f8f6f4 v[136:139], v[10:17], v[198:205], v[136:139]
	v_mfma_f32_16x16x128_f8f6f4 v[120:123], v[10:17], v[224:231], v[120:123]
	v_mfma_f32_16x16x128_f8f6f4 v[112:115], v[2:9], v[224:231], v[112:115]
	v_mfma_f32_16x16x128_f8f6f4 v[100:103], v[2:9], v[232:239], v[100:103]
	s_barrier
	s_setprio 3
	v_mfma_f32_16x16x128_f8f6f4 v[104:107], v[10:17], v[232:239], v[104:107]
	s_setprio 0
	s_add_i32 s14, s65, s42
	v_lshl_add_u64 v[174:175], s[36:37], 0, v[34:35]
	s_mov_b32 m0, s14
	ds_read_b128 v[196:199], v223 offset:16384
	ds_read_b128 v[200:203], v223 offset:17408
	ds_read_b128 v[204:207], v223 offset:18432
	ds_read_b128 v[208:211], v223 offset:19456
	ds_read_b128 v[224:227], v223 offset:20480
	ds_read_b128 v[228:231], v223 offset:21504
	ds_read_b128 v[232:235], v223 offset:22528
	ds_read_b128 v[236:239], v223 offset:23552
	global_load_lds_dwordx4 v[174:175], off
	s_add_i32 m0, s14, 0x2000
	s_add_u32 s30, s36, 0x58000
	v_lshl_add_u64 v[190:191], s[36:37], 0, v[164:165]
	s_addc_u32 s31, s37, 0
	s_add_i32 s14, s66, s42
	global_load_lds_dwordx4 v[190:191], off
	v_lshl_add_u64 v[178:179], s[30:31], 0, v[34:35]
	s_mov_b32 m0, s14
	v_lshl_add_u64 v[192:193], s[40:41], 0, v[168:169]
	global_load_lds_dwordx4 v[178:179], off
	v_lshl_add_u64 v[178:179], s[30:31], 0, v[164:165]
	s_add_i32 m0, s14, 0x2000
	v_lshl_add_u64 v[194:195], s[40:41], 0, v[166:167]
	global_load_lds_dwordx4 v[178:179], off
	s_mov_b32 m0, s43
	s_nop 0
	global_load_lds_dwordx4 v[192:193], off
	s_mov_b32 m0, s44
	s_nop 0
	global_load_lds_dwordx4 v[194:195], off
	s_waitcnt vmcnt(8)
	s_waitcnt lgkmcnt(0)
	s_barrier
	s_setprio 1
	s_waitcnt lgkmcnt(0)
	v_mfma_f32_16x16x128_f8f6f4 v[96:99], v[26:33], v[196:203], v[96:99]
	v_mfma_f32_16x16x128_f8f6f4 v[92:95], v[18:25], v[196:203], v[92:95]
	v_mfma_f32_16x16x128_f8f6f4 v[76:79], v[18:25], v[204:211], v[76:79]
	v_mfma_f32_16x16x128_f8f6f4 v[84:87], v[26:33], v[204:211], v[84:87]
	v_mfma_f32_16x16x128_f8f6f4 v[68:71], v[26:33], v[224:231], v[68:71]
	v_mfma_f32_16x16x128_f8f6f4 v[60:63], v[18:25], v[224:231], v[60:63]
	v_mfma_f32_16x16x128_f8f6f4 v[44:47], v[18:25], v[232:239], v[44:47]
	v_mfma_f32_16x16x128_f8f6f4 v[52:55], v[26:33], v[232:239], v[52:55]
	s_setprio 0
	s_setprio 1
	v_mfma_f32_16x16x128_f8f6f4 v[88:91], v[10:17], v[196:203], v[88:91]
	v_mfma_f32_16x16x128_f8f6f4 v[80:83], v[2:9], v[196:203], v[80:83]
	v_mfma_f32_16x16x128_f8f6f4 v[64:67], v[2:9], v[204:211], v[64:67]
	v_mfma_f32_16x16x128_f8f6f4 v[72:75], v[10:17], v[204:211], v[72:75]
	v_mfma_f32_16x16x128_f8f6f4 v[56:59], v[10:17], v[224:231], v[56:59]
	v_mfma_f32_16x16x128_f8f6f4 v[48:51], v[2:9], v[224:231], v[48:51]
	v_mfma_f32_16x16x128_f8f6f4 v[36:39], v[2:9], v[232:239], v[36:39]
	s_barrier
	s_setprio 3
	v_mfma_f32_16x16x128_f8f6f4 v[40:43], v[10:17], v[232:239], v[40:43]
	s_setprio 0
	s_add_i32 s14, 0, 0x18000
	s_add_i32 s65, 0, 0x1c000
	v_add_u32_e32 v14, s14, v222
	v_add_u32_e32 v30, s65, v222
	ds_read_b128 v[2:5], v14
	ds_read_b128 v[6:9], v14 offset:1024
	ds_read_b128 v[10:13], v14 offset:2048
	ds_read_b128 v[14:17], v14 offset:3072
	ds_read_b128 v[18:21], v30
	ds_read_b128 v[22:25], v30 offset:1024
	ds_read_b128 v[26:29], v30 offset:2048
	ds_read_b128 v[30:33], v30 offset:3072
	s_add_u32 s30, s40, 0x58000
	s_addc_u32 s31, s41, 0
	s_mov_b32 m0, s45
	v_lshl_add_u64 v[178:179], s[30:31], 0, v[168:169]
	ds_read_b128 v[196:199], v223 offset:32768
	ds_read_b128 v[200:203], v223 offset:33792
	ds_read_b128 v[204:207], v223 offset:34816
	ds_read_b128 v[208:211], v223 offset:35840
	ds_read_b128 v[224:227], v223 offset:36864
	ds_read_b128 v[228:231], v223 offset:37888
	ds_read_b128 v[232:235], v223 offset:38912
	ds_read_b128 v[236:239], v223 offset:39936
	global_load_lds_dwordx4 v[178:179], off
	v_lshl_add_u64 v[178:179], s[30:31], 0, v[166:167]
	s_mov_b32 m0, s46
	s_nop 0
	global_load_lds_dwordx4 v[178:179], off
	s_waitcnt vmcnt(8)
	s_waitcnt lgkmcnt(0)
	s_barrier
	s_setprio 1
	s_waitcnt lgkmcnt(0)
	v_mfma_f32_16x16x128_f8f6f4 v[160:163], v[2:9], v[196:203], v[160:163]
	v_mfma_f32_16x16x128_f8f6f4 v[156:159], v[10:17], v[196:203], v[156:159]
	v_mfma_f32_16x16x128_f8f6f4 v[140:143], v[10:17], v[204:211], v[140:143]
	v_mfma_f32_16x16x128_f8f6f4 v[144:147], v[2:9], v[204:211], v[144:147]
	v_mfma_f32_16x16x128_f8f6f4 v[132:135], v[2:9], v[224:231], v[132:135]
	v_mfma_f32_16x16x128_f8f6f4 v[124:127], v[10:17], v[224:231], v[124:127]
	v_mfma_f32_16x16x128_f8f6f4 v[108:111], v[10:17], v[232:239], v[108:111]
	v_mfma_f32_16x16x128_f8f6f4 v[116:119], v[2:9], v[232:239], v[116:119]
	s_setprio 0
	s_setprio 1
	v_mfma_f32_16x16x128_f8f6f4 v[152:155], v[18:25], v[196:203], v[152:155]
	v_mfma_f32_16x16x128_f8f6f4 v[148:151], v[26:33], v[196:203], v[148:151]
	v_mfma_f32_16x16x128_f8f6f4 v[128:131], v[26:33], v[204:211], v[128:131]
	v_mfma_f32_16x16x128_f8f6f4 v[136:139], v[18:25], v[204:211], v[136:139]
	v_mfma_f32_16x16x128_f8f6f4 v[120:123], v[18:25], v[224:231], v[120:123]
	v_mfma_f32_16x16x128_f8f6f4 v[112:115], v[26:33], v[224:231], v[112:115]
	v_mfma_f32_16x16x128_f8f6f4 v[100:103], v[26:33], v[232:239], v[100:103]
	s_barrier
	s_setprio 3
	v_mfma_f32_16x16x128_f8f6f4 v[104:107], v[18:25], v[232:239], v[104:107]
	s_setprio 0
	s_add_i32 s14, s14, s42
	v_lshl_add_u64 v[174:175], v[174:175], 0, s[18:19]
	s_mov_b32 m0, s14
	ds_read_b128 v[196:199], v223 offset:49152
	ds_read_b128 v[200:203], v223 offset:50176
	ds_read_b128 v[204:207], v223 offset:51200
	ds_read_b128 v[208:211], v223 offset:52224
	ds_read_b128 v[224:227], v223 offset:53248
	ds_read_b128 v[228:231], v223 offset:54272
	ds_read_b128 v[232:235], v223 offset:55296
	ds_read_b128 v[236:239], v223 offset:56320
	global_load_lds_dwordx4 v[174:175], off
	s_add_i32 m0, s14, 0x2000
	s_add_u32 s30, s36, 0x58080
	v_lshl_add_u64 v[174:175], v[190:191], 0, s[18:19]
	s_addc_u32 s31, s37, 0
	s_add_i32 s14, s65, s42
	global_load_lds_dwordx4 v[174:175], off
	v_lshl_add_u64 v[174:175], s[30:31], 0, v[34:35]
	s_mov_b32 m0, s14
	s_nop 0
	global_load_lds_dwordx4 v[174:175], off
	v_lshl_add_u64 v[174:175], s[30:31], 0, v[164:165]
	s_add_i32 m0, s14, 0x2000
	s_nop 0
	global_load_lds_dwordx4 v[174:175], off
	v_lshl_add_u64 v[174:175], v[192:193], 0, s[18:19]
	s_mov_b32 m0, s51
	s_nop 0
	global_load_lds_dwordx4 v[174:175], off
	v_lshl_add_u64 v[174:175], v[194:195], 0, s[18:19]
	s_mov_b32 m0, s52
	s_nop 0
	global_load_lds_dwordx4 v[174:175], off
	s_waitcnt vmcnt(8)
	s_waitcnt lgkmcnt(0)
	s_barrier
	s_setprio 1
	s_waitcnt lgkmcnt(0)
	v_mfma_f32_16x16x128_f8f6f4 v[96:99], v[2:9], v[196:203], v[96:99]
	v_mfma_f32_16x16x128_f8f6f4 v[92:95], v[10:17], v[196:203], v[92:95]
	v_mfma_f32_16x16x128_f8f6f4 v[76:79], v[10:17], v[204:211], v[76:79]
	v_mfma_f32_16x16x128_f8f6f4 v[84:87], v[2:9], v[204:211], v[84:87]
	v_mfma_f32_16x16x128_f8f6f4 v[68:71], v[2:9], v[224:231], v[68:71]
	v_mfma_f32_16x16x128_f8f6f4 v[60:63], v[10:17], v[224:231], v[60:63]
	v_mfma_f32_16x16x128_f8f6f4 v[44:47], v[10:17], v[232:239], v[44:47]
	v_mfma_f32_16x16x128_f8f6f4 v[52:55], v[2:9], v[232:239], v[52:55]
	s_setprio 0
	s_setprio 1
	v_mfma_f32_16x16x128_f8f6f4 v[88:91], v[18:25], v[196:203], v[88:91]
	v_mfma_f32_16x16x128_f8f6f4 v[80:83], v[26:33], v[196:203], v[80:83]
	v_mfma_f32_16x16x128_f8f6f4 v[64:67], v[26:33], v[204:211], v[64:67]
	v_mfma_f32_16x16x128_f8f6f4 v[72:75], v[18:25], v[204:211], v[72:75]
	v_mfma_f32_16x16x128_f8f6f4 v[56:59], v[18:25], v[224:231], v[56:59]
	v_mfma_f32_16x16x128_f8f6f4 v[48:51], v[26:33], v[224:231], v[48:51]
	v_mfma_f32_16x16x128_f8f6f4 v[36:39], v[26:33], v[232:239], v[36:39]
	s_barrier
	s_setprio 3
	v_mfma_f32_16x16x128_f8f6f4 v[40:43], v[18:25], v[232:239], v[40:43]
	s_setprio 0
	s_add_i32 s64, s64, 2
	s_add_u32 s62, s62, 0x100
	s_addc_u32 s63, s63, 0
	s_cmp_gt_u32 s64, 19
	s_mov_b64 s[30:31], s[22:23]
	s_cbranch_scc0 .LBB0_1160
	s_and_b64 vcc, exec, s[8:9]
	s_mov_b32 s58, 0x19b00000
	v_readlane_b32 s59, v255, 10
	s_mov_b32 s60, 0xff61b1e6
	s_mov_b64 s[62:63], 0x800
	s_cbranch_vccz .LBB0_1163
	s_barrier
